# precise f32 division chains -> v_rcp_f32 (+mul) in shift sigmoid (p2) and ret_out silu (p13), 126 sites
# baseline (speedup 1.0000x reference)
.LBB0_372:
	s_or_b64 exec, exec, s[40:41]
	v_lshlrev_b64 v[132:133], 2, v[130:131]
	v_lshl_add_u64 v[126:127], s[22:23], 0, v[132:133]
	global_load_dwordx4 v[168:171], v[126:127], off offset:16
	s_nop 0
	global_load_dwordx4 v[126:129], v[126:127], off
	v_lshl_add_u64 v[132:133], s[28:29], 0, v[132:133]
	global_load_dwordx4 v[172:175], v[132:133], off offset:16
	global_load_dwordx4 v[176:179], v[132:133], off
	s_waitcnt vmcnt(4)
	v_lshlrev_b32_e32 v132, 16, v114
	v_and_b32_e32 v133, 0xffff0000, v114
	v_lshlrev_b32_e32 v180, 16, v118
	v_and_b32_e32 v181, 0xffff0000, v118
	v_lshlrev_b32_e32 v114, 16, v115
	v_and_b32_e32 v115, 0xffff0000, v115
	v_lshlrev_b32_e32 v118, 16, v119
	v_and_b32_e32 v119, 0xffff0000, v119
	v_lshlrev_b32_e32 v182, 16, v122
	v_and_b32_e32 v183, 0xffff0000, v122
	v_lshlrev_b32_e32 v122, 16, v123
	v_and_b32_e32 v123, 0xffff0000, v123
	v_pk_add_f32 v[118:119], v[118:119], v[114:115] neg_lo:[0,1] neg_hi:[0,1]
	v_pk_add_f32 v[180:181], v[180:181], v[132:133] neg_lo:[0,1] neg_hi:[0,1]
	v_cmp_lt_u32_e32 vcc, s71, v130
	s_waitcnt vmcnt(2)
	v_pk_fma_f32 v[118:119], v[118:119], v[128:129], v[114:115]
	v_pk_add_f32 v[114:115], v[122:123], v[114:115] neg_lo:[0,1] neg_hi:[0,1]
	v_lshlrev_b32_e32 v122, 16, v120
	s_waitcnt vmcnt(0)
	v_pk_fma_f32 v[114:115], v[114:115], v[178:179], v[118:119]
	v_lshlrev_b32_e32 v118, 16, v116
	v_and_b32_e32 v119, 0xffff0000, v116
	v_and_b32_e32 v123, 0xffff0000, v120
	v_lshlrev_b32_e32 v128, 16, v124
	v_and_b32_e32 v129, 0xffff0000, v124
	v_pk_add_f32 v[122:123], v[122:123], v[118:119] neg_lo:[0,1] neg_hi:[0,1]
	v_lshlrev_b32_e32 v116, 16, v117
	v_pk_fma_f32 v[122:123], v[122:123], v[168:169], v[118:119]
	v_pk_add_f32 v[118:119], v[128:129], v[118:119] neg_lo:[0,1] neg_hi:[0,1]
	v_and_b32_e32 v117, 0xffff0000, v117
	v_lshlrev_b32_e32 v120, 16, v121
	v_and_b32_e32 v121, 0xffff0000, v121
	v_pk_fma_f32 v[118:119], v[118:119], v[172:173], v[122:123]
	v_lshlrev_b32_e32 v122, 16, v125
	v_and_b32_e32 v123, 0xffff0000, v125
	v_pk_add_f32 v[120:121], v[120:121], v[116:117] neg_lo:[0,1] neg_hi:[0,1]
	v_pk_fma_f32 v[126:127], v[180:181], v[126:127], v[132:133]
	v_pk_add_f32 v[132:133], v[182:183], v[132:133] neg_lo:[0,1] neg_hi:[0,1]
	v_pk_fma_f32 v[120:121], v[120:121], v[170:171], v[116:117]
	v_pk_add_f32 v[116:117], v[122:123], v[116:117] neg_lo:[0,1] neg_hi:[0,1]
	v_pk_fma_f32 v[126:127], v[132:133], v[176:177], v[126:127]
	v_pk_fma_f32 v[116:117], v[116:117], v[174:175], v[120:121]
	s_and_saveexec_b64 s[40:41], vcc
	s_xor_b64 s[40:41], exec, s[40:41]
	s_cbranch_execz .LBB0_420
	v_cmp_lt_u32_e32 vcc, s72, v130
	s_and_saveexec_b64 s[42:43], vcc
	s_xor_b64 s[42:43], exec, s[42:43]
	s_cbranch_execz .LBB0_417
	v_cmp_lt_u32_e32 vcc, s73, v130
	s_and_saveexec_b64 s[44:45], vcc
	s_xor_b64 s[44:45], exec, s[44:45]
	s_cbranch_execz .LBB0_414
	v_cmp_lt_u32_e32 vcc, s76, v130
	s_and_saveexec_b64 s[46:47], vcc
	s_xor_b64 s[46:47], exec, s[46:47]
	s_cbranch_execz .LBB0_379
	v_cmp_lt_u32_e32 vcc, s77, v130
	s_and_saveexec_b64 s[48:49], vcc
	s_cbranch_execz .LBB0_378
	v_mul_f32_e32 v120, 0xbfb8aa3b, v126
	v_rndne_f32_e32 v121, v120
	v_sub_f32_e32 v122, v120, v121
	v_fma_f32 v120, v126, s78, -v120
	v_fmac_f32_e32 v120, 0xb2a5705f, v126
	v_add_f32_e32 v120, v122, v120
	v_exp_f32_e32 v120, v120
	v_cvt_i32_f32_e32 v121, v121
	v_cmp_nlt_f32_e32 vcc, s79, v126
	v_ldexp_f32 v120, v120, v121
	v_mul_f32_e32 v121, 0xbfb8aa3b, v127
	v_rndne_f32_e32 v122, v121
	v_sub_f32_e32 v123, v121, v122
	v_fma_f32 v121, v127, s78, -v121
	v_fmac_f32_e32 v121, 0xb2a5705f, v127
	v_add_f32_e32 v121, v123, v121
	v_exp_f32_e32 v121, v121
	v_cvt_i32_f32_e32 v122, v122
	v_cndmask_b32_e32 v120, 0, v120, vcc
	v_cmp_ngt_f32_e32 vcc, s80, v126
	v_ldexp_f32 v121, v121, v122
	v_mul_f32_e32 v122, 0xbfb8aa3b, v114
	v_rndne_f32_e32 v123, v122
	v_sub_f32_e32 v124, v122, v123
	v_fma_f32 v122, v114, s78, -v122
	v_fmac_f32_e32 v122, 0xb2a5705f, v114
	v_add_f32_e32 v122, v124, v122
	v_exp_f32_e32 v122, v122
	v_cvt_i32_f32_e32 v123, v123
	v_cndmask_b32_e32 v120, v143, v120, vcc
	v_cmp_nlt_f32_e32 vcc, s79, v127
	v_ldexp_f32 v122, v122, v123
	s_nop 0
	v_cndmask_b32_e32 v121, 0, v121, vcc
	v_cmp_ngt_f32_e32 vcc, s80, v127
	s_nop 1
	v_cndmask_b32_e32 v121, v143, v121, vcc
	v_cmp_nlt_f32_e32 vcc, s79, v114
	v_pk_add_f32 v[120:121], v[120:121], 1.0 op_sel_hi:[1,0]
	s_nop 0
	v_cndmask_b32_e32 v122, 0, v122, vcc
	v_cmp_ngt_f32_e32 vcc, s80, v114
	s_nop 1
	v_cndmask_b32_e32 v114, v143, v122, vcc
	v_mul_f32_e32 v122, 0xbfb8aa3b, v115
	v_rndne_f32_e32 v123, v122
	v_sub_f32_e32 v124, v122, v123
	v_fma_f32 v122, v115, s78, -v122
	v_fmac_f32_e32 v122, 0xb2a5705f, v115
	v_add_f32_e32 v122, v124, v122
	v_exp_f32_e32 v122, v122
	v_cvt_i32_f32_e32 v123, v123
	v_cmp_nlt_f32_e32 vcc, s79, v115
	v_ldexp_f32 v122, v122, v123
	s_nop 0
	v_cndmask_b32_e32 v122, 0, v122, vcc
	v_cmp_ngt_f32_e32 vcc, s80, v115
	s_nop 1
	v_cndmask_b32_e32 v115, v143, v122, vcc
	v_mul_f32_e32 v122, 0xbfb8aa3b, v118
	v_rndne_f32_e32 v123, v122
	v_sub_f32_e32 v124, v122, v123
	v_fma_f32 v122, v118, s78, -v122
	v_fmac_f32_e32 v122, 0xb2a5705f, v118
	v_add_f32_e32 v122, v124, v122
	v_exp_f32_e32 v122, v122
	v_cvt_i32_f32_e32 v123, v123
	v_cmp_nlt_f32_e32 vcc, s79, v118
	v_pk_add_f32 v[114:115], v[114:115], 1.0 op_sel_hi:[1,0]
	v_ldexp_f32 v122, v122, v123
	v_cndmask_b32_e32 v122, 0, v122, vcc
	v_cmp_ngt_f32_e32 vcc, s80, v118
	s_nop 1
	v_cndmask_b32_e32 v118, v143, v122, vcc
	v_mul_f32_e32 v122, 0xbfb8aa3b, v119
	v_rndne_f32_e32 v123, v122
	v_sub_f32_e32 v124, v122, v123
	v_fma_f32 v122, v119, s78, -v122
	v_fmac_f32_e32 v122, 0xb2a5705f, v119
	v_add_f32_e32 v122, v124, v122
	v_exp_f32_e32 v122, v122
	v_cvt_i32_f32_e32 v123, v123
	v_cmp_nlt_f32_e32 vcc, s79, v119
	v_ldexp_f32 v122, v122, v123
	s_nop 0
	v_cndmask_b32_e32 v122, 0, v122, vcc
	v_cmp_ngt_f32_e32 vcc, s80, v119
	s_nop 1
	v_cndmask_b32_e32 v119, v143, v122, vcc
	v_mul_f32_e32 v122, 0xbfb8aa3b, v116
	v_rndne_f32_e32 v123, v122
	v_sub_f32_e32 v124, v122, v123
	v_fma_f32 v122, v116, s78, -v122
	v_fmac_f32_e32 v122, 0xb2a5705f, v116
	v_add_f32_e32 v122, v124, v122
	v_exp_f32_e32 v122, v122
	v_cvt_i32_f32_e32 v123, v123
	v_cmp_nlt_f32_e32 vcc, s79, v116
	v_pk_add_f32 v[118:119], v[118:119], 1.0 op_sel_hi:[1,0]
	v_ldexp_f32 v122, v122, v123
	v_cndmask_b32_e32 v122, 0, v122, vcc
	v_cmp_ngt_f32_e32 vcc, s80, v116
	s_nop 1
	v_cndmask_b32_e32 v116, v143, v122, vcc
	v_mul_f32_e32 v122, 0xbfb8aa3b, v117
	v_rndne_f32_e32 v123, v122
	v_sub_f32_e32 v124, v122, v123
	v_fma_f32 v122, v117, s78, -v122
	v_fmac_f32_e32 v122, 0xb2a5705f, v117
	v_add_f32_e32 v122, v124, v122
	v_exp_f32_e32 v122, v122
	v_cvt_i32_f32_e32 v123, v123
	v_cmp_nlt_f32_e32 vcc, s79, v117
	v_ldexp_f32 v122, v122, v123
	s_nop 0
	v_cndmask_b32_e32 v122, 0, v122, vcc
	v_cmp_ngt_f32_e32 vcc, s80, v117
	s_nop 1
	v_cndmask_b32_e32 v117, v143, v122, vcc
	v_div_scale_f32 v122, s[74:75], v120, v120, 1.0
	v_rcp_f32_e32 v123, v122
	v_pk_add_f32 v[116:117], v[116:117], 1.0 op_sel_hi:[1,0]
	v_fma_f32 v124, -v122, v123, 1.0
	v_fmac_f32_e32 v123, v124, v123
	v_div_scale_f32 v124, vcc, 1.0, v120, 1.0
	v_mul_f32_e32 v125, v124, v123
	v_fma_f32 v126, -v122, v125, v124
	v_fmac_f32_e32 v125, v126, v123
	v_fma_f32 v122, -v122, v125, v124
	v_div_fmas_f32 v122, v122, v123, v125
	v_div_fixup_f32 v126, v122, v120, 1.0
	v_rcp_f32_e32 v127, v121
	s_nop 3
	v_rcp_f32_e32 v114, v114
	s_nop 3
	v_rcp_f32_e32 v115, v115
	s_nop 3
	v_rcp_f32_e32 v118, v118
	s_nop 3
	v_rcp_f32_e32 v119, v119
	s_nop 3
	v_rcp_f32_e32 v116, v116
	s_nop 3
	v_div_scale_f32 v120, s[74:75], v117, v117, 1.0
	v_rcp_f32_e32 v121, v120
	s_nop 0
	v_fma_f32 v122, -v120, v121, 1.0
	v_fmac_f32_e32 v121, v122, v121
	v_div_scale_f32 v122, vcc, 1.0, v117, 1.0
	v_mul_f32_e32 v123, v122, v121
	v_fma_f32 v124, -v120, v123, v122
	v_fmac_f32_e32 v123, v124, v121
	v_fma_f32 v120, -v120, v123, v122
	v_div_fmas_f32 v120, v120, v121, v123
	v_div_fixup_f32 v117, v120, v117, 1.0

.LBB0_429:
	v_add_u32_e32 v130, v120, v165
	v_lshlrev_b64 v[114:115], 2, v[130:131]
	v_lshl_add_u64 v[122:123], s[22:23], 0, v[114:115]
	global_load_dwordx4 v[116:119], v[122:123], off offset:16
	s_nop 0
	global_load_dwordx4 v[122:125], v[122:123], off
	v_lshl_add_u64 v[114:115], s[28:29], 0, v[114:115]
	v_lshrrev_b32_e32 v121, 2, v166
	global_load_dwordx4 v[126:129], v[114:115], off offset:16
	global_load_dwordx4 v[164:167], v[114:115], off
	v_lshlrev_b32_e32 v114, 16, v10
	v_and_b32_e32 v115, 0xffff0000, v10
	v_lshlrev_b32_e32 v132, 16, v110
	v_and_b32_e32 v133, 0xffff0000, v110
	v_lshlrev_b32_e32 v168, 16, v38
	v_and_b32_e32 v169, 0xffff0000, v38
	v_pk_add_f32 v[132:133], v[132:133], v[114:115] neg_lo:[0,1] neg_hi:[0,1]
	v_lshlrev_b32_e32 v110, 16, v111
	v_and_b32_e32 v111, 0xffff0000, v111
	v_cmp_lt_u32_e32 vcc, s71, v130
	s_waitcnt vmcnt(2)
	v_pk_fma_f32 v[122:123], v[132:133], v[122:123], v[114:115]
	v_pk_add_f32 v[114:115], v[168:169], v[114:115] neg_lo:[0,1] neg_hi:[0,1]
	v_lshlrev_b32_e32 v132, 16, v39
	s_waitcnt vmcnt(0)
	v_pk_fma_f32 v[114:115], v[114:115], v[164:165], v[122:123]
	v_lshlrev_b32_e32 v122, 16, v11
	v_and_b32_e32 v123, 0xffff0000, v11
	v_and_b32_e32 v133, 0xffff0000, v39
	v_pk_add_f32 v[110:111], v[110:111], v[122:123] neg_lo:[0,1] neg_hi:[0,1]
	s_nop 0
	v_pk_fma_f32 v[110:111], v[110:111], v[124:125], v[122:123]
	v_pk_add_f32 v[122:123], v[132:133], v[122:123] neg_lo:[0,1] neg_hi:[0,1]
	v_lshlrev_b32_e32 v124, 16, v112
	v_pk_fma_f32 v[110:111], v[122:123], v[166:167], v[110:111]
	v_lshlrev_b32_e32 v122, 16, v12
	v_and_b32_e32 v123, 0xffff0000, v12
	v_and_b32_e32 v125, 0xffff0000, v112
	v_lshlrev_b32_e32 v132, 16, v40
	v_and_b32_e32 v133, 0xffff0000, v40
	v_pk_add_f32 v[124:125], v[124:125], v[122:123] neg_lo:[0,1] neg_hi:[0,1]
	v_lshlrev_b32_e32 v112, 16, v113
	v_pk_fma_f32 v[116:117], v[124:125], v[116:117], v[122:123]
	v_pk_add_f32 v[122:123], v[132:133], v[122:123] neg_lo:[0,1] neg_hi:[0,1]
	v_and_b32_e32 v113, 0xffff0000, v113
	v_pk_fma_f32 v[116:117], v[122:123], v[126:127], v[116:117]
	v_lshlrev_b32_e32 v122, 16, v13
	v_and_b32_e32 v123, 0xffff0000, v13
	v_lshlrev_b32_e32 v124, 16, v41
	v_and_b32_e32 v125, 0xffff0000, v41
	v_pk_add_f32 v[112:113], v[112:113], v[122:123] neg_lo:[0,1] neg_hi:[0,1]
	s_nop 0
	v_pk_fma_f32 v[112:113], v[112:113], v[118:119], v[122:123]
	v_pk_add_f32 v[118:119], v[124:125], v[122:123] neg_lo:[0,1] neg_hi:[0,1]
	s_nop 0
	v_pk_fma_f32 v[112:113], v[118:119], v[128:129], v[112:113]
	s_and_saveexec_b64 s[18:19], vcc
	s_xor_b64 s[18:19], exec, s[18:19]
	s_cbranch_execz .LBB0_477
	v_cmp_lt_u32_e32 vcc, s72, v130
	s_and_saveexec_b64 s[42:43], vcc
	s_xor_b64 s[42:43], exec, s[42:43]
	s_cbranch_execz .LBB0_474
	v_cmp_lt_u32_e32 vcc, s73, v130
	s_and_saveexec_b64 s[44:45], vcc
	s_xor_b64 s[44:45], exec, s[44:45]
	s_cbranch_execz .LBB0_471
	v_cmp_lt_u32_e32 vcc, s76, v130
	s_and_saveexec_b64 s[46:47], vcc
	s_xor_b64 s[46:47], exec, s[46:47]
	s_cbranch_execz .LBB0_436
	v_cmp_lt_u32_e32 vcc, s77, v130
	s_and_saveexec_b64 s[48:49], vcc
	s_cbranch_execz .LBB0_435
	v_mul_f32_e32 v118, 0xbfb8aa3b, v114
	v_rndne_f32_e32 v119, v118
	v_sub_f32_e32 v122, v118, v119
	v_fma_f32 v118, v114, s78, -v118
	v_fmac_f32_e32 v118, 0xb2a5705f, v114
	v_add_f32_e32 v118, v122, v118
	v_exp_f32_e32 v118, v118
	v_cvt_i32_f32_e32 v119, v119
	v_cmp_nlt_f32_e32 vcc, s79, v114
	v_ldexp_f32 v118, v118, v119
	s_nop 0
	v_cndmask_b32_e32 v118, 0, v118, vcc
	v_cmp_ngt_f32_e32 vcc, s80, v114
	s_nop 1
	v_cndmask_b32_e32 v114, v143, v118, vcc
	v_mul_f32_e32 v118, 0xbfb8aa3b, v115
	v_rndne_f32_e32 v119, v118
	v_sub_f32_e32 v122, v118, v119
	v_fma_f32 v118, v115, s78, -v118
	v_fmac_f32_e32 v118, 0xb2a5705f, v115
	v_add_f32_e32 v118, v122, v118
	v_exp_f32_e32 v118, v118
	v_cvt_i32_f32_e32 v119, v119
	v_cmp_nlt_f32_e32 vcc, s79, v115
	v_ldexp_f32 v118, v118, v119
	s_nop 0
	v_cndmask_b32_e32 v118, 0, v118, vcc
	v_cmp_ngt_f32_e32 vcc, s80, v115
	s_nop 1
	v_cndmask_b32_e32 v115, v143, v118, vcc
	v_mul_f32_e32 v118, 0xbfb8aa3b, v110
	v_rndne_f32_e32 v119, v118
	v_sub_f32_e32 v122, v118, v119
	v_fma_f32 v118, v110, s78, -v118
	v_fmac_f32_e32 v118, 0xb2a5705f, v110
	v_add_f32_e32 v118, v122, v118
	v_exp_f32_e32 v118, v118
	v_cvt_i32_f32_e32 v119, v119
	v_cmp_nlt_f32_e32 vcc, s79, v110
	v_pk_add_f32 v[114:115], v[114:115], 1.0 op_sel_hi:[1,0]
	v_ldexp_f32 v118, v118, v119
	v_cndmask_b32_e32 v118, 0, v118, vcc
	v_cmp_ngt_f32_e32 vcc, s80, v110
	s_nop 1
	v_cndmask_b32_e32 v110, v143, v118, vcc
	v_mul_f32_e32 v118, 0xbfb8aa3b, v111
	v_rndne_f32_e32 v119, v118
	v_sub_f32_e32 v122, v118, v119
	v_fma_f32 v118, v111, s78, -v118
	v_fmac_f32_e32 v118, 0xb2a5705f, v111
	v_add_f32_e32 v118, v122, v118
	v_exp_f32_e32 v118, v118
	v_cvt_i32_f32_e32 v119, v119
	v_cmp_nlt_f32_e32 vcc, s79, v111
	v_ldexp_f32 v118, v118, v119
	s_nop 0
	v_cndmask_b32_e32 v118, 0, v118, vcc
	v_cmp_ngt_f32_e32 vcc, s80, v111
	s_nop 1
	v_cndmask_b32_e32 v111, v143, v118, vcc
	v_mul_f32_e32 v118, 0xbfb8aa3b, v116
	v_rndne_f32_e32 v119, v118
	v_sub_f32_e32 v122, v118, v119
	v_fma_f32 v118, v116, s78, -v118
	v_fmac_f32_e32 v118, 0xb2a5705f, v116
	v_add_f32_e32 v118, v122, v118
	v_exp_f32_e32 v118, v118
	v_cvt_i32_f32_e32 v119, v119
	v_cmp_nlt_f32_e32 vcc, s79, v116
	v_pk_add_f32 v[110:111], v[110:111], 1.0 op_sel_hi:[1,0]
	v_ldexp_f32 v118, v118, v119
	v_cndmask_b32_e32 v118, 0, v118, vcc
	v_cmp_ngt_f32_e32 vcc, s80, v116
	s_nop 1
	v_cndmask_b32_e32 v116, v143, v118, vcc
	v_mul_f32_e32 v118, 0xbfb8aa3b, v117
	v_rndne_f32_e32 v119, v118
	v_sub_f32_e32 v122, v118, v119
	v_fma_f32 v118, v117, s78, -v118
	v_fmac_f32_e32 v118, 0xb2a5705f, v117
	v_add_f32_e32 v118, v122, v118
	v_exp_f32_e32 v118, v118
	v_cvt_i32_f32_e32 v119, v119
	v_cmp_nlt_f32_e32 vcc, s79, v117
	v_ldexp_f32 v118, v118, v119
	s_nop 0
	v_cndmask_b32_e32 v118, 0, v118, vcc
	v_cmp_ngt_f32_e32 vcc, s80, v117
	s_nop 1
	v_cndmask_b32_e32 v117, v143, v118, vcc
	v_mul_f32_e32 v118, 0xbfb8aa3b, v112
	v_rndne_f32_e32 v119, v118
	v_sub_f32_e32 v122, v118, v119
	v_fma_f32 v118, v112, s78, -v118
	v_fmac_f32_e32 v118, 0xb2a5705f, v112
	v_add_f32_e32 v118, v122, v118
	v_exp_f32_e32 v118, v118
	v_cvt_i32_f32_e32 v119, v119
	v_cmp_nlt_f32_e32 vcc, s79, v112
	v_pk_add_f32 v[116:117], v[116:117], 1.0 op_sel_hi:[1,0]
	v_ldexp_f32 v118, v118, v119
	v_cndmask_b32_e32 v118, 0, v118, vcc
	v_cmp_ngt_f32_e32 vcc, s80, v112
	s_nop 1
	v_cndmask_b32_e32 v112, v143, v118, vcc
	v_mul_f32_e32 v118, 0xbfb8aa3b, v113
	v_rndne_f32_e32 v119, v118
	v_sub_f32_e32 v122, v118, v119
	v_fma_f32 v118, v113, s78, -v118
	v_fmac_f32_e32 v118, 0xb2a5705f, v113
	v_add_f32_e32 v118, v122, v118
	v_exp_f32_e32 v118, v118
	v_cvt_i32_f32_e32 v119, v119
	v_cmp_nlt_f32_e32 vcc, s79, v113
	v_ldexp_f32 v118, v118, v119
	s_nop 0
	v_cndmask_b32_e32 v118, 0, v118, vcc
	v_cmp_ngt_f32_e32 vcc, s80, v113
	s_nop 1
	v_cndmask_b32_e32 v113, v143, v118, vcc
	v_div_scale_f32 v118, s[74:75], v114, v114, 1.0
	v_rcp_f32_e32 v119, v118
	v_pk_add_f32 v[112:113], v[112:113], 1.0 op_sel_hi:[1,0]
	v_fma_f32 v122, -v118, v119, 1.0
	v_fmac_f32_e32 v119, v122, v119
	v_div_scale_f32 v122, vcc, 1.0, v114, 1.0
	v_mul_f32_e32 v123, v122, v119
	v_fma_f32 v124, -v118, v123, v122
	v_fmac_f32_e32 v123, v124, v119
	v_fma_f32 v118, -v118, v123, v122
	v_div_fmas_f32 v118, v118, v119, v123
	v_div_fixup_f32 v114, v118, v114, 1.0
	v_rcp_f32_e32 v115, v115
	s_nop 3
	v_rcp_f32_e32 v110, v110
	s_nop 3
	v_rcp_f32_e32 v111, v111
	s_nop 3
	v_rcp_f32_e32 v116, v116
	s_nop 3
	v_rcp_f32_e32 v117, v117
	s_nop 3
	v_rcp_f32_e32 v112, v112
	s_nop 3
	v_div_scale_f32 v118, s[74:75], v113, v113, 1.0
	v_rcp_f32_e32 v119, v118
	s_nop 0
	v_fma_f32 v122, -v118, v119, 1.0
	v_fmac_f32_e32 v119, v122, v119
	v_div_scale_f32 v122, vcc, 1.0, v113, 1.0
	v_mul_f32_e32 v123, v122, v119
	v_fma_f32 v124, -v118, v123, v122
	v_fmac_f32_e32 v123, v124, v119
	v_fma_f32 v118, -v118, v123, v122
	v_div_fmas_f32 v118, v118, v119, v123
	v_div_fixup_f32 v113, v118, v113, 1.0

.LBB0_480:
	v_add_u32_e32 v130, v120, v162
	v_lshlrev_b64 v[110:111], 2, v[130:131]
	v_lshl_add_u64 v[118:119], s[22:23], 0, v[110:111]
	global_load_dwordx4 v[112:115], v[118:119], off offset:16
	global_load_dwordx4 v[122:125], v[118:119], off
	v_lshl_add_u64 v[110:111], s[28:29], 0, v[110:111]
	v_lshrrev_b32_e32 v116, 2, v163
	global_load_dwordx4 v[126:129], v[110:111], off offset:16
	global_load_dwordx4 v[162:165], v[110:111], off
	v_lshlrev_b32_e32 v110, 16, v6
	v_and_b32_e32 v111, 0xffff0000, v6
	v_lshlrev_b32_e32 v118, 16, v106
	v_and_b32_e32 v119, 0xffff0000, v106
	v_lshlrev_b32_e32 v132, 16, v34
	v_and_b32_e32 v133, 0xffff0000, v34
	v_pk_add_f32 v[118:119], v[118:119], v[110:111] neg_lo:[0,1] neg_hi:[0,1]
	v_lshlrev_b32_e32 v106, 16, v107
	v_and_b32_e32 v107, 0xffff0000, v107
	v_cmp_lt_u32_e32 vcc, s71, v130
	s_waitcnt vmcnt(2)
	v_pk_fma_f32 v[118:119], v[118:119], v[122:123], v[110:111]
	v_pk_add_f32 v[110:111], v[132:133], v[110:111] neg_lo:[0,1] neg_hi:[0,1]
	v_lshlrev_b32_e32 v122, 16, v35
	s_waitcnt vmcnt(0)
	v_pk_fma_f32 v[110:111], v[110:111], v[162:163], v[118:119]
	v_lshlrev_b32_e32 v118, 16, v7
	v_and_b32_e32 v119, 0xffff0000, v7
	v_and_b32_e32 v123, 0xffff0000, v35
	v_pk_add_f32 v[106:107], v[106:107], v[118:119] neg_lo:[0,1] neg_hi:[0,1]
	s_nop 0
	v_pk_fma_f32 v[106:107], v[106:107], v[124:125], v[118:119]
	v_pk_add_f32 v[118:119], v[122:123], v[118:119] neg_lo:[0,1] neg_hi:[0,1]
	v_lshlrev_b32_e32 v122, 16, v108
	v_pk_fma_f32 v[106:107], v[118:119], v[164:165], v[106:107]
	v_lshlrev_b32_e32 v118, 16, v8
	v_and_b32_e32 v119, 0xffff0000, v8
	v_and_b32_e32 v123, 0xffff0000, v108
	v_lshlrev_b32_e32 v124, 16, v36
	v_and_b32_e32 v125, 0xffff0000, v36
	v_pk_add_f32 v[122:123], v[122:123], v[118:119] neg_lo:[0,1] neg_hi:[0,1]
	v_lshlrev_b32_e32 v108, 16, v109
	v_pk_fma_f32 v[112:113], v[122:123], v[112:113], v[118:119]
	v_pk_add_f32 v[118:119], v[124:125], v[118:119] neg_lo:[0,1] neg_hi:[0,1]
	v_and_b32_e32 v109, 0xffff0000, v109
	v_pk_fma_f32 v[112:113], v[118:119], v[126:127], v[112:113]
	v_lshlrev_b32_e32 v118, 16, v9
	v_and_b32_e32 v119, 0xffff0000, v9
	v_lshlrev_b32_e32 v122, 16, v37
	v_and_b32_e32 v123, 0xffff0000, v37
	v_pk_add_f32 v[108:109], v[108:109], v[118:119] neg_lo:[0,1] neg_hi:[0,1]
	s_nop 0
	v_pk_fma_f32 v[108:109], v[108:109], v[114:115], v[118:119]
	v_pk_add_f32 v[114:115], v[122:123], v[118:119] neg_lo:[0,1] neg_hi:[0,1]
	s_nop 0
	v_pk_fma_f32 v[108:109], v[114:115], v[128:129], v[108:109]
	s_and_saveexec_b64 s[16:17], vcc
	s_xor_b64 s[16:17], exec, s[16:17]
	s_cbranch_execz .LBB0_528
	v_cmp_lt_u32_e32 vcc, s72, v130
	s_and_saveexec_b64 s[40:41], vcc
	s_xor_b64 s[40:41], exec, s[40:41]
	s_cbranch_execz .LBB0_525
	v_cmp_lt_u32_e32 vcc, s73, v130
	s_and_saveexec_b64 s[42:43], vcc
	s_xor_b64 s[42:43], exec, s[42:43]
	s_cbranch_execz .LBB0_522
	v_cmp_lt_u32_e32 vcc, s76, v130
	s_and_saveexec_b64 s[44:45], vcc
	s_xor_b64 s[44:45], exec, s[44:45]
	s_cbranch_execz .LBB0_487
	v_cmp_lt_u32_e32 vcc, s77, v130
	s_and_saveexec_b64 s[46:47], vcc
	s_cbranch_execz .LBB0_486
	v_mul_f32_e32 v114, 0xbfb8aa3b, v110
	v_rndne_f32_e32 v115, v114
	v_sub_f32_e32 v117, v114, v115
	v_fma_f32 v114, v110, s78, -v114
	v_fmac_f32_e32 v114, 0xb2a5705f, v110
	v_add_f32_e32 v114, v117, v114
	v_exp_f32_e32 v114, v114
	v_cvt_i32_f32_e32 v115, v115
	v_cmp_nlt_f32_e32 vcc, s79, v110
	v_ldexp_f32 v114, v114, v115
	s_nop 0
	v_cndmask_b32_e32 v114, 0, v114, vcc
	v_cmp_ngt_f32_e32 vcc, s80, v110
	s_nop 1
	v_cndmask_b32_e32 v110, v143, v114, vcc
	v_mul_f32_e32 v114, 0xbfb8aa3b, v111
	v_rndne_f32_e32 v115, v114
	v_sub_f32_e32 v117, v114, v115
	v_fma_f32 v114, v111, s78, -v114
	v_fmac_f32_e32 v114, 0xb2a5705f, v111
	v_add_f32_e32 v114, v117, v114
	v_exp_f32_e32 v114, v114
	v_cvt_i32_f32_e32 v115, v115
	v_cmp_nlt_f32_e32 vcc, s79, v111
	v_ldexp_f32 v114, v114, v115
	s_nop 0
	v_cndmask_b32_e32 v114, 0, v114, vcc
	v_cmp_ngt_f32_e32 vcc, s80, v111
	s_nop 1
	v_cndmask_b32_e32 v111, v143, v114, vcc
	v_mul_f32_e32 v114, 0xbfb8aa3b, v106
	v_rndne_f32_e32 v115, v114
	v_sub_f32_e32 v117, v114, v115
	v_fma_f32 v114, v106, s78, -v114
	v_fmac_f32_e32 v114, 0xb2a5705f, v106
	v_add_f32_e32 v114, v117, v114
	v_exp_f32_e32 v114, v114
	v_cvt_i32_f32_e32 v115, v115
	v_cmp_nlt_f32_e32 vcc, s79, v106
	v_pk_add_f32 v[110:111], v[110:111], 1.0 op_sel_hi:[1,0]
	v_ldexp_f32 v114, v114, v115
	v_cndmask_b32_e32 v114, 0, v114, vcc
	v_cmp_ngt_f32_e32 vcc, s80, v106
	s_nop 1
	v_cndmask_b32_e32 v106, v143, v114, vcc
	v_mul_f32_e32 v114, 0xbfb8aa3b, v107
	v_rndne_f32_e32 v115, v114
	v_sub_f32_e32 v117, v114, v115
	v_fma_f32 v114, v107, s78, -v114
	v_fmac_f32_e32 v114, 0xb2a5705f, v107
	v_add_f32_e32 v114, v117, v114
	v_exp_f32_e32 v114, v114
	v_cvt_i32_f32_e32 v115, v115
	v_cmp_nlt_f32_e32 vcc, s79, v107
	v_ldexp_f32 v114, v114, v115
	s_nop 0
	v_cndmask_b32_e32 v114, 0, v114, vcc
	v_cmp_ngt_f32_e32 vcc, s80, v107
	s_nop 1
	v_cndmask_b32_e32 v107, v143, v114, vcc
	v_mul_f32_e32 v114, 0xbfb8aa3b, v112
	v_rndne_f32_e32 v115, v114
	v_sub_f32_e32 v117, v114, v115
	v_fma_f32 v114, v112, s78, -v114
	v_fmac_f32_e32 v114, 0xb2a5705f, v112
	v_add_f32_e32 v114, v117, v114
	v_exp_f32_e32 v114, v114
	v_cvt_i32_f32_e32 v115, v115
	v_cmp_nlt_f32_e32 vcc, s79, v112
	v_pk_add_f32 v[106:107], v[106:107], 1.0 op_sel_hi:[1,0]
	v_ldexp_f32 v114, v114, v115
	v_cndmask_b32_e32 v114, 0, v114, vcc
	v_cmp_ngt_f32_e32 vcc, s80, v112
	s_nop 1
	v_cndmask_b32_e32 v112, v143, v114, vcc
	v_mul_f32_e32 v114, 0xbfb8aa3b, v113
	v_rndne_f32_e32 v115, v114
	v_sub_f32_e32 v117, v114, v115
	v_fma_f32 v114, v113, s78, -v114
	v_fmac_f32_e32 v114, 0xb2a5705f, v113
	v_add_f32_e32 v114, v117, v114
	v_exp_f32_e32 v114, v114
	v_cvt_i32_f32_e32 v115, v115
	v_cmp_nlt_f32_e32 vcc, s79, v113
	v_ldexp_f32 v114, v114, v115
	s_nop 0
	v_cndmask_b32_e32 v114, 0, v114, vcc
	v_cmp_ngt_f32_e32 vcc, s80, v113
	s_nop 1
	v_cndmask_b32_e32 v113, v143, v114, vcc
	v_mul_f32_e32 v114, 0xbfb8aa3b, v108
	v_rndne_f32_e32 v115, v114
	v_sub_f32_e32 v117, v114, v115
	v_fma_f32 v114, v108, s78, -v114
	v_fmac_f32_e32 v114, 0xb2a5705f, v108
	v_add_f32_e32 v114, v117, v114
	v_exp_f32_e32 v114, v114
	v_cvt_i32_f32_e32 v115, v115
	v_cmp_nlt_f32_e32 vcc, s79, v108
	v_pk_add_f32 v[112:113], v[112:113], 1.0 op_sel_hi:[1,0]
	v_ldexp_f32 v114, v114, v115
	v_cndmask_b32_e32 v114, 0, v114, vcc
	v_cmp_ngt_f32_e32 vcc, s80, v108
	s_nop 1
	v_cndmask_b32_e32 v108, v143, v114, vcc
	v_mul_f32_e32 v114, 0xbfb8aa3b, v109
	v_rndne_f32_e32 v115, v114
	v_sub_f32_e32 v117, v114, v115
	v_fma_f32 v114, v109, s78, -v114
	v_fmac_f32_e32 v114, 0xb2a5705f, v109
	v_add_f32_e32 v114, v117, v114
	v_exp_f32_e32 v114, v114
	v_cvt_i32_f32_e32 v115, v115
	v_cmp_nlt_f32_e32 vcc, s79, v109
	v_ldexp_f32 v114, v114, v115
	s_nop 0
	v_cndmask_b32_e32 v114, 0, v114, vcc
	v_cmp_ngt_f32_e32 vcc, s80, v109
	s_nop 1
	v_cndmask_b32_e32 v109, v143, v114, vcc
	v_div_scale_f32 v114, s[48:49], v110, v110, 1.0
	v_rcp_f32_e32 v115, v114
	v_pk_add_f32 v[108:109], v[108:109], 1.0 op_sel_hi:[1,0]
	v_fma_f32 v117, -v114, v115, 1.0
	v_fmac_f32_e32 v115, v117, v115
	v_div_scale_f32 v117, vcc, 1.0, v110, 1.0
	v_mul_f32_e32 v118, v117, v115
	v_fma_f32 v119, -v114, v118, v117
	v_fmac_f32_e32 v118, v119, v115
	v_fma_f32 v114, -v114, v118, v117
	v_div_fmas_f32 v114, v114, v115, v118
	v_div_fixup_f32 v110, v114, v110, 1.0
	v_rcp_f32_e32 v111, v111
	s_nop 3
	v_rcp_f32_e32 v106, v106
	s_nop 3
	v_rcp_f32_e32 v107, v107
	s_nop 3
	v_rcp_f32_e32 v112, v112
	s_nop 3
	v_rcp_f32_e32 v113, v113
	s_nop 3
	v_rcp_f32_e32 v108, v108
	s_nop 3
	v_div_scale_f32 v114, s[48:49], v109, v109, 1.0
	v_rcp_f32_e32 v115, v114
	s_nop 0
	v_fma_f32 v117, -v114, v115, 1.0
	v_fmac_f32_e32 v115, v117, v115
	v_div_scale_f32 v117, vcc, 1.0, v109, 1.0
	v_mul_f32_e32 v118, v117, v115
	v_fma_f32 v119, -v114, v118, v117
	v_fmac_f32_e32 v118, v119, v115
	v_fma_f32 v114, -v114, v118, v117
	v_div_fmas_f32 v114, v114, v115, v118
	v_div_fixup_f32 v109, v114, v109, 1.0

.LBB0_531:
	v_add_u32_e32 v130, v120, v159
	v_lshlrev_b64 v[106:107], 2, v[130:131]
	v_lshl_add_u64 v[114:115], s[22:23], 0, v[106:107]
	global_load_dwordx4 v[108:111], v[114:115], off offset:16
	s_nop 0
	global_load_dwordx4 v[114:117], v[114:115], off
	v_lshl_add_u64 v[106:107], s[28:29], 0, v[106:107]
	global_load_dwordx4 v[122:125], v[106:107], off offset:16
	global_load_dwordx4 v[126:129], v[106:107], off
	v_lshlrev_b32_e32 v106, 16, v2
	v_and_b32_e32 v107, 0xffff0000, v2
	v_lshlrev_b32_e32 v118, 16, v102
	v_and_b32_e32 v119, 0xffff0000, v102
	v_lshlrev_b32_e32 v132, 16, v30
	v_and_b32_e32 v133, 0xffff0000, v30
	v_pk_add_f32 v[118:119], v[118:119], v[106:107] neg_lo:[0,1] neg_hi:[0,1]
	v_lshlrev_b32_e32 v102, 16, v103
	v_and_b32_e32 v103, 0xffff0000, v103
	v_lshrrev_b32_e32 v112, 2, v160
	v_cmp_lt_u32_e32 vcc, s71, v130
	s_waitcnt vmcnt(2)
	v_pk_fma_f32 v[114:115], v[118:119], v[114:115], v[106:107]
	v_pk_add_f32 v[106:107], v[132:133], v[106:107] neg_lo:[0,1] neg_hi:[0,1]
	v_lshlrev_b32_e32 v118, 16, v31
	s_waitcnt vmcnt(0)
	v_pk_fma_f32 v[106:107], v[106:107], v[126:127], v[114:115]
	v_lshlrev_b32_e32 v114, 16, v3
	v_and_b32_e32 v115, 0xffff0000, v3
	v_and_b32_e32 v119, 0xffff0000, v31
	v_pk_add_f32 v[102:103], v[102:103], v[114:115] neg_lo:[0,1] neg_hi:[0,1]
	s_nop 0
	v_pk_fma_f32 v[102:103], v[102:103], v[116:117], v[114:115]
	v_pk_add_f32 v[114:115], v[118:119], v[114:115] neg_lo:[0,1] neg_hi:[0,1]
	v_lshlrev_b32_e32 v116, 16, v104
	v_pk_fma_f32 v[102:103], v[114:115], v[128:129], v[102:103]
	v_lshlrev_b32_e32 v114, 16, v4
	v_and_b32_e32 v115, 0xffff0000, v4
	v_and_b32_e32 v117, 0xffff0000, v104
	v_lshlrev_b32_e32 v118, 16, v32
	v_and_b32_e32 v119, 0xffff0000, v32
	v_pk_add_f32 v[116:117], v[116:117], v[114:115] neg_lo:[0,1] neg_hi:[0,1]
	v_lshlrev_b32_e32 v104, 16, v105
	v_pk_fma_f32 v[108:109], v[116:117], v[108:109], v[114:115]
	v_pk_add_f32 v[114:115], v[118:119], v[114:115] neg_lo:[0,1] neg_hi:[0,1]
	v_and_b32_e32 v105, 0xffff0000, v105
	v_pk_fma_f32 v[108:109], v[114:115], v[122:123], v[108:109]
	v_lshlrev_b32_e32 v114, 16, v5
	v_and_b32_e32 v115, 0xffff0000, v5
	v_lshlrev_b32_e32 v116, 16, v33
	v_and_b32_e32 v117, 0xffff0000, v33
	v_pk_add_f32 v[104:105], v[104:105], v[114:115] neg_lo:[0,1] neg_hi:[0,1]
	s_nop 0
	v_pk_fma_f32 v[104:105], v[104:105], v[110:111], v[114:115]
	v_pk_add_f32 v[110:111], v[116:117], v[114:115] neg_lo:[0,1] neg_hi:[0,1]
	s_nop 0
	v_pk_fma_f32 v[104:105], v[110:111], v[124:125], v[104:105]
	s_and_saveexec_b64 s[14:15], vcc
	s_xor_b64 s[14:15], exec, s[14:15]
	s_cbranch_execz .LBB0_579
	v_cmp_lt_u32_e32 vcc, s72, v130
	s_and_saveexec_b64 s[18:19], vcc
	s_xor_b64 s[18:19], exec, s[18:19]
	s_cbranch_execz .LBB0_576
	v_cmp_lt_u32_e32 vcc, s73, v130
	s_and_saveexec_b64 s[40:41], vcc
	s_xor_b64 s[40:41], exec, s[40:41]
	s_cbranch_execz .LBB0_573
	v_cmp_lt_u32_e32 vcc, s76, v130
	s_and_saveexec_b64 s[42:43], vcc
	s_xor_b64 s[42:43], exec, s[42:43]
	s_cbranch_execz .LBB0_538
	v_cmp_lt_u32_e32 vcc, s77, v130
	s_and_saveexec_b64 s[44:45], vcc
	s_cbranch_execz .LBB0_537
	v_mul_f32_e32 v110, 0xbfb8aa3b, v106
	v_rndne_f32_e32 v111, v110
	v_sub_f32_e32 v113, v110, v111
	v_fma_f32 v110, v106, s78, -v110
	v_fmac_f32_e32 v110, 0xb2a5705f, v106
	v_add_f32_e32 v110, v113, v110
	v_exp_f32_e32 v110, v110
	v_cvt_i32_f32_e32 v111, v111
	v_cmp_nlt_f32_e32 vcc, s79, v106
	v_ldexp_f32 v110, v110, v111
	s_nop 0
	v_cndmask_b32_e32 v110, 0, v110, vcc
	v_cmp_ngt_f32_e32 vcc, s80, v106
	s_nop 1
	v_cndmask_b32_e32 v106, v143, v110, vcc
	v_mul_f32_e32 v110, 0xbfb8aa3b, v107
	v_rndne_f32_e32 v111, v110
	v_sub_f32_e32 v113, v110, v111
	v_fma_f32 v110, v107, s78, -v110
	v_fmac_f32_e32 v110, 0xb2a5705f, v107
	v_add_f32_e32 v110, v113, v110
	v_exp_f32_e32 v110, v110
	v_cvt_i32_f32_e32 v111, v111
	v_cmp_nlt_f32_e32 vcc, s79, v107
	v_ldexp_f32 v110, v110, v111
	s_nop 0
	v_cndmask_b32_e32 v110, 0, v110, vcc
	v_cmp_ngt_f32_e32 vcc, s80, v107
	s_nop 1
	v_cndmask_b32_e32 v107, v143, v110, vcc
	v_mul_f32_e32 v110, 0xbfb8aa3b, v102
	v_rndne_f32_e32 v111, v110
	v_sub_f32_e32 v113, v110, v111
	v_fma_f32 v110, v102, s78, -v110
	v_fmac_f32_e32 v110, 0xb2a5705f, v102
	v_add_f32_e32 v110, v113, v110
	v_exp_f32_e32 v110, v110
	v_cvt_i32_f32_e32 v111, v111
	v_cmp_nlt_f32_e32 vcc, s79, v102
	v_pk_add_f32 v[106:107], v[106:107], 1.0 op_sel_hi:[1,0]
	v_ldexp_f32 v110, v110, v111
	v_cndmask_b32_e32 v110, 0, v110, vcc
	v_cmp_ngt_f32_e32 vcc, s80, v102
	s_nop 1
	v_cndmask_b32_e32 v102, v143, v110, vcc
	v_mul_f32_e32 v110, 0xbfb8aa3b, v103
	v_rndne_f32_e32 v111, v110
	v_sub_f32_e32 v113, v110, v111
	v_fma_f32 v110, v103, s78, -v110
	v_fmac_f32_e32 v110, 0xb2a5705f, v103
	v_add_f32_e32 v110, v113, v110
	v_exp_f32_e32 v110, v110
	v_cvt_i32_f32_e32 v111, v111
	v_cmp_nlt_f32_e32 vcc, s79, v103
	v_ldexp_f32 v110, v110, v111
	s_nop 0
	v_cndmask_b32_e32 v110, 0, v110, vcc
	v_cmp_ngt_f32_e32 vcc, s80, v103
	s_nop 1
	v_cndmask_b32_e32 v103, v143, v110, vcc
	v_mul_f32_e32 v110, 0xbfb8aa3b, v108
	v_rndne_f32_e32 v111, v110
	v_sub_f32_e32 v113, v110, v111
	v_fma_f32 v110, v108, s78, -v110
	v_fmac_f32_e32 v110, 0xb2a5705f, v108
	v_add_f32_e32 v110, v113, v110
	v_exp_f32_e32 v110, v110
	v_cvt_i32_f32_e32 v111, v111
	v_cmp_nlt_f32_e32 vcc, s79, v108
	v_pk_add_f32 v[102:103], v[102:103], 1.0 op_sel_hi:[1,0]
	v_ldexp_f32 v110, v110, v111
	v_cndmask_b32_e32 v110, 0, v110, vcc
	v_cmp_ngt_f32_e32 vcc, s80, v108
	s_nop 1
	v_cndmask_b32_e32 v108, v143, v110, vcc
	v_mul_f32_e32 v110, 0xbfb8aa3b, v109
	v_rndne_f32_e32 v111, v110
	v_sub_f32_e32 v113, v110, v111
	v_fma_f32 v110, v109, s78, -v110
	v_fmac_f32_e32 v110, 0xb2a5705f, v109
	v_add_f32_e32 v110, v113, v110
	v_exp_f32_e32 v110, v110
	v_cvt_i32_f32_e32 v111, v111
	v_cmp_nlt_f32_e32 vcc, s79, v109
	v_ldexp_f32 v110, v110, v111
	s_nop 0
	v_cndmask_b32_e32 v110, 0, v110, vcc
	v_cmp_ngt_f32_e32 vcc, s80, v109
	s_nop 1
	v_cndmask_b32_e32 v109, v143, v110, vcc
	v_mul_f32_e32 v110, 0xbfb8aa3b, v104
	v_rndne_f32_e32 v111, v110
	v_sub_f32_e32 v113, v110, v111
	v_fma_f32 v110, v104, s78, -v110
	v_fmac_f32_e32 v110, 0xb2a5705f, v104
	v_add_f32_e32 v110, v113, v110
	v_exp_f32_e32 v110, v110
	v_cvt_i32_f32_e32 v111, v111
	v_cmp_nlt_f32_e32 vcc, s79, v104
	v_pk_add_f32 v[108:109], v[108:109], 1.0 op_sel_hi:[1,0]
	v_ldexp_f32 v110, v110, v111
	v_cndmask_b32_e32 v110, 0, v110, vcc
	v_cmp_ngt_f32_e32 vcc, s80, v104
	s_nop 1
	v_cndmask_b32_e32 v104, v143, v110, vcc
	v_mul_f32_e32 v110, 0xbfb8aa3b, v105
	v_rndne_f32_e32 v111, v110
	v_sub_f32_e32 v113, v110, v111
	v_fma_f32 v110, v105, s78, -v110
	v_fmac_f32_e32 v110, 0xb2a5705f, v105
	v_add_f32_e32 v110, v113, v110
	v_exp_f32_e32 v110, v110
	v_cvt_i32_f32_e32 v111, v111
	v_cmp_nlt_f32_e32 vcc, s79, v105
	v_ldexp_f32 v110, v110, v111
	s_nop 0
	v_cndmask_b32_e32 v110, 0, v110, vcc
	v_cmp_ngt_f32_e32 vcc, s80, v105
	s_nop 1
	v_cndmask_b32_e32 v105, v143, v110, vcc
	v_div_scale_f32 v110, s[46:47], v106, v106, 1.0
	v_rcp_f32_e32 v111, v110
	v_pk_add_f32 v[104:105], v[104:105], 1.0 op_sel_hi:[1,0]
	v_fma_f32 v113, -v110, v111, 1.0
	v_fmac_f32_e32 v111, v113, v111
	v_div_scale_f32 v113, vcc, 1.0, v106, 1.0
	v_mul_f32_e32 v114, v113, v111
	v_fma_f32 v115, -v110, v114, v113
	v_fmac_f32_e32 v114, v115, v111
	v_fma_f32 v110, -v110, v114, v113
	v_div_fmas_f32 v110, v110, v111, v114
	v_div_fixup_f32 v106, v110, v106, 1.0
	v_rcp_f32_e32 v107, v107
	s_nop 3
	v_rcp_f32_e32 v102, v102
	s_nop 3
	v_rcp_f32_e32 v103, v103
	s_nop 3
	v_rcp_f32_e32 v108, v108
	s_nop 3
	v_rcp_f32_e32 v109, v109
	s_nop 3
	v_rcp_f32_e32 v104, v104
	s_nop 3
	v_div_scale_f32 v110, s[46:47], v105, v105, 1.0
	v_rcp_f32_e32 v111, v110
	s_nop 0
	v_fma_f32 v113, -v110, v111, 1.0
	v_fmac_f32_e32 v111, v113, v111
	v_div_scale_f32 v113, vcc, 1.0, v105, 1.0
	v_mul_f32_e32 v114, v113, v111
	v_fma_f32 v115, -v110, v114, v113
	v_fmac_f32_e32 v114, v115, v111
	v_fma_f32 v110, -v110, v114, v113
	v_div_fmas_f32 v110, v110, v111, v114
	v_div_fixup_f32 v105, v110, v105, 1.0

.LBB0_582:
	v_add_u32_e32 v130, v120, v156
	v_lshlrev_b64 v[102:103], 2, v[130:131]
	v_lshl_add_u64 v[110:111], s[22:23], 0, v[102:103]
	global_load_dwordx4 v[104:107], v[110:111], off offset:16
	s_nop 0
	global_load_dwordx4 v[110:113], v[110:111], off
	v_lshl_add_u64 v[102:103], s[28:29], 0, v[102:103]
	global_load_dwordx4 v[114:117], v[102:103], off offset:16
	global_load_dwordx4 v[122:125], v[102:103], off
	v_lshlrev_b32_e32 v102, 16, v14
	v_and_b32_e32 v103, 0xffff0000, v14
	v_lshlrev_b32_e32 v118, 16, v98
	v_and_b32_e32 v119, 0xffff0000, v98
	v_lshlrev_b32_e32 v126, 16, v46
	v_and_b32_e32 v127, 0xffff0000, v46
	v_pk_add_f32 v[118:119], v[118:119], v[102:103] neg_lo:[0,1] neg_hi:[0,1]
	v_lshlrev_b32_e32 v98, 16, v99
	v_and_b32_e32 v99, 0xffff0000, v99
	v_lshrrev_b32_e32 v108, 2, v157
	v_cmp_lt_u32_e32 vcc, s71, v130
	s_waitcnt vmcnt(2)
	v_pk_fma_f32 v[110:111], v[118:119], v[110:111], v[102:103]
	v_pk_add_f32 v[102:103], v[126:127], v[102:103] neg_lo:[0,1] neg_hi:[0,1]
	v_lshlrev_b32_e32 v118, 16, v47
	s_waitcnt vmcnt(0)
	v_pk_fma_f32 v[102:103], v[102:103], v[122:123], v[110:111]
	v_lshlrev_b32_e32 v110, 16, v15
	v_and_b32_e32 v111, 0xffff0000, v15
	v_and_b32_e32 v119, 0xffff0000, v47
	v_pk_add_f32 v[98:99], v[98:99], v[110:111] neg_lo:[0,1] neg_hi:[0,1]
	s_nop 0
	v_pk_fma_f32 v[98:99], v[98:99], v[112:113], v[110:111]
	v_pk_add_f32 v[110:111], v[118:119], v[110:111] neg_lo:[0,1] neg_hi:[0,1]
	v_lshlrev_b32_e32 v112, 16, v100
	v_pk_fma_f32 v[98:99], v[110:111], v[124:125], v[98:99]
	v_lshlrev_b32_e32 v110, 16, v16
	v_and_b32_e32 v111, 0xffff0000, v16
	v_and_b32_e32 v113, 0xffff0000, v100
	v_lshlrev_b32_e32 v118, 16, v48
	v_and_b32_e32 v119, 0xffff0000, v48
	v_pk_add_f32 v[112:113], v[112:113], v[110:111] neg_lo:[0,1] neg_hi:[0,1]
	v_lshlrev_b32_e32 v100, 16, v101
	v_pk_fma_f32 v[104:105], v[112:113], v[104:105], v[110:111]
	v_pk_add_f32 v[110:111], v[118:119], v[110:111] neg_lo:[0,1] neg_hi:[0,1]
	v_and_b32_e32 v101, 0xffff0000, v101
	v_pk_fma_f32 v[104:105], v[110:111], v[114:115], v[104:105]
	v_lshlrev_b32_e32 v110, 16, v17
	v_and_b32_e32 v111, 0xffff0000, v17
	v_lshlrev_b32_e32 v112, 16, v49
	v_and_b32_e32 v113, 0xffff0000, v49
	v_pk_add_f32 v[100:101], v[100:101], v[110:111] neg_lo:[0,1] neg_hi:[0,1]
	s_nop 0
	v_pk_fma_f32 v[100:101], v[100:101], v[106:107], v[110:111]
	v_pk_add_f32 v[106:107], v[112:113], v[110:111] neg_lo:[0,1] neg_hi:[0,1]
	s_nop 0
	v_pk_fma_f32 v[100:101], v[106:107], v[116:117], v[100:101]
	s_and_saveexec_b64 s[12:13], vcc
	s_xor_b64 s[12:13], exec, s[12:13]
	s_cbranch_execz .LBB0_630
	v_cmp_lt_u32_e32 vcc, s72, v130
	s_and_saveexec_b64 s[16:17], vcc
	s_xor_b64 s[16:17], exec, s[16:17]
	s_cbranch_execz .LBB0_627
	v_cmp_lt_u32_e32 vcc, s73, v130
	s_and_saveexec_b64 s[18:19], vcc
	s_xor_b64 s[18:19], exec, s[18:19]
	s_cbranch_execz .LBB0_624
	v_cmp_lt_u32_e32 vcc, s76, v130
	s_and_saveexec_b64 s[40:41], vcc
	s_xor_b64 s[40:41], exec, s[40:41]
	s_cbranch_execz .LBB0_589
	v_cmp_lt_u32_e32 vcc, s77, v130
	s_and_saveexec_b64 s[42:43], vcc
	s_cbranch_execz .LBB0_588
	v_mul_f32_e32 v106, 0xbfb8aa3b, v102
	v_rndne_f32_e32 v107, v106
	v_sub_f32_e32 v109, v106, v107
	v_fma_f32 v106, v102, s78, -v106
	v_fmac_f32_e32 v106, 0xb2a5705f, v102
	v_add_f32_e32 v106, v109, v106
	v_exp_f32_e32 v106, v106
	v_cvt_i32_f32_e32 v107, v107
	v_cmp_nlt_f32_e32 vcc, s79, v102
	v_ldexp_f32 v106, v106, v107
	s_nop 0
	v_cndmask_b32_e32 v106, 0, v106, vcc
	v_cmp_ngt_f32_e32 vcc, s80, v102
	s_nop 1
	v_cndmask_b32_e32 v102, v143, v106, vcc
	v_mul_f32_e32 v106, 0xbfb8aa3b, v103
	v_rndne_f32_e32 v107, v106
	v_sub_f32_e32 v109, v106, v107
	v_fma_f32 v106, v103, s78, -v106
	v_fmac_f32_e32 v106, 0xb2a5705f, v103
	v_add_f32_e32 v106, v109, v106
	v_exp_f32_e32 v106, v106
	v_cvt_i32_f32_e32 v107, v107
	v_cmp_nlt_f32_e32 vcc, s79, v103
	v_ldexp_f32 v106, v106, v107
	s_nop 0
	v_cndmask_b32_e32 v106, 0, v106, vcc
	v_cmp_ngt_f32_e32 vcc, s80, v103
	s_nop 1
	v_cndmask_b32_e32 v103, v143, v106, vcc
	v_mul_f32_e32 v106, 0xbfb8aa3b, v98
	v_rndne_f32_e32 v107, v106
	v_sub_f32_e32 v109, v106, v107
	v_fma_f32 v106, v98, s78, -v106
	v_fmac_f32_e32 v106, 0xb2a5705f, v98
	v_add_f32_e32 v106, v109, v106
	v_exp_f32_e32 v106, v106
	v_cvt_i32_f32_e32 v107, v107
	v_cmp_nlt_f32_e32 vcc, s79, v98
	v_pk_add_f32 v[102:103], v[102:103], 1.0 op_sel_hi:[1,0]
	v_ldexp_f32 v106, v106, v107
	v_cndmask_b32_e32 v106, 0, v106, vcc
	v_cmp_ngt_f32_e32 vcc, s80, v98
	s_nop 1
	v_cndmask_b32_e32 v98, v143, v106, vcc
	v_mul_f32_e32 v106, 0xbfb8aa3b, v99
	v_rndne_f32_e32 v107, v106
	v_sub_f32_e32 v109, v106, v107
	v_fma_f32 v106, v99, s78, -v106
	v_fmac_f32_e32 v106, 0xb2a5705f, v99
	v_add_f32_e32 v106, v109, v106
	v_exp_f32_e32 v106, v106
	v_cvt_i32_f32_e32 v107, v107
	v_cmp_nlt_f32_e32 vcc, s79, v99
	v_ldexp_f32 v106, v106, v107
	s_nop 0
	v_cndmask_b32_e32 v106, 0, v106, vcc
	v_cmp_ngt_f32_e32 vcc, s80, v99
	s_nop 1
	v_cndmask_b32_e32 v99, v143, v106, vcc
	v_mul_f32_e32 v106, 0xbfb8aa3b, v104
	v_rndne_f32_e32 v107, v106
	v_sub_f32_e32 v109, v106, v107
	v_fma_f32 v106, v104, s78, -v106
	v_fmac_f32_e32 v106, 0xb2a5705f, v104
	v_add_f32_e32 v106, v109, v106
	v_exp_f32_e32 v106, v106
	v_cvt_i32_f32_e32 v107, v107
	v_cmp_nlt_f32_e32 vcc, s79, v104
	v_pk_add_f32 v[98:99], v[98:99], 1.0 op_sel_hi:[1,0]
	v_ldexp_f32 v106, v106, v107
	v_cndmask_b32_e32 v106, 0, v106, vcc
	v_cmp_ngt_f32_e32 vcc, s80, v104
	s_nop 1
	v_cndmask_b32_e32 v104, v143, v106, vcc
	v_mul_f32_e32 v106, 0xbfb8aa3b, v105
	v_rndne_f32_e32 v107, v106
	v_sub_f32_e32 v109, v106, v107
	v_fma_f32 v106, v105, s78, -v106
	v_fmac_f32_e32 v106, 0xb2a5705f, v105
	v_add_f32_e32 v106, v109, v106
	v_exp_f32_e32 v106, v106
	v_cvt_i32_f32_e32 v107, v107
	v_cmp_nlt_f32_e32 vcc, s79, v105
	v_ldexp_f32 v106, v106, v107
	s_nop 0
	v_cndmask_b32_e32 v106, 0, v106, vcc
	v_cmp_ngt_f32_e32 vcc, s80, v105
	s_nop 1
	v_cndmask_b32_e32 v105, v143, v106, vcc
	v_mul_f32_e32 v106, 0xbfb8aa3b, v100
	v_rndne_f32_e32 v107, v106
	v_sub_f32_e32 v109, v106, v107
	v_fma_f32 v106, v100, s78, -v106
	v_fmac_f32_e32 v106, 0xb2a5705f, v100
	v_add_f32_e32 v106, v109, v106
	v_exp_f32_e32 v106, v106
	v_cvt_i32_f32_e32 v107, v107
	v_cmp_nlt_f32_e32 vcc, s79, v100
	v_pk_add_f32 v[104:105], v[104:105], 1.0 op_sel_hi:[1,0]
	v_ldexp_f32 v106, v106, v107
	v_cndmask_b32_e32 v106, 0, v106, vcc
	v_cmp_ngt_f32_e32 vcc, s80, v100
	s_nop 1
	v_cndmask_b32_e32 v100, v143, v106, vcc
	v_mul_f32_e32 v106, 0xbfb8aa3b, v101
	v_rndne_f32_e32 v107, v106
	v_sub_f32_e32 v109, v106, v107
	v_fma_f32 v106, v101, s78, -v106
	v_fmac_f32_e32 v106, 0xb2a5705f, v101
	v_add_f32_e32 v106, v109, v106
	v_exp_f32_e32 v106, v106
	v_cvt_i32_f32_e32 v107, v107
	v_cmp_nlt_f32_e32 vcc, s79, v101
	v_ldexp_f32 v106, v106, v107
	s_nop 0
	v_cndmask_b32_e32 v106, 0, v106, vcc
	v_cmp_ngt_f32_e32 vcc, s80, v101
	s_nop 1
	v_cndmask_b32_e32 v101, v143, v106, vcc
	v_div_scale_f32 v106, s[44:45], v102, v102, 1.0
	v_rcp_f32_e32 v107, v106
	v_pk_add_f32 v[100:101], v[100:101], 1.0 op_sel_hi:[1,0]
	v_fma_f32 v109, -v106, v107, 1.0
	v_fmac_f32_e32 v107, v109, v107
	v_div_scale_f32 v109, vcc, 1.0, v102, 1.0
	v_mul_f32_e32 v110, v109, v107
	v_fma_f32 v111, -v106, v110, v109
	v_fmac_f32_e32 v110, v111, v107
	v_fma_f32 v106, -v106, v110, v109
	v_div_fmas_f32 v106, v106, v107, v110
	v_div_fixup_f32 v102, v106, v102, 1.0
	v_rcp_f32_e32 v103, v103
	s_nop 3
	v_rcp_f32_e32 v98, v98
	s_nop 3
	v_rcp_f32_e32 v99, v99
	s_nop 3
	v_rcp_f32_e32 v104, v104
	s_nop 3
	v_rcp_f32_e32 v105, v105
	s_nop 3
	v_rcp_f32_e32 v100, v100
	s_nop 3
	v_div_scale_f32 v106, s[44:45], v101, v101, 1.0
	v_rcp_f32_e32 v107, v106
	s_nop 0
	v_fma_f32 v109, -v106, v107, 1.0
	v_fmac_f32_e32 v107, v109, v107
	v_div_scale_f32 v109, vcc, 1.0, v101, 1.0
	v_mul_f32_e32 v110, v109, v107
	v_fma_f32 v111, -v106, v110, v109
	v_fmac_f32_e32 v110, v111, v107
	v_fma_f32 v106, -v106, v110, v109
	v_div_fmas_f32 v106, v106, v107, v110
	v_div_fixup_f32 v101, v106, v101, 1.0

.LBB0_633:
	v_add_u32_e32 v130, v120, v153
	v_lshlrev_b64 v[98:99], 2, v[130:131]
	v_lshl_add_u64 v[106:107], s[22:23], 0, v[98:99]
	global_load_dwordx4 v[100:103], v[106:107], off offset:16
	s_nop 0
	global_load_dwordx4 v[106:109], v[106:107], off
	v_lshl_add_u64 v[98:99], s[28:29], 0, v[98:99]
	global_load_dwordx4 v[110:113], v[98:99], off offset:16
	global_load_dwordx4 v[114:117], v[98:99], off
	v_lshlrev_b32_e32 v98, 16, v18
	v_and_b32_e32 v99, 0xffff0000, v18
	v_lshlrev_b32_e32 v118, 16, v94
	v_and_b32_e32 v119, 0xffff0000, v94
	v_lshlrev_b32_e32 v122, 16, v54
	v_and_b32_e32 v123, 0xffff0000, v54
	v_pk_add_f32 v[118:119], v[118:119], v[98:99] neg_lo:[0,1] neg_hi:[0,1]
	v_lshlrev_b32_e32 v94, 16, v95
	v_and_b32_e32 v95, 0xffff0000, v95
	v_lshrrev_b32_e32 v104, 2, v154
	v_cmp_lt_u32_e32 vcc, s71, v130
	s_waitcnt vmcnt(2)
	v_pk_fma_f32 v[106:107], v[118:119], v[106:107], v[98:99]
	v_pk_add_f32 v[98:99], v[122:123], v[98:99] neg_lo:[0,1] neg_hi:[0,1]
	s_waitcnt vmcnt(0)
	v_pk_fma_f32 v[98:99], v[98:99], v[114:115], v[106:107]
	v_lshlrev_b32_e32 v106, 16, v19
	v_and_b32_e32 v107, 0xffff0000, v19
	v_lshlrev_b32_e32 v114, 16, v55
	v_and_b32_e32 v115, 0xffff0000, v55
	v_pk_add_f32 v[94:95], v[94:95], v[106:107] neg_lo:[0,1] neg_hi:[0,1]
	s_nop 0
	v_pk_fma_f32 v[94:95], v[94:95], v[108:109], v[106:107]
	v_pk_add_f32 v[106:107], v[114:115], v[106:107] neg_lo:[0,1] neg_hi:[0,1]
	v_lshlrev_b32_e32 v108, 16, v96
	v_pk_fma_f32 v[94:95], v[106:107], v[116:117], v[94:95]
	v_lshlrev_b32_e32 v106, 16, v20
	v_and_b32_e32 v107, 0xffff0000, v20
	v_and_b32_e32 v109, 0xffff0000, v96
	v_lshlrev_b32_e32 v114, 16, v56
	v_and_b32_e32 v115, 0xffff0000, v56
	v_pk_add_f32 v[108:109], v[108:109], v[106:107] neg_lo:[0,1] neg_hi:[0,1]
	v_lshlrev_b32_e32 v96, 16, v97
	v_pk_fma_f32 v[100:101], v[108:109], v[100:101], v[106:107]
	v_pk_add_f32 v[106:107], v[114:115], v[106:107] neg_lo:[0,1] neg_hi:[0,1]
	v_and_b32_e32 v97, 0xffff0000, v97
	v_pk_fma_f32 v[100:101], v[106:107], v[110:111], v[100:101]
	v_lshlrev_b32_e32 v106, 16, v21
	v_and_b32_e32 v107, 0xffff0000, v21
	v_lshlrev_b32_e32 v108, 16, v57
	v_and_b32_e32 v109, 0xffff0000, v57
	v_pk_add_f32 v[96:97], v[96:97], v[106:107] neg_lo:[0,1] neg_hi:[0,1]
	s_nop 0
	v_pk_fma_f32 v[96:97], v[96:97], v[102:103], v[106:107]
	v_pk_add_f32 v[102:103], v[108:109], v[106:107] neg_lo:[0,1] neg_hi:[0,1]
	s_nop 0
	v_pk_fma_f32 v[96:97], v[102:103], v[112:113], v[96:97]
	s_and_saveexec_b64 s[10:11], vcc
	s_xor_b64 s[10:11], exec, s[10:11]
	s_cbranch_execz .LBB0_681
	v_cmp_lt_u32_e32 vcc, s72, v130
	s_and_saveexec_b64 s[14:15], vcc
	s_xor_b64 s[14:15], exec, s[14:15]
	s_cbranch_execz .LBB0_678
	v_cmp_lt_u32_e32 vcc, s73, v130
	s_and_saveexec_b64 s[16:17], vcc
	s_xor_b64 s[16:17], exec, s[16:17]
	s_cbranch_execz .LBB0_675
	v_cmp_lt_u32_e32 vcc, s76, v130
	s_and_saveexec_b64 s[18:19], vcc
	s_xor_b64 s[18:19], exec, s[18:19]
	s_cbranch_execz .LBB0_640
	v_cmp_lt_u32_e32 vcc, s77, v130
	s_and_saveexec_b64 s[40:41], vcc
	s_cbranch_execz .LBB0_639
	v_mul_f32_e32 v102, 0xbfb8aa3b, v98
	v_rndne_f32_e32 v103, v102
	v_sub_f32_e32 v105, v102, v103
	v_fma_f32 v102, v98, s78, -v102
	v_fmac_f32_e32 v102, 0xb2a5705f, v98
	v_add_f32_e32 v102, v105, v102
	v_exp_f32_e32 v102, v102
	v_cvt_i32_f32_e32 v103, v103
	v_cmp_nlt_f32_e32 vcc, s79, v98
	v_ldexp_f32 v102, v102, v103
	s_nop 0
	v_cndmask_b32_e32 v102, 0, v102, vcc
	v_cmp_ngt_f32_e32 vcc, s80, v98
	s_nop 1
	v_cndmask_b32_e32 v98, v143, v102, vcc
	v_mul_f32_e32 v102, 0xbfb8aa3b, v99
	v_rndne_f32_e32 v103, v102
	v_sub_f32_e32 v105, v102, v103
	v_fma_f32 v102, v99, s78, -v102
	v_fmac_f32_e32 v102, 0xb2a5705f, v99
	v_add_f32_e32 v102, v105, v102
	v_exp_f32_e32 v102, v102
	v_cvt_i32_f32_e32 v103, v103
	v_cmp_nlt_f32_e32 vcc, s79, v99
	v_ldexp_f32 v102, v102, v103
	s_nop 0
	v_cndmask_b32_e32 v102, 0, v102, vcc
	v_cmp_ngt_f32_e32 vcc, s80, v99
	s_nop 1
	v_cndmask_b32_e32 v99, v143, v102, vcc
	v_mul_f32_e32 v102, 0xbfb8aa3b, v94
	v_rndne_f32_e32 v103, v102
	v_sub_f32_e32 v105, v102, v103
	v_fma_f32 v102, v94, s78, -v102
	v_fmac_f32_e32 v102, 0xb2a5705f, v94
	v_add_f32_e32 v102, v105, v102
	v_exp_f32_e32 v102, v102
	v_cvt_i32_f32_e32 v103, v103
	v_cmp_nlt_f32_e32 vcc, s79, v94
	v_pk_add_f32 v[98:99], v[98:99], 1.0 op_sel_hi:[1,0]
	v_ldexp_f32 v102, v102, v103
	v_cndmask_b32_e32 v102, 0, v102, vcc
	v_cmp_ngt_f32_e32 vcc, s80, v94
	s_nop 1
	v_cndmask_b32_e32 v94, v143, v102, vcc
	v_mul_f32_e32 v102, 0xbfb8aa3b, v95
	v_rndne_f32_e32 v103, v102
	v_sub_f32_e32 v105, v102, v103
	v_fma_f32 v102, v95, s78, -v102
	v_fmac_f32_e32 v102, 0xb2a5705f, v95
	v_add_f32_e32 v102, v105, v102
	v_exp_f32_e32 v102, v102
	v_cvt_i32_f32_e32 v103, v103
	v_cmp_nlt_f32_e32 vcc, s79, v95
	v_ldexp_f32 v102, v102, v103
	s_nop 0
	v_cndmask_b32_e32 v102, 0, v102, vcc
	v_cmp_ngt_f32_e32 vcc, s80, v95
	s_nop 1
	v_cndmask_b32_e32 v95, v143, v102, vcc
	v_mul_f32_e32 v102, 0xbfb8aa3b, v100
	v_rndne_f32_e32 v103, v102
	v_sub_f32_e32 v105, v102, v103
	v_fma_f32 v102, v100, s78, -v102
	v_fmac_f32_e32 v102, 0xb2a5705f, v100
	v_add_f32_e32 v102, v105, v102
	v_exp_f32_e32 v102, v102
	v_cvt_i32_f32_e32 v103, v103
	v_cmp_nlt_f32_e32 vcc, s79, v100
	v_pk_add_f32 v[94:95], v[94:95], 1.0 op_sel_hi:[1,0]
	v_ldexp_f32 v102, v102, v103
	v_cndmask_b32_e32 v102, 0, v102, vcc
	v_cmp_ngt_f32_e32 vcc, s80, v100
	s_nop 1
	v_cndmask_b32_e32 v100, v143, v102, vcc
	v_mul_f32_e32 v102, 0xbfb8aa3b, v101
	v_rndne_f32_e32 v103, v102
	v_sub_f32_e32 v105, v102, v103
	v_fma_f32 v102, v101, s78, -v102
	v_fmac_f32_e32 v102, 0xb2a5705f, v101
	v_add_f32_e32 v102, v105, v102
	v_exp_f32_e32 v102, v102
	v_cvt_i32_f32_e32 v103, v103
	v_cmp_nlt_f32_e32 vcc, s79, v101
	v_ldexp_f32 v102, v102, v103
	s_nop 0
	v_cndmask_b32_e32 v102, 0, v102, vcc
	v_cmp_ngt_f32_e32 vcc, s80, v101
	s_nop 1
	v_cndmask_b32_e32 v101, v143, v102, vcc
	v_mul_f32_e32 v102, 0xbfb8aa3b, v96
	v_rndne_f32_e32 v103, v102
	v_sub_f32_e32 v105, v102, v103
	v_fma_f32 v102, v96, s78, -v102
	v_fmac_f32_e32 v102, 0xb2a5705f, v96
	v_add_f32_e32 v102, v105, v102
	v_exp_f32_e32 v102, v102
	v_cvt_i32_f32_e32 v103, v103
	v_cmp_nlt_f32_e32 vcc, s79, v96
	v_pk_add_f32 v[100:101], v[100:101], 1.0 op_sel_hi:[1,0]
	v_ldexp_f32 v102, v102, v103
	v_cndmask_b32_e32 v102, 0, v102, vcc
	v_cmp_ngt_f32_e32 vcc, s80, v96
	s_nop 1
	v_cndmask_b32_e32 v96, v143, v102, vcc
	v_mul_f32_e32 v102, 0xbfb8aa3b, v97
	v_rndne_f32_e32 v103, v102
	v_sub_f32_e32 v105, v102, v103
	v_fma_f32 v102, v97, s78, -v102
	v_fmac_f32_e32 v102, 0xb2a5705f, v97
	v_add_f32_e32 v102, v105, v102
	v_exp_f32_e32 v102, v102
	v_cvt_i32_f32_e32 v103, v103
	v_cmp_nlt_f32_e32 vcc, s79, v97
	v_ldexp_f32 v102, v102, v103
	s_nop 0
	v_cndmask_b32_e32 v102, 0, v102, vcc
	v_cmp_ngt_f32_e32 vcc, s80, v97
	s_nop 1
	v_cndmask_b32_e32 v97, v143, v102, vcc
	v_div_scale_f32 v102, s[42:43], v98, v98, 1.0
	v_rcp_f32_e32 v103, v102
	v_pk_add_f32 v[96:97], v[96:97], 1.0 op_sel_hi:[1,0]
	v_fma_f32 v105, -v102, v103, 1.0
	v_fmac_f32_e32 v103, v105, v103
	v_div_scale_f32 v105, vcc, 1.0, v98, 1.0
	v_mul_f32_e32 v106, v105, v103
	v_fma_f32 v107, -v102, v106, v105
	v_fmac_f32_e32 v106, v107, v103
	v_fma_f32 v102, -v102, v106, v105
	v_div_fmas_f32 v102, v102, v103, v106
	v_div_fixup_f32 v98, v102, v98, 1.0
	v_rcp_f32_e32 v99, v99
	s_nop 3
	v_rcp_f32_e32 v94, v94
	s_nop 3
	v_rcp_f32_e32 v95, v95
	s_nop 3
	v_rcp_f32_e32 v100, v100
	s_nop 3
	v_rcp_f32_e32 v101, v101
	s_nop 3
	v_rcp_f32_e32 v96, v96
	s_nop 3
	v_div_scale_f32 v102, s[42:43], v97, v97, 1.0
	v_rcp_f32_e32 v103, v102
	s_nop 0
	v_fma_f32 v105, -v102, v103, 1.0
	v_fmac_f32_e32 v103, v105, v103
	v_div_scale_f32 v105, vcc, 1.0, v97, 1.0
	v_mul_f32_e32 v106, v105, v103
	v_fma_f32 v107, -v102, v106, v105
	v_fmac_f32_e32 v106, v107, v103
	v_fma_f32 v102, -v102, v106, v105
	v_div_fmas_f32 v102, v102, v103, v106
	v_div_fixup_f32 v97, v102, v97, 1.0

.LBB0_684:
	v_add_u32_e32 v130, v120, v150
	v_lshlrev_b64 v[94:95], 2, v[130:131]
	v_lshl_add_u64 v[102:103], s[22:23], 0, v[94:95]
	global_load_dwordx4 v[96:99], v[102:103], off offset:16
	s_nop 0
	global_load_dwordx4 v[102:105], v[102:103], off
	v_lshl_add_u64 v[94:95], s[28:29], 0, v[94:95]
	global_load_dwordx4 v[106:109], v[94:95], off offset:16
	global_load_dwordx4 v[110:113], v[94:95], off
	v_lshlrev_b32_e32 v94, 16, v22
	v_and_b32_e32 v95, 0xffff0000, v22
	v_lshlrev_b32_e32 v114, 16, v90
	v_and_b32_e32 v115, 0xffff0000, v90
	v_lshlrev_b32_e32 v116, 16, v62
	v_and_b32_e32 v117, 0xffff0000, v62
	v_pk_add_f32 v[114:115], v[114:115], v[94:95] neg_lo:[0,1] neg_hi:[0,1]
	v_lshlrev_b32_e32 v90, 16, v91
	v_and_b32_e32 v91, 0xffff0000, v91
	v_lshrrev_b32_e32 v100, 2, v151
	v_cmp_lt_u32_e32 vcc, s71, v130
	s_waitcnt vmcnt(2)
	v_pk_fma_f32 v[102:103], v[114:115], v[102:103], v[94:95]
	v_pk_add_f32 v[94:95], v[116:117], v[94:95] neg_lo:[0,1] neg_hi:[0,1]
	s_waitcnt vmcnt(0)
	v_pk_fma_f32 v[94:95], v[94:95], v[110:111], v[102:103]
	v_lshlrev_b32_e32 v102, 16, v23
	v_and_b32_e32 v103, 0xffff0000, v23
	v_lshlrev_b32_e32 v110, 16, v63
	v_and_b32_e32 v111, 0xffff0000, v63
	v_pk_add_f32 v[90:91], v[90:91], v[102:103] neg_lo:[0,1] neg_hi:[0,1]
	s_nop 0
	v_pk_fma_f32 v[90:91], v[90:91], v[104:105], v[102:103]
	v_pk_add_f32 v[102:103], v[110:111], v[102:103] neg_lo:[0,1] neg_hi:[0,1]
	v_lshlrev_b32_e32 v104, 16, v92
	v_pk_fma_f32 v[90:91], v[102:103], v[112:113], v[90:91]
	v_lshlrev_b32_e32 v102, 16, v24
	v_and_b32_e32 v103, 0xffff0000, v24
	v_and_b32_e32 v105, 0xffff0000, v92
	v_lshlrev_b32_e32 v110, 16, v64
	v_and_b32_e32 v111, 0xffff0000, v64
	v_pk_add_f32 v[104:105], v[104:105], v[102:103] neg_lo:[0,1] neg_hi:[0,1]
	v_lshlrev_b32_e32 v92, 16, v93
	v_pk_fma_f32 v[96:97], v[104:105], v[96:97], v[102:103]
	v_pk_add_f32 v[102:103], v[110:111], v[102:103] neg_lo:[0,1] neg_hi:[0,1]
	v_and_b32_e32 v93, 0xffff0000, v93
	v_pk_fma_f32 v[96:97], v[102:103], v[106:107], v[96:97]
	v_lshlrev_b32_e32 v102, 16, v25
	v_and_b32_e32 v103, 0xffff0000, v25
	v_lshlrev_b32_e32 v104, 16, v65
	v_and_b32_e32 v105, 0xffff0000, v65
	v_pk_add_f32 v[92:93], v[92:93], v[102:103] neg_lo:[0,1] neg_hi:[0,1]
	s_nop 0
	v_pk_fma_f32 v[92:93], v[92:93], v[98:99], v[102:103]
	v_pk_add_f32 v[98:99], v[104:105], v[102:103] neg_lo:[0,1] neg_hi:[0,1]
	s_nop 0
	v_pk_fma_f32 v[92:93], v[98:99], v[108:109], v[92:93]
	s_and_saveexec_b64 s[8:9], vcc
	s_xor_b64 s[8:9], exec, s[8:9]
	s_cbranch_execz .LBB0_732
	v_cmp_lt_u32_e32 vcc, s72, v130
	s_and_saveexec_b64 s[12:13], vcc
	s_xor_b64 s[12:13], exec, s[12:13]
	s_cbranch_execz .LBB0_729
	v_cmp_lt_u32_e32 vcc, s73, v130
	s_and_saveexec_b64 s[14:15], vcc
	s_xor_b64 s[14:15], exec, s[14:15]
	s_cbranch_execz .LBB0_726
	v_cmp_lt_u32_e32 vcc, s76, v130
	s_and_saveexec_b64 s[16:17], vcc
	s_xor_b64 s[16:17], exec, s[16:17]
	s_cbranch_execz .LBB0_691
	v_cmp_lt_u32_e32 vcc, s77, v130
	s_and_saveexec_b64 s[18:19], vcc
	s_cbranch_execz .LBB0_690
	v_mul_f32_e32 v98, 0xbfb8aa3b, v94
	v_rndne_f32_e32 v99, v98
	v_sub_f32_e32 v101, v98, v99
	v_fma_f32 v98, v94, s78, -v98
	v_fmac_f32_e32 v98, 0xb2a5705f, v94
	v_add_f32_e32 v98, v101, v98
	v_exp_f32_e32 v98, v98
	v_cvt_i32_f32_e32 v99, v99
	v_cmp_nlt_f32_e32 vcc, s79, v94
	v_ldexp_f32 v98, v98, v99
	s_nop 0
	v_cndmask_b32_e32 v98, 0, v98, vcc
	v_cmp_ngt_f32_e32 vcc, s80, v94
	s_nop 1
	v_cndmask_b32_e32 v94, v143, v98, vcc
	v_mul_f32_e32 v98, 0xbfb8aa3b, v95
	v_rndne_f32_e32 v99, v98
	v_sub_f32_e32 v101, v98, v99
	v_fma_f32 v98, v95, s78, -v98
	v_fmac_f32_e32 v98, 0xb2a5705f, v95
	v_add_f32_e32 v98, v101, v98
	v_exp_f32_e32 v98, v98
	v_cvt_i32_f32_e32 v99, v99
	v_cmp_nlt_f32_e32 vcc, s79, v95
	v_ldexp_f32 v98, v98, v99
	s_nop 0
	v_cndmask_b32_e32 v98, 0, v98, vcc
	v_cmp_ngt_f32_e32 vcc, s80, v95
	s_nop 1
	v_cndmask_b32_e32 v95, v143, v98, vcc
	v_mul_f32_e32 v98, 0xbfb8aa3b, v90
	v_rndne_f32_e32 v99, v98
	v_sub_f32_e32 v101, v98, v99
	v_fma_f32 v98, v90, s78, -v98
	v_fmac_f32_e32 v98, 0xb2a5705f, v90
	v_add_f32_e32 v98, v101, v98
	v_exp_f32_e32 v98, v98
	v_cvt_i32_f32_e32 v99, v99
	v_cmp_nlt_f32_e32 vcc, s79, v90
	v_pk_add_f32 v[94:95], v[94:95], 1.0 op_sel_hi:[1,0]
	v_ldexp_f32 v98, v98, v99
	v_cndmask_b32_e32 v98, 0, v98, vcc
	v_cmp_ngt_f32_e32 vcc, s80, v90
	s_nop 1
	v_cndmask_b32_e32 v90, v143, v98, vcc
	v_mul_f32_e32 v98, 0xbfb8aa3b, v91
	v_rndne_f32_e32 v99, v98
	v_sub_f32_e32 v101, v98, v99
	v_fma_f32 v98, v91, s78, -v98
	v_fmac_f32_e32 v98, 0xb2a5705f, v91
	v_add_f32_e32 v98, v101, v98
	v_exp_f32_e32 v98, v98
	v_cvt_i32_f32_e32 v99, v99
	v_cmp_nlt_f32_e32 vcc, s79, v91
	v_ldexp_f32 v98, v98, v99
	s_nop 0
	v_cndmask_b32_e32 v98, 0, v98, vcc
	v_cmp_ngt_f32_e32 vcc, s80, v91
	s_nop 1
	v_cndmask_b32_e32 v91, v143, v98, vcc
	v_mul_f32_e32 v98, 0xbfb8aa3b, v96
	v_rndne_f32_e32 v99, v98
	v_sub_f32_e32 v101, v98, v99
	v_fma_f32 v98, v96, s78, -v98
	v_fmac_f32_e32 v98, 0xb2a5705f, v96
	v_add_f32_e32 v98, v101, v98
	v_exp_f32_e32 v98, v98
	v_cvt_i32_f32_e32 v99, v99
	v_cmp_nlt_f32_e32 vcc, s79, v96
	v_pk_add_f32 v[90:91], v[90:91], 1.0 op_sel_hi:[1,0]
	v_ldexp_f32 v98, v98, v99
	v_cndmask_b32_e32 v98, 0, v98, vcc
	v_cmp_ngt_f32_e32 vcc, s80, v96
	s_nop 1
	v_cndmask_b32_e32 v96, v143, v98, vcc
	v_mul_f32_e32 v98, 0xbfb8aa3b, v97
	v_rndne_f32_e32 v99, v98
	v_sub_f32_e32 v101, v98, v99
	v_fma_f32 v98, v97, s78, -v98
	v_fmac_f32_e32 v98, 0xb2a5705f, v97
	v_add_f32_e32 v98, v101, v98
	v_exp_f32_e32 v98, v98
	v_cvt_i32_f32_e32 v99, v99
	v_cmp_nlt_f32_e32 vcc, s79, v97
	v_ldexp_f32 v98, v98, v99
	s_nop 0
	v_cndmask_b32_e32 v98, 0, v98, vcc
	v_cmp_ngt_f32_e32 vcc, s80, v97
	s_nop 1
	v_cndmask_b32_e32 v97, v143, v98, vcc
	v_mul_f32_e32 v98, 0xbfb8aa3b, v92
	v_rndne_f32_e32 v99, v98
	v_sub_f32_e32 v101, v98, v99
	v_fma_f32 v98, v92, s78, -v98
	v_fmac_f32_e32 v98, 0xb2a5705f, v92
	v_add_f32_e32 v98, v101, v98
	v_exp_f32_e32 v98, v98
	v_cvt_i32_f32_e32 v99, v99
	v_cmp_nlt_f32_e32 vcc, s79, v92
	v_pk_add_f32 v[96:97], v[96:97], 1.0 op_sel_hi:[1,0]
	v_ldexp_f32 v98, v98, v99
	v_cndmask_b32_e32 v98, 0, v98, vcc
	v_cmp_ngt_f32_e32 vcc, s80, v92
	s_nop 1
	v_cndmask_b32_e32 v92, v143, v98, vcc
	v_mul_f32_e32 v98, 0xbfb8aa3b, v93
	v_rndne_f32_e32 v99, v98
	v_sub_f32_e32 v101, v98, v99
	v_fma_f32 v98, v93, s78, -v98
	v_fmac_f32_e32 v98, 0xb2a5705f, v93
	v_add_f32_e32 v98, v101, v98
	v_exp_f32_e32 v98, v98
	v_cvt_i32_f32_e32 v99, v99
	v_cmp_nlt_f32_e32 vcc, s79, v93
	v_ldexp_f32 v98, v98, v99
	s_nop 0
	v_cndmask_b32_e32 v98, 0, v98, vcc
	v_cmp_ngt_f32_e32 vcc, s80, v93
	s_nop 1
	v_cndmask_b32_e32 v93, v143, v98, vcc
	v_div_scale_f32 v98, s[40:41], v94, v94, 1.0
	v_rcp_f32_e32 v99, v98
	v_pk_add_f32 v[92:93], v[92:93], 1.0 op_sel_hi:[1,0]
	v_fma_f32 v101, -v98, v99, 1.0
	v_fmac_f32_e32 v99, v101, v99
	v_div_scale_f32 v101, vcc, 1.0, v94, 1.0
	v_mul_f32_e32 v102, v101, v99
	v_fma_f32 v103, -v98, v102, v101
	v_fmac_f32_e32 v102, v103, v99
	v_fma_f32 v98, -v98, v102, v101
	v_div_fmas_f32 v98, v98, v99, v102
	v_div_fixup_f32 v94, v98, v94, 1.0
	v_rcp_f32_e32 v95, v95
	s_nop 3
	v_rcp_f32_e32 v90, v90
	s_nop 3
	v_rcp_f32_e32 v91, v91
	s_nop 3
	v_rcp_f32_e32 v96, v96
	s_nop 3
	v_rcp_f32_e32 v97, v97
	s_nop 3
	v_rcp_f32_e32 v92, v92
	s_nop 3
	v_div_scale_f32 v98, s[40:41], v93, v93, 1.0
	v_rcp_f32_e32 v99, v98
	s_nop 0
	v_fma_f32 v101, -v98, v99, 1.0
	v_fmac_f32_e32 v99, v101, v99
	v_div_scale_f32 v101, vcc, 1.0, v93, 1.0
	v_mul_f32_e32 v102, v101, v99
	v_fma_f32 v103, -v98, v102, v101
	v_fmac_f32_e32 v102, v103, v99
	v_fma_f32 v98, -v98, v102, v101
	v_div_fmas_f32 v98, v98, v99, v102
	v_div_fixup_f32 v93, v98, v93, 1.0

.LBB0_735:
	v_add_u32_e32 v130, v120, v147
	v_lshlrev_b64 v[90:91], 2, v[130:131]
	v_lshl_add_u64 v[98:99], s[22:23], 0, v[90:91]
	global_load_dwordx4 v[92:95], v[98:99], off offset:16
	s_nop 0
	global_load_dwordx4 v[98:101], v[98:99], off
	v_lshl_add_u64 v[90:91], s[28:29], 0, v[90:91]
	global_load_dwordx4 v[102:105], v[90:91], off offset:16
	global_load_dwordx4 v[106:109], v[90:91], off
	v_lshlrev_b32_e32 v90, 16, v26
	v_and_b32_e32 v91, 0xffff0000, v26
	v_lshlrev_b32_e32 v110, 16, v86
	v_and_b32_e32 v111, 0xffff0000, v86
	v_lshlrev_b32_e32 v112, 16, v70
	v_and_b32_e32 v113, 0xffff0000, v70
	v_pk_add_f32 v[110:111], v[110:111], v[90:91] neg_lo:[0,1] neg_hi:[0,1]
	v_lshlrev_b32_e32 v86, 16, v87
	v_and_b32_e32 v87, 0xffff0000, v87
	v_lshrrev_b32_e32 v96, 2, v148
	v_cmp_lt_u32_e32 vcc, s71, v130
	s_waitcnt vmcnt(2)
	v_pk_fma_f32 v[98:99], v[110:111], v[98:99], v[90:91]
	v_pk_add_f32 v[90:91], v[112:113], v[90:91] neg_lo:[0,1] neg_hi:[0,1]
	s_waitcnt vmcnt(0)
	v_pk_fma_f32 v[90:91], v[90:91], v[106:107], v[98:99]
	v_lshlrev_b32_e32 v98, 16, v27
	v_and_b32_e32 v99, 0xffff0000, v27
	v_lshlrev_b32_e32 v106, 16, v71
	v_and_b32_e32 v107, 0xffff0000, v71
	v_pk_add_f32 v[86:87], v[86:87], v[98:99] neg_lo:[0,1] neg_hi:[0,1]
	s_nop 0
	v_pk_fma_f32 v[86:87], v[86:87], v[100:101], v[98:99]
	v_pk_add_f32 v[98:99], v[106:107], v[98:99] neg_lo:[0,1] neg_hi:[0,1]
	v_lshlrev_b32_e32 v100, 16, v88
	v_pk_fma_f32 v[86:87], v[98:99], v[108:109], v[86:87]
	v_lshlrev_b32_e32 v98, 16, v28
	v_and_b32_e32 v99, 0xffff0000, v28
	v_and_b32_e32 v101, 0xffff0000, v88
	v_lshlrev_b32_e32 v106, 16, v72
	v_and_b32_e32 v107, 0xffff0000, v72
	v_pk_add_f32 v[100:101], v[100:101], v[98:99] neg_lo:[0,1] neg_hi:[0,1]
	v_lshlrev_b32_e32 v88, 16, v89
	v_pk_fma_f32 v[92:93], v[100:101], v[92:93], v[98:99]
	v_pk_add_f32 v[98:99], v[106:107], v[98:99] neg_lo:[0,1] neg_hi:[0,1]
	v_and_b32_e32 v89, 0xffff0000, v89
	v_pk_fma_f32 v[92:93], v[98:99], v[102:103], v[92:93]
	v_lshlrev_b32_e32 v98, 16, v29
	v_and_b32_e32 v99, 0xffff0000, v29
	v_lshlrev_b32_e32 v100, 16, v73
	v_and_b32_e32 v101, 0xffff0000, v73
	v_pk_add_f32 v[88:89], v[88:89], v[98:99] neg_lo:[0,1] neg_hi:[0,1]
	s_nop 0
	v_pk_fma_f32 v[88:89], v[88:89], v[94:95], v[98:99]
	v_pk_add_f32 v[94:95], v[100:101], v[98:99] neg_lo:[0,1] neg_hi:[0,1]
	s_nop 0
	v_pk_fma_f32 v[88:89], v[94:95], v[104:105], v[88:89]
	s_and_saveexec_b64 s[4:5], vcc
	s_xor_b64 s[4:5], exec, s[4:5]
	s_cbranch_execz .LBB0_783
	v_cmp_lt_u32_e32 vcc, s72, v130
	s_and_saveexec_b64 s[10:11], vcc
	s_xor_b64 s[10:11], exec, s[10:11]
	s_cbranch_execz .LBB0_780
	v_cmp_lt_u32_e32 vcc, s73, v130
	s_and_saveexec_b64 s[12:13], vcc
	s_xor_b64 s[12:13], exec, s[12:13]
	s_cbranch_execz .LBB0_777
	v_cmp_lt_u32_e32 vcc, s76, v130
	s_and_saveexec_b64 s[14:15], vcc
	s_xor_b64 s[14:15], exec, s[14:15]
	s_cbranch_execz .LBB0_742
	v_cmp_lt_u32_e32 vcc, s77, v130
	s_and_saveexec_b64 s[16:17], vcc
	s_cbranch_execz .LBB0_741
	v_mul_f32_e32 v94, 0xbfb8aa3b, v90
	v_rndne_f32_e32 v95, v94
	v_sub_f32_e32 v97, v94, v95
	v_fma_f32 v94, v90, s78, -v94
	v_fmac_f32_e32 v94, 0xb2a5705f, v90
	v_add_f32_e32 v94, v97, v94
	v_exp_f32_e32 v94, v94
	v_cvt_i32_f32_e32 v95, v95
	v_cmp_nlt_f32_e32 vcc, s79, v90
	v_ldexp_f32 v94, v94, v95
	s_nop 0
	v_cndmask_b32_e32 v94, 0, v94, vcc
	v_cmp_ngt_f32_e32 vcc, s80, v90
	s_nop 1
	v_cndmask_b32_e32 v90, v143, v94, vcc
	v_mul_f32_e32 v94, 0xbfb8aa3b, v91
	v_rndne_f32_e32 v95, v94
	v_sub_f32_e32 v97, v94, v95
	v_fma_f32 v94, v91, s78, -v94
	v_fmac_f32_e32 v94, 0xb2a5705f, v91
	v_add_f32_e32 v94, v97, v94
	v_exp_f32_e32 v94, v94
	v_cvt_i32_f32_e32 v95, v95
	v_cmp_nlt_f32_e32 vcc, s79, v91
	v_ldexp_f32 v94, v94, v95
	s_nop 0
	v_cndmask_b32_e32 v94, 0, v94, vcc
	v_cmp_ngt_f32_e32 vcc, s80, v91
	s_nop 1
	v_cndmask_b32_e32 v91, v143, v94, vcc
	v_mul_f32_e32 v94, 0xbfb8aa3b, v86
	v_rndne_f32_e32 v95, v94
	v_sub_f32_e32 v97, v94, v95
	v_fma_f32 v94, v86, s78, -v94
	v_fmac_f32_e32 v94, 0xb2a5705f, v86
	v_add_f32_e32 v94, v97, v94
	v_exp_f32_e32 v94, v94
	v_cvt_i32_f32_e32 v95, v95
	v_cmp_nlt_f32_e32 vcc, s79, v86
	v_pk_add_f32 v[90:91], v[90:91], 1.0 op_sel_hi:[1,0]
	v_ldexp_f32 v94, v94, v95
	v_cndmask_b32_e32 v94, 0, v94, vcc
	v_cmp_ngt_f32_e32 vcc, s80, v86
	s_nop 1
	v_cndmask_b32_e32 v86, v143, v94, vcc
	v_mul_f32_e32 v94, 0xbfb8aa3b, v87
	v_rndne_f32_e32 v95, v94
	v_sub_f32_e32 v97, v94, v95
	v_fma_f32 v94, v87, s78, -v94
	v_fmac_f32_e32 v94, 0xb2a5705f, v87
	v_add_f32_e32 v94, v97, v94
	v_exp_f32_e32 v94, v94
	v_cvt_i32_f32_e32 v95, v95
	v_cmp_nlt_f32_e32 vcc, s79, v87
	v_ldexp_f32 v94, v94, v95
	s_nop 0
	v_cndmask_b32_e32 v94, 0, v94, vcc
	v_cmp_ngt_f32_e32 vcc, s80, v87
	s_nop 1
	v_cndmask_b32_e32 v87, v143, v94, vcc
	v_mul_f32_e32 v94, 0xbfb8aa3b, v92
	v_rndne_f32_e32 v95, v94
	v_sub_f32_e32 v97, v94, v95
	v_fma_f32 v94, v92, s78, -v94
	v_fmac_f32_e32 v94, 0xb2a5705f, v92
	v_add_f32_e32 v94, v97, v94
	v_exp_f32_e32 v94, v94
	v_cvt_i32_f32_e32 v95, v95
	v_cmp_nlt_f32_e32 vcc, s79, v92
	v_pk_add_f32 v[86:87], v[86:87], 1.0 op_sel_hi:[1,0]
	v_ldexp_f32 v94, v94, v95
	v_cndmask_b32_e32 v94, 0, v94, vcc
	v_cmp_ngt_f32_e32 vcc, s80, v92
	s_nop 1
	v_cndmask_b32_e32 v92, v143, v94, vcc
	v_mul_f32_e32 v94, 0xbfb8aa3b, v93
	v_rndne_f32_e32 v95, v94
	v_sub_f32_e32 v97, v94, v95
	v_fma_f32 v94, v93, s78, -v94
	v_fmac_f32_e32 v94, 0xb2a5705f, v93
	v_add_f32_e32 v94, v97, v94
	v_exp_f32_e32 v94, v94
	v_cvt_i32_f32_e32 v95, v95
	v_cmp_nlt_f32_e32 vcc, s79, v93
	v_ldexp_f32 v94, v94, v95
	s_nop 0
	v_cndmask_b32_e32 v94, 0, v94, vcc
	v_cmp_ngt_f32_e32 vcc, s80, v93
	s_nop 1
	v_cndmask_b32_e32 v93, v143, v94, vcc
	v_mul_f32_e32 v94, 0xbfb8aa3b, v88
	v_rndne_f32_e32 v95, v94
	v_sub_f32_e32 v97, v94, v95
	v_fma_f32 v94, v88, s78, -v94
	v_fmac_f32_e32 v94, 0xb2a5705f, v88
	v_add_f32_e32 v94, v97, v94
	v_exp_f32_e32 v94, v94
	v_cvt_i32_f32_e32 v95, v95
	v_cmp_nlt_f32_e32 vcc, s79, v88
	v_pk_add_f32 v[92:93], v[92:93], 1.0 op_sel_hi:[1,0]
	v_ldexp_f32 v94, v94, v95
	v_cndmask_b32_e32 v94, 0, v94, vcc
	v_cmp_ngt_f32_e32 vcc, s80, v88
	s_nop 1
	v_cndmask_b32_e32 v88, v143, v94, vcc
	v_mul_f32_e32 v94, 0xbfb8aa3b, v89
	v_rndne_f32_e32 v95, v94
	v_sub_f32_e32 v97, v94, v95
	v_fma_f32 v94, v89, s78, -v94
	v_fmac_f32_e32 v94, 0xb2a5705f, v89
	v_add_f32_e32 v94, v97, v94
	v_exp_f32_e32 v94, v94
	v_cvt_i32_f32_e32 v95, v95
	v_cmp_nlt_f32_e32 vcc, s79, v89
	v_ldexp_f32 v94, v94, v95
	s_nop 0
	v_cndmask_b32_e32 v94, 0, v94, vcc
	v_cmp_ngt_f32_e32 vcc, s80, v89
	s_nop 1
	v_cndmask_b32_e32 v89, v143, v94, vcc
	v_div_scale_f32 v94, s[18:19], v90, v90, 1.0
	v_rcp_f32_e32 v95, v94
	v_pk_add_f32 v[88:89], v[88:89], 1.0 op_sel_hi:[1,0]
	v_fma_f32 v97, -v94, v95, 1.0
	v_fmac_f32_e32 v95, v97, v95
	v_div_scale_f32 v97, vcc, 1.0, v90, 1.0
	v_mul_f32_e32 v98, v97, v95
	v_fma_f32 v99, -v94, v98, v97
	v_fmac_f32_e32 v98, v99, v95
	v_fma_f32 v94, -v94, v98, v97
	v_div_fmas_f32 v94, v94, v95, v98
	v_div_fixup_f32 v90, v94, v90, 1.0
	v_rcp_f32_e32 v91, v91
	s_nop 3
	v_rcp_f32_e32 v86, v86
	s_nop 3
	v_rcp_f32_e32 v87, v87
	s_nop 3
	v_rcp_f32_e32 v92, v92
	s_nop 3
	v_rcp_f32_e32 v93, v93
	s_nop 3
	v_rcp_f32_e32 v88, v88
	s_nop 3
	v_div_scale_f32 v94, s[18:19], v89, v89, 1.0
	v_rcp_f32_e32 v95, v94
	s_nop 0
	v_fma_f32 v97, -v94, v95, 1.0
	v_fmac_f32_e32 v95, v97, v95
	v_div_scale_f32 v97, vcc, 1.0, v89, 1.0
	v_mul_f32_e32 v98, v97, v95
	v_fma_f32 v99, -v94, v98, v97
	v_fmac_f32_e32 v98, v99, v95
	v_fma_f32 v94, -v94, v98, v97
	v_div_fmas_f32 v94, v94, v95, v98
	v_div_fixup_f32 v89, v94, v89, 1.0

.LBB0_1275:
	ds_read_b128 v[30:33], v183
	ds_read_b128 v[26:29], v183 offset:64
	ds_read_b128 v[34:37], v184 offset:18432
	ds_read_b128 v[38:41], v184 offset:18496
	s_lshl_b32 s0, s87, 5
	s_sub_i32 s2, s82, s0
	s_lshr_b32 s0, s86, 24
	s_waitcnt lgkmcnt(1)
	v_mfma_f32_16x16x32_bf16 v[34:37], v[34:37], v[30:33], 0
	s_add_i32 s0, s82, s0
	s_ashr_i32 s0, s0, 8
	s_ashr_i32 s1, s0, 31
	s_waitcnt lgkmcnt(0)
	v_mfma_f32_16x16x32_bf16 v[54:57], v[38:41], v[26:29], v[34:37]
	ds_read_b128 v[38:41], v184 offset:20800
	s_ashr_i32 s3, s2, 31
	s_nop 0
	ds_read_b128 v[34:37], v184 offset:20736
	s_lshl_b64 s[0:1], s[0:1], 12
	s_lshl_b64 s[86:87], s[2:3], 7
	s_add_u32 s0, s0, s86
	s_addc_u32 s1, s1, s87
	s_waitcnt lgkmcnt(0)
	v_mfma_f32_16x16x32_bf16 v[34:37], v[34:37], v[30:33], 0
	s_lshl_b32 s82, s97, 7
	ds_read_b128 v[58:61], v184 offset:34624
	v_mfma_f32_16x16x32_bf16 v[62:65], v[38:41], v[26:29], v[34:37]
	ds_read_b128 v[38:41], v184 offset:23104
	s_nop 3
	ds_read_b128 v[34:37], v184 offset:23040
	s_waitcnt lgkmcnt(0)
	v_mfma_f32_16x16x32_bf16 v[34:37], v[34:37], v[30:33], 0
	v_mfma_f32_16x16x32_bf16 v[66:69], v[38:41], v[26:29], v[34:37]
	ds_read_b128 v[38:41], v184 offset:25408
	s_nop 5
	ds_read_b128 v[34:37], v184 offset:25344
	s_waitcnt lgkmcnt(0)
	v_mfma_f32_16x16x32_bf16 v[34:37], v[34:37], v[30:33], 0
	v_mfma_f32_16x16x32_bf16 v[50:53], v[38:41], v[26:29], v[34:37]
	ds_read_b128 v[38:41], v184 offset:27712
	s_nop 5
	ds_read_b128 v[34:37], v184 offset:27648
	s_waitcnt lgkmcnt(0)
	v_mfma_f32_16x16x32_bf16 v[34:37], v[34:37], v[30:33], 0
	v_mfma_f32_16x16x32_bf16 v[46:49], v[38:41], v[26:29], v[34:37]
	ds_read_b128 v[38:41], v184 offset:30016
	s_nop 5
	ds_read_b128 v[34:37], v184 offset:29952
	s_waitcnt lgkmcnt(0)
	v_mfma_f32_16x16x32_bf16 v[34:37], v[34:37], v[30:33], 0
	v_mfma_f32_16x16x32_bf16 v[42:45], v[38:41], v[26:29], v[34:37]
	ds_read_b128 v[38:41], v184 offset:32320
	s_nop 5
	ds_read_b128 v[34:37], v184 offset:32256
	s_waitcnt lgkmcnt(0)
	v_mfma_f32_16x16x32_bf16 v[34:37], v[34:37], v[30:33], 0
	v_mfma_f32_16x16x32_bf16 v[38:41], v[38:41], v[26:29], v[34:37]
	s_nop 6
	ds_read_b128 v[34:37], v184 offset:34560
	s_waitcnt lgkmcnt(0)
	v_mfma_f32_16x16x32_bf16 v[34:37], v[34:37], v[30:33], 0
	v_mfma_f32_16x16x32_bf16 v[34:37], v[58:61], v[26:29], v[34:37]
	v_mul_f32_e32 v58, v107, v89
	v_mul_f32_e32 v59, v108, v87
	v_cndmask_b32_e64 v58, v59, v58, s[8:9]
	v_mul_f32_e32 v59, v107, v91
	v_mul_f32_e32 v60, v108, v93
	v_cndmask_b32_e64 v59, v59, v60, s[10:11]
	v_mul_f32_e32 v58, 0x3fb8aa3b, v58
	v_mul_f32_e32 v59, 0x3fb8aa3b, v59
	v_exp_f32_e32 v58, v58
	v_exp_f32_e32 v59, v59
	v_mul_f32_e32 v60, v108, v120
	v_pk_mul_f32 v[58:59], v[58:59], v[54:55]
	v_mul_f32_e32 v54, v107, v119
	v_mul_f32_e32 v55, v108, v118
	v_cndmask_b32_e64 v54, v55, v54, s[12:13]
	v_mul_f32_e32 v55, v107, v121
	v_cndmask_b32_e64 v55, v60, v55, s[14:15]
	v_mul_f32_e32 v54, 0x3fb8aa3b, v54
	v_mul_f32_e32 v55, 0x3fb8aa3b, v55
	v_exp_f32_e32 v54, v54
	v_exp_f32_e32 v55, v55
	v_cvt_pk_bf16_f32 v58, v58, v59
	v_pk_mul_f32 v[60:61], v[54:55], v[56:57]
	v_mul_f32_e32 v54, v107, v123
	v_mul_f32_e32 v55, v108, v122
	v_cndmask_b32_e64 v54, v55, v54, s[16:17]
	v_mul_f32_e32 v55, v107, v125
	v_mul_f32_e32 v56, v108, v124
	v_cndmask_b32_e64 v55, v56, v55, s[18:19]
	v_mul_f32_e32 v54, 0x3fb8aa3b, v54
	v_mul_f32_e32 v55, 0x3fb8aa3b, v55
	v_exp_f32_e32 v54, v54
	v_exp_f32_e32 v55, v55
	v_mul_f32_e32 v56, v108, v128
	v_mul_f32_e32 v57, v108, v134
	v_cvt_pk_bf16_f32 v59, v60, v61
	v_pk_mul_f32 v[62:63], v[54:55], v[62:63]
	v_mul_f32_e32 v54, v107, v127
	v_mul_f32_e32 v55, v108, v126
	v_cndmask_b32_e64 v54, v55, v54, s[20:21]
	v_mul_f32_e32 v55, v107, v129
	v_cndmask_b32_e64 v55, v56, v55, s[22:23]
	v_mul_f32_e32 v54, 0x3fb8aa3b, v54
	v_mul_f32_e32 v55, 0x3fb8aa3b, v55
	v_exp_f32_e32 v54, v54
	v_exp_f32_e32 v55, v55
	v_mul_f32_e32 v56, v108, v132
	v_cvt_pk_bf16_f32 v60, v62, v63
	v_pk_mul_f32 v[64:65], v[54:55], v[64:65]
	v_mul_f32_e32 v54, v107, v131
	v_mul_f32_e32 v55, v108, v130
	v_cndmask_b32_e64 v54, v55, v54, s[24:25]
	v_mul_f32_e32 v55, v107, v133
	v_cndmask_b32_e64 v55, v56, v55, s[26:27]
	v_mul_f32_e32 v54, 0x3fb8aa3b, v54
	v_mul_f32_e32 v55, 0x3fb8aa3b, v55
	v_exp_f32_e32 v54, v54
	v_exp_f32_e32 v55, v55
	v_mul_f32_e32 v56, v107, v135
	v_cndmask_b32_e64 v56, v57, v56, s[28:29]
	v_mul_f32_e32 v57, v107, v137
	v_pk_mul_f32 v[54:55], v[54:55], v[66:67]
	v_mul_f32_e32 v66, v108, v136
	v_cndmask_b32_e64 v57, v66, v57, s[30:31]
	v_mul_f32_e32 v56, 0x3fb8aa3b, v56
	v_mul_f32_e32 v57, 0x3fb8aa3b, v57
	v_exp_f32_e32 v56, v56
	v_exp_f32_e32 v57, v57
	v_mul_f32_e32 v66, v107, v139
	v_mul_f32_e32 v67, v108, v138
	v_cndmask_b32_e64 v66, v67, v66, s[34:35]
	v_pk_mul_f32 v[56:57], v[56:57], v[68:69]
	v_mul_f32_e32 v67, v107, v141
	v_mul_f32_e32 v68, v108, v140
	v_cndmask_b32_e64 v67, v68, v67, s[36:37]
	v_mul_f32_e32 v66, 0x3fb8aa3b, v66
	v_mul_f32_e32 v67, 0x3fb8aa3b, v67
	v_exp_f32_e32 v66, v66
	v_exp_f32_e32 v67, v67
	v_mul_f32_e32 v68, v108, v144
	v_cvt_pk_bf16_f32 v61, v64, v65
	v_cvt_pk_bf16_f32 v54, v54, v55
	v_pk_mul_f32 v[50:51], v[66:67], v[50:51]
	v_mul_f32_e32 v66, v107, v143
	v_mul_f32_e32 v67, v108, v142
	v_cndmask_b32_e64 v66, v67, v66, s[38:39]
	v_mul_f32_e32 v67, v107, v145
	v_cndmask_b32_e64 v67, v68, v67, s[40:41]
	v_mul_f32_e32 v66, 0x3fb8aa3b, v66
	v_mul_f32_e32 v67, 0x3fb8aa3b, v67
	v_exp_f32_e32 v66, v66
	v_exp_f32_e32 v67, v67
	v_mul_f32_e32 v68, v108, v148
	v_cvt_pk_bf16_f32 v55, v56, v57
	v_cvt_pk_bf16_f32 v56, v50, v51
	v_pk_mul_f32 v[52:53], v[66:67], v[52:53]
	v_mul_f32_e32 v66, v107, v147
	v_mul_f32_e32 v67, v108, v146
	v_cndmask_b32_e64 v66, v67, v66, s[42:43]
	v_mul_f32_e32 v67, v107, v149
	v_cndmask_b32_e64 v67, v68, v67, s[44:45]
	v_mul_f32_e32 v66, 0x3fb8aa3b, v66
	v_mul_f32_e32 v67, 0x3fb8aa3b, v67
	v_exp_f32_e32 v66, v66
	v_exp_f32_e32 v67, v67
	v_mul_f32_e32 v68, v108, v152
	v_cvt_pk_bf16_f32 v57, v52, v53
	v_pk_mul_f32 v[46:47], v[66:67], v[46:47]
	v_mul_f32_e32 v66, v107, v151
	v_mul_f32_e32 v67, v108, v150
	v_cndmask_b32_e64 v66, v67, v66, s[46:47]
	v_mul_f32_e32 v67, v107, v153
	v_cndmask_b32_e64 v67, v68, v67, s[48:49]
	v_mul_f32_e32 v66, 0x3fb8aa3b, v66
	v_mul_f32_e32 v67, 0x3fb8aa3b, v67
	v_exp_f32_e32 v66, v66
	v_exp_f32_e32 v67, v67
	v_mul_f32_e32 v68, v108, v156
	v_cvt_pk_bf16_f32 v46, v46, v47
	v_pk_mul_f32 v[48:49], v[66:67], v[48:49]
	v_mul_f32_e32 v66, v107, v155
	v_mul_f32_e32 v67, v108, v154
	v_cndmask_b32_e64 v66, v67, v66, s[50:51]
	v_mul_f32_e32 v67, v107, v157
	v_cndmask_b32_e64 v67, v68, v67, s[52:53]
	v_mul_f32_e32 v66, 0x3fb8aa3b, v66
	v_mul_f32_e32 v67, 0x3fb8aa3b, v67
	v_exp_f32_e32 v66, v66
	v_exp_f32_e32 v67, v67
	v_mul_f32_e32 v68, v108, v160
	v_cvt_pk_bf16_f32 v47, v48, v49
	v_pk_mul_f32 v[42:43], v[66:67], v[42:43]
	v_mul_f32_e32 v66, v107, v159
	v_mul_f32_e32 v67, v108, v158
	v_cndmask_b32_e64 v66, v67, v66, s[54:55]
	v_mul_f32_e32 v67, v107, v161
	v_cndmask_b32_e64 v67, v68, v67, s[94:95]
	v_mul_f32_e32 v66, 0x3fb8aa3b, v66
	v_mul_f32_e32 v67, 0x3fb8aa3b, v67
	v_exp_f32_e32 v66, v66
	v_exp_f32_e32 v67, v67
	v_mul_f32_e32 v68, v108, v164
	v_cvt_pk_bf16_f32 v48, v42, v43
	v_pk_mul_f32 v[44:45], v[66:67], v[44:45]
	v_mul_f32_e32 v66, v107, v163
	v_mul_f32_e32 v67, v108, v162
	v_cndmask_b32_e64 v66, v67, v66, s[58:59]
	v_mul_f32_e32 v67, v107, v165
	v_cndmask_b32_e64 v67, v68, v67, s[60:61]
	v_mul_f32_e32 v66, 0x3fb8aa3b, v66
	v_mul_f32_e32 v67, 0x3fb8aa3b, v67
	v_exp_f32_e32 v66, v66
	v_exp_f32_e32 v67, v67
	v_mul_f32_e32 v68, v108, v168
	v_cvt_pk_bf16_f32 v49, v44, v45
	v_pk_mul_f32 v[38:39], v[66:67], v[38:39]
	v_mul_f32_e32 v66, v107, v167
	v_mul_f32_e32 v67, v108, v166
	v_cndmask_b32_e64 v66, v67, v66, s[62:63]
	v_mul_f32_e32 v67, v107, v169
	v_cndmask_b32_e64 v67, v68, v67, s[64:65]
	v_mul_f32_e32 v66, 0x3fb8aa3b, v66
	v_mul_f32_e32 v67, 0x3fb8aa3b, v67
	v_exp_f32_e32 v66, v66
	v_exp_f32_e32 v67, v67
	v_mul_f32_e32 v68, v108, v172
	v_cvt_pk_bf16_f32 v38, v38, v39
	v_pk_mul_f32 v[40:41], v[66:67], v[40:41]
	v_mul_f32_e32 v66, v107, v171
	v_mul_f32_e32 v67, v108, v170
	v_cndmask_b32_e64 v66, v67, v66, s[66:67]
	v_mul_f32_e32 v67, v107, v173
	v_cndmask_b32_e64 v67, v68, v67, s[68:69]
	v_mul_f32_e32 v66, 0x3fb8aa3b, v66
	v_mul_f32_e32 v67, 0x3fb8aa3b, v67
	v_exp_f32_e32 v66, v66
	v_exp_f32_e32 v67, v67
	v_mul_f32_e32 v68, v108, v176
	v_cvt_pk_bf16_f32 v39, v40, v41
	v_pk_mul_f32 v[34:35], v[66:67], v[34:35]
	v_mul_f32_e32 v66, v107, v175
	v_mul_f32_e32 v67, v108, v174
	v_cndmask_b32_e64 v66, v67, v66, s[70:71]
	v_mul_f32_e32 v67, v107, v177
	v_cndmask_b32_e64 v67, v68, v67, s[72:73]
	v_mul_f32_e32 v66, 0x3fb8aa3b, v66
	v_mul_f32_e32 v67, 0x3fb8aa3b, v67
	v_exp_f32_e32 v66, v66
	v_exp_f32_e32 v67, v67
	v_cvt_pk_bf16_f32 v40, v34, v35
	v_pk_mul_f32 v[36:37], v[66:67], v[36:37]
	ds_read_b64_tr_b16 v[64:65], v185 offset:39168
	ds_read_b64_tr_b16 v[62:63], v185 offset:36864
	ds_read_b64_tr_b16 v[66:67], v185 offset:36896
	ds_read_b64_tr_b16 v[68:69], v185 offset:39200
	ds_read_b64_tr_b16 v[110:111], v185 offset:36928
	ds_read_b64_tr_b16 v[112:113], v185 offset:39232
	ds_read_b64_tr_b16 v[192:193], v185 offset:36960
	ds_read_b64_tr_b16 v[194:195], v185 offset:39264
	s_waitcnt lgkmcnt(6)
	v_mfma_f32_16x16x32_bf16 v[62:65], v[62:65], v[58:61], 0
	v_cvt_pk_bf16_f32 v41, v36, v37
	s_waitcnt lgkmcnt(4)
	v_mfma_f32_16x16x32_bf16 v[66:69], v[66:69], v[58:61], 0
	s_waitcnt lgkmcnt(2)
	v_mfma_f32_16x16x32_bf16 v[110:113], v[110:113], v[58:61], 0
	s_waitcnt lgkmcnt(0)
	v_mfma_f32_16x16x32_bf16 v[58:61], v[192:195], v[58:61], 0
	ds_read_b64_tr_b16 v[52:53], v186 offset:39168
	ds_read_b64_tr_b16 v[50:51], v186 offset:36864
	ds_read_b64_tr_b16 v[192:193], v186 offset:36896
	ds_read_b64_tr_b16 v[194:195], v186 offset:39200
	s_waitcnt lgkmcnt(2)
	v_mfma_f32_16x16x32_bf16 v[50:53], v[50:53], v[54:57], v[62:65]
	s_waitcnt lgkmcnt(0)
	v_mfma_f32_16x16x32_bf16 v[62:65], v[192:195], v[54:57], v[66:69]
	s_nop 2
	ds_read_b64_tr_b16 v[66:67], v186 offset:36928
	ds_read_b64_tr_b16 v[68:69], v186 offset:39232
	s_waitcnt lgkmcnt(0)
	v_mfma_f32_16x16x32_bf16 v[66:69], v[66:69], v[54:57], v[110:113]
	s_nop 2
	ds_read_b64_tr_b16 v[110:111], v186 offset:36960
	ds_read_b64_tr_b16 v[112:113], v186 offset:39264
	s_waitcnt lgkmcnt(0)
	v_mfma_f32_16x16x32_bf16 v[54:57], v[110:113], v[54:57], v[58:61]
	ds_read_b64_tr_b16 v[44:45], v187 offset:39168
	ds_read_b64_tr_b16 v[42:43], v187 offset:36864
	s_nop 0
	ds_read_b64_tr_b16 v[58:59], v187 offset:36896
	ds_read_b64_tr_b16 v[60:61], v187 offset:39200
	s_waitcnt lgkmcnt(2)
	v_mfma_f32_16x16x32_bf16 v[42:45], v[42:45], v[46:49], v[50:53]
	s_nop 2
	ds_read_b64_tr_b16 v[50:51], v187 offset:36928
	ds_read_b64_tr_b16 v[52:53], v187 offset:39232
	s_waitcnt lgkmcnt(2)
	v_mfma_f32_16x16x32_bf16 v[58:61], v[58:61], v[46:49], v[62:65]
	s_waitcnt lgkmcnt(0)
	v_mfma_f32_16x16x32_bf16 v[62:65], v[50:53], v[46:49], v[66:69]
	ds_read_b64_tr_b16 v[50:51], v187 offset:36960
	ds_read_b64_tr_b16 v[52:53], v187 offset:39264
	s_waitcnt lgkmcnt(0)
	v_mfma_f32_16x16x32_bf16 v[54:57], v[50:53], v[46:49], v[54:57]
	ds_read_b64_tr_b16 v[36:37], v188 offset:39168
	ds_read_b64_tr_b16 v[34:35], v188 offset:36864
	ds_read_b64_tr_b16 v[46:47], v188 offset:36896
	ds_read_b64_tr_b16 v[48:49], v188 offset:39200
	s_waitcnt lgkmcnt(2)
	v_mfma_f32_16x16x32_bf16 v[50:53], v[34:37], v[38:41], v[42:45]
	s_nop 2
	ds_read_b64_tr_b16 v[42:43], v188 offset:36928
	ds_read_b64_tr_b16 v[44:45], v188 offset:39232
	s_waitcnt lgkmcnt(2)
	v_mfma_f32_16x16x32_bf16 v[34:37], v[46:49], v[38:41], v[58:61]
	s_waitcnt lgkmcnt(0)
	v_mfma_f32_16x16x32_bf16 v[46:49], v[42:45], v[38:41], v[62:65]
	ds_read_b64_tr_b16 v[42:43], v188 offset:36960
	ds_read_b64_tr_b16 v[44:45], v188 offset:39264
	ds_read_b128 v[110:113], v178 offset:59968
	ds_read_b128 v[62:65], v178 offset:57664
	s_waitcnt lgkmcnt(2)
	v_mfma_f32_16x16x32_bf16 v[192:195], v[42:45], v[38:41], v[54:57]
	ds_read_b128 v[38:41], v178 offset:55296
	s_nop 1
	ds_read_b128 v[54:57], v178 offset:55360
	ds_read_b128 v[42:45], v178 offset:64512
	s_waitcnt lgkmcnt(2)
	v_mfma_f32_16x16x32_bf16 v[38:41], v[38:41], v[30:33], 0
	ds_read_b128 v[66:69], v180 offset:64512
	ds_read_b128 v[196:199], v181 offset:64512
	s_waitcnt lgkmcnt(3)
	v_mfma_f32_16x16x32_bf16 v[54:57], v[54:57], v[26:29], v[38:41]
	s_nop 3
	ds_read_b128 v[38:41], v178 offset:64576
	s_waitcnt lgkmcnt(3)
	v_mfma_f32_16x16x32_bf16 v[42:45], v[42:45], v[30:33], 0
	s_waitcnt lgkmcnt(0)
	v_mfma_f32_16x16x32_bf16 v[58:61], v[38:41], v[26:29], v[42:45]
	ds_read_b128 v[38:41], v178 offset:57600
	s_nop 4
	ds_read_b128 v[42:45], v179 offset:64512
	s_waitcnt lgkmcnt(1)
	v_mfma_f32_16x16x32_bf16 v[38:41], v[38:41], v[30:33], 0
	v_mfma_f32_16x16x32_bf16 v[38:41], v[62:65], v[26:29], v[38:41]
	ds_read_b128 v[62:65], v179 offset:64576
	s_waitcnt lgkmcnt(1)
	v_mfma_f32_16x16x32_bf16 v[42:45], v[42:45], v[30:33], 0
	s_waitcnt lgkmcnt(0)
	v_mfma_f32_16x16x32_bf16 v[42:45], v[62:65], v[26:29], v[42:45]
	ds_read_b128 v[62:65], v178 offset:59904
	s_waitcnt lgkmcnt(0)
	v_mfma_f32_16x16x32_bf16 v[62:65], v[62:65], v[30:33], 0
	v_mfma_f32_16x16x32_bf16 v[62:65], v[110:113], v[26:29], v[62:65]
	ds_read_b128 v[110:113], v180 offset:64576
	v_mfma_f32_16x16x32_bf16 v[66:69], v[66:69], v[30:33], 0
	s_waitcnt lgkmcnt(0)
	v_mfma_f32_16x16x32_bf16 v[66:69], v[110:113], v[26:29], v[66:69]
	ds_read_b128 v[110:113], v178 offset:62208
	s_waitcnt lgkmcnt(0)
	v_mfma_f32_16x16x32_bf16 v[110:113], v[110:113], v[30:33], 0
	v_mfma_f32_16x16x32_bf16 v[30:33], v[196:199], v[30:33], 0
	ds_read_b128 v[196:199], v178 offset:62272
	s_waitcnt lgkmcnt(0)
	v_mfma_f32_16x16x32_bf16 v[196:199], v[196:199], v[26:29], v[110:113]
	s_nop 3
	ds_read_b128 v[110:113], v181 offset:64576
	s_waitcnt lgkmcnt(0)
	v_mfma_f32_16x16x32_bf16 v[26:29], v[110:113], v[26:29], v[30:33]
	s_nop 2
	v_mul_f32_e32 v30, v108, v1
	v_mul_f32_e32 v30, 0x3fb8aa3b, v30
	v_exp_f32_e32 v110, v30
	v_mul_f32_e32 v30, v107, v71
	v_mul_f32_e32 v30, 0x3fb8aa3b, v30
	v_exp_f32_e32 v112, v30
	s_nop 0
	v_pk_mul_f32 v[26:27], v[112:113], v[26:27] op_sel_hi:[0,1]
	v_pk_fma_f32 v[26:27], v[110:111], v[196:197], v[26:27] op_sel_hi:[0,1,1]
	v_pk_add_f32 v[32:33], v[192:193], v[26:27]
	v_pk_mul_f32 v[26:27], v[112:113], v[28:29] op_sel_hi:[0,1]
	v_pk_fma_f32 v[26:27], v[110:111], v[198:199], v[26:27] op_sel_hi:[0,1,1]
	v_pk_add_f32 v[108:109], v[194:195], v[26:27]
	v_lshl_add_u64 v[26:27], s[0:1], 0, v[82:83]
	v_mov_b64_e32 v[28:29], s[80:81]
	v_mad_u64_u32 v[28:29], s[0:1], v26, s90, v[28:29]
	v_pk_mul_f32 v[30:31], v[112:113], v[66:67] op_sel_hi:[0,1]
	v_mad_i32_i24 v29, v27, s90, v29
	v_lshlrev_b64 v[26:27], 12, v[26:27]
	v_pk_fma_f32 v[30:31], v[110:111], v[62:63], v[30:31] op_sel_hi:[0,1,1]
	v_lshl_add_u64 v[28:29], v[28:29], 0, s[82:83]
	v_lshl_add_u64 v[26:27], s[92:93], 0, v[26:27]
	v_pk_add_f32 v[66:67], v[46:47], v[30:31]
	v_lshl_add_u64 v[46:47], v[28:29], 0, v[72:73]
	v_lshl_add_u64 v[26:27], v[26:27], 0, s[82:83]
	s_lshl_b32 s82, s97, 8
	v_lshl_add_u64 v[30:31], v[26:27], 0, v[72:73]
	v_lshl_add_u64 v[62:63], v[84:85], 0, s[82:83]
	global_load_dwordx2 v[114:115], v[46:47], off offset:3072
	global_load_dwordx4 v[26:29], v[62:63], off
	v_pk_mul_f32 v[60:61], v[112:113], v[60:61] op_sel_hi:[0,1]
	v_pk_fma_f32 v[56:57], v[110:111], v[56:57], v[60:61] op_sel_hi:[0,1,1]
	v_pk_add_f32 v[52:53], v[52:53], v[56:57]
	v_pk_mul_f32 v[56:57], v[112:113], v[58:59] op_sel_hi:[0,1]
	v_pk_fma_f32 v[54:55], v[110:111], v[54:55], v[56:57] op_sel_hi:[0,1,1]
	v_pk_add_f32 v[54:55], v[50:51], v[54:55]
	v_pk_mul_f32 v[44:45], v[112:113], v[44:45] op_sel_hi:[0,1]
	v_add_f32_e32 v50, 0, v54
	v_add_f32_e32 v56, v55, v50
	v_add_f32_e32 v56, v52, v56
	s_mov_b32 s82, s96
	s_waitcnt vmcnt(1)
	v_lshlrev_b32_e32 v57, 16, v114
	v_mul_f32_e32 v50, 0xbfb8aa3b, v57
	v_fma_f32 v51, v57, s91, -v50
	v_rndne_f32_e32 v59, v50
	v_fmac_f32_e32 v51, 0xb2a5705f, v57
	v_sub_f32_e32 v50, v50, v59
	v_add_f32_e32 v50, v50, v51
	v_exp_f32_e32 v50, v50
	v_cvt_i32_f32_e32 v51, v59
	v_and_b32_e32 v58, 0xffff0000, v114
	v_cmp_nlt_f32_e32 vcc, s89, v57
	v_lshlrev_b32_e32 v60, 16, v115
	v_ldexp_f32 v50, v50, v51
	v_mul_f32_e32 v51, 0xbfb8aa3b, v58
	v_fma_f32 v59, v58, s91, -v51
	v_rndne_f32_e32 v103, v51
	v_fmac_f32_e32 v59, 0xb2a5705f, v58
	v_sub_f32_e32 v51, v51, v103
	v_add_f32_e32 v51, v51, v59
	v_exp_f32_e32 v51, v51
	v_cvt_i32_f32_e32 v59, v103
	v_cndmask_b32_e32 v50, 0, v50, vcc
	v_cmp_ngt_f32_e32 vcc, s88, v57
	v_and_b32_e32 v61, 0xffff0000, v115
	v_ldexp_f32 v51, v51, v59
	v_cndmask_b32_e32 v50, v191, v50, vcc
	v_cmp_nlt_f32_e32 vcc, s89, v58
	s_nop 1
	v_cndmask_b32_e32 v51, 0, v51, vcc
	v_cmp_ngt_f32_e32 vcc, s88, v58
	s_nop 1
	v_cndmask_b32_e32 v51, v191, v51, vcc
	v_pk_add_f32 v[50:51], v[50:51], 1.0 op_sel_hi:[1,0]
	s_nop 0
	v_rcp_f32_e32 v59, v51
	s_nop 3
	v_mul_f32_e32 v51, v58, v59
	s_nop 1
	v_div_scale_f32 v58, s[0:1], v50, v50, v57
	v_rcp_f32_e32 v59, v58
	v_pk_fma_f32 v[40:41], v[110:111], v[40:41], v[44:45] op_sel_hi:[0,1,1]
	v_pk_add_f32 v[36:37], v[36:37], v[40:41]
	v_pk_mul_f32 v[40:41], v[112:113], v[42:43] op_sel_hi:[0,1]
	v_fma_f32 v103, -v58, v59, 1.0
	v_fmac_f32_e32 v59, v103, v59
	v_div_scale_f32 v103, vcc, v57, v50, v57
	v_mul_f32_e32 v105, v103, v59
	v_fma_f32 v107, -v58, v105, v103
	v_fmac_f32_e32 v105, v107, v59
	v_fma_f32 v58, -v58, v105, v103
	v_div_fmas_f32 v58, v58, v59, v105
	v_div_fixup_f32 v50, v58, v50, v57
	v_add_f32_e32 v58, v53, v56
	v_pk_mul_f32 v[56:57], v[112:113], v[68:69] op_sel_hi:[0,1]
	v_pk_fma_f32 v[56:57], v[110:111], v[64:65], v[56:57] op_sel_hi:[0,1,1]
	v_pk_add_f32 v[56:57], v[48:49], v[56:57]
	v_mul_f32_e32 v48, 0xbfb8aa3b, v60
	v_fma_f32 v49, v60, s91, -v48
	v_rndne_f32_e32 v59, v48
	v_fmac_f32_e32 v49, 0xb2a5705f, v60
	v_sub_f32_e32 v48, v48, v59
	v_add_f32_e32 v48, v48, v49
	v_exp_f32_e32 v48, v48
	v_cvt_i32_f32_e32 v49, v59
	v_cmp_nlt_f32_e32 vcc, s89, v60
	v_pk_fma_f32 v[38:39], v[110:111], v[38:39], v[40:41] op_sel_hi:[0,1,1]
	v_pk_add_f32 v[34:35], v[34:35], v[38:39]
	v_ldexp_f32 v48, v48, v49
	v_mul_f32_e32 v49, 0xbfb8aa3b, v61
	v_fma_f32 v59, v61, s91, -v49
	v_rndne_f32_e32 v64, v49
	v_fmac_f32_e32 v59, 0xb2a5705f, v61
	v_sub_f32_e32 v49, v49, v64
	v_add_f32_e32 v49, v49, v59
	v_exp_f32_e32 v49, v49
	v_cvt_i32_f32_e32 v59, v64
	v_cndmask_b32_e32 v48, 0, v48, vcc
	v_cmp_ngt_f32_e32 vcc, s88, v60
	v_add_f32_e32 v38, v58, v34
	v_ldexp_f32 v49, v49, v59
	v_cndmask_b32_e32 v48, v191, v48, vcc
	v_cmp_nlt_f32_e32 vcc, s89, v61
	v_add_f32_e32 v42, v35, v38
	s_nop 0
	v_cndmask_b32_e32 v49, 0, v49, vcc
	v_cmp_ngt_f32_e32 vcc, s88, v61
	s_nop 1
	v_cndmask_b32_e32 v49, v191, v49, vcc
	v_pk_add_f32 v[48:49], v[48:49], 1.0 op_sel_hi:[1,0]
	s_nop 0
	v_rcp_f32_e32 v59, v49
	s_nop 3
	v_mul_f32_e32 v49, v61, v59
	s_nop 1
	v_rcp_f32_e32 v59, v48
	s_nop 3
	v_mul_f32_e32 v48, v60, v59
	s_nop 1
	global_load_dwordx2 v[60:61], v[46:47], off offset:3104
	s_waitcnt vmcnt(0)
	v_lshlrev_b32_e32 v40, 16, v60
	v_mul_f32_e32 v38, 0xbfb8aa3b, v40
	v_fma_f32 v39, v40, s91, -v38
	v_rndne_f32_e32 v43, v38
	v_fmac_f32_e32 v39, 0xb2a5705f, v40
	v_sub_f32_e32 v38, v38, v43
	v_add_f32_e32 v38, v38, v39
	v_exp_f32_e32 v38, v38
	v_cvt_i32_f32_e32 v39, v43
	v_and_b32_e32 v41, 0xffff0000, v60
	v_cmp_nlt_f32_e32 vcc, s89, v40
	v_lshlrev_b32_e32 v65, 16, v61
	v_ldexp_f32 v38, v38, v39
	v_mul_f32_e32 v39, 0xbfb8aa3b, v41
	v_fma_f32 v43, v41, s91, -v39
	v_rndne_f32_e32 v44, v39
	v_fmac_f32_e32 v43, 0xb2a5705f, v41
	v_sub_f32_e32 v39, v39, v44
	v_add_f32_e32 v39, v39, v43
	v_exp_f32_e32 v39, v39
	v_cvt_i32_f32_e32 v43, v44
	v_cndmask_b32_e32 v38, 0, v38, vcc
	v_cmp_ngt_f32_e32 vcc, s88, v40
	v_and_b32_e32 v103, 0xffff0000, v61
	v_ldexp_f32 v39, v39, v43
	v_cndmask_b32_e32 v38, v191, v38, vcc
	v_cmp_nlt_f32_e32 vcc, s89, v41
	s_nop 1
	v_cndmask_b32_e32 v39, 0, v39, vcc
	v_cmp_ngt_f32_e32 vcc, s88, v41
	s_nop 1
	v_cndmask_b32_e32 v39, v191, v39, vcc
	v_pk_add_f32 v[38:39], v[38:39], 1.0 op_sel_hi:[1,0]
	s_nop 0
	v_rcp_f32_e32 v43, v39
	s_nop 3
	v_mul_f32_e32 v41, v41, v43
	s_nop 1
	v_rcp_f32_e32 v39, v38
	s_nop 3
	v_mul_f32_e32 v40, v40, v39
	s_nop 1
	v_add_f32_e32 v38, v36, v42
	v_add_f32_e32 v38, v37, v38
	v_add_f32_e32 v38, v38, v66
	v_add_f32_e32 v38, v67, v38
	v_add_f32_e32 v38, v56, v38
	v_add_f32_e32 v38, v57, v38
	v_add_f32_e32 v38, v38, v32
	v_add_f32_e32 v38, v33, v38
	v_add_f32_e32 v38, v108, v38
	v_add_f32_e32 v38, v109, v38
	ds_bpermute_b32 v39, v116, v38
	v_cmp_nlt_f32_e32 vcc, s89, v65
	s_waitcnt lgkmcnt(0)
	v_add_f32_e32 v38, v38, v39
	ds_bpermute_b32 v39, v117, v38
	s_waitcnt lgkmcnt(0)
	v_add_f32_e32 v38, v38, v39
	v_mul_f32_e32 v64, 0x3c800000, v38
	v_pk_add_f32 v[38:39], v[56:57], v[64:65] op_sel_hi:[1,0] neg_lo:[0,1] neg_hi:[0,1]
	v_mul_f32_e32 v56, 0xbfb8aa3b, v65
	v_fma_f32 v57, v65, s91, -v56
	v_rndne_f32_e32 v105, v56
	v_fmac_f32_e32 v57, 0xb2a5705f, v65
	v_sub_f32_e32 v56, v56, v105
	v_add_f32_e32 v56, v56, v57
	v_exp_f32_e32 v56, v56
	v_cvt_i32_f32_e32 v57, v105
	v_pk_add_f32 v[44:45], v[34:35], v[64:65] op_sel_hi:[1,0] neg_lo:[0,1] neg_hi:[0,1]
	v_pk_add_f32 v[34:35], v[32:33], v[64:65] op_sel_hi:[1,0] neg_lo:[0,1] neg_hi:[0,1]
	v_pk_add_f32 v[32:33], v[108:109], v[64:65] op_sel_hi:[1,0] neg_lo:[0,1] neg_hi:[0,1]
	v_ldexp_f32 v56, v56, v57
	v_mul_f32_e32 v57, 0xbfb8aa3b, v103
	v_fma_f32 v105, v103, s91, -v57
	v_rndne_f32_e32 v107, v57
	v_fmac_f32_e32 v105, 0xb2a5705f, v103
	v_sub_f32_e32 v57, v57, v107
	v_add_f32_e32 v57, v57, v105
	v_exp_f32_e32 v57, v57
	v_cvt_i32_f32_e32 v105, v107
	v_cndmask_b32_e32 v56, 0, v56, vcc
	v_cmp_ngt_f32_e32 vcc, s88, v65
	v_pk_add_f32 v[54:55], v[54:55], v[64:65] op_sel_hi:[1,0] neg_lo:[0,1] neg_hi:[0,1]
	v_ldexp_f32 v57, v57, v105
	v_cndmask_b32_e32 v56, v191, v56, vcc
	v_cmp_nlt_f32_e32 vcc, s89, v103
	v_pk_mul_f32 v[68:69], v[54:55], v[54:55]
	v_pk_add_f32 v[52:53], v[52:53], v[64:65] op_sel_hi:[1,0] neg_lo:[0,1] neg_hi:[0,1]
	v_cndmask_b32_e32 v57, 0, v57, vcc
	v_cmp_ngt_f32_e32 vcc, s88, v103
	v_pk_mul_f32 v[110:111], v[52:53], v[52:53]
	v_add_f32_e32 v68, v68, v69
	v_cndmask_b32_e32 v57, v191, v57, vcc
	v_pk_add_f32 v[56:57], v[56:57], 1.0 op_sel_hi:[1,0]
	v_add_f32_e32 v68, v110, v68
	v_div_scale_f32 v105, s[0:1], v57, v57, v103
	v_rcp_f32_e32 v107, v105
	v_pk_mul_f32 v[112:113], v[44:45], v[44:45]
	v_add_f32_e32 v68, v111, v68
	v_pk_add_f32 v[42:43], v[36:37], v[64:65] op_sel_hi:[1,0] neg_lo:[0,1] neg_hi:[0,1]
	v_fma_f32 v108, -v105, v107, 1.0
	v_fmac_f32_e32 v107, v108, v107
	v_div_scale_f32 v108, vcc, v103, v57, v103
	v_mul_f32_e32 v109, v108, v107
	v_fma_f32 v192, -v105, v109, v108
	v_fmac_f32_e32 v109, v192, v107
	v_fma_f32 v105, -v105, v109, v108
	v_div_fmas_f32 v105, v105, v107, v109
	v_div_fixup_f32 v57, v105, v57, v103
	v_div_scale_f32 v103, s[0:1], v56, v56, v65
	v_rcp_f32_e32 v105, v103
	v_add_f32_e32 v68, v112, v68
	v_pk_mul_f32 v[114:115], v[42:43], v[42:43]
	v_add_f32_e32 v68, v113, v68
	v_fma_f32 v107, -v103, v105, 1.0
	v_fmac_f32_e32 v105, v107, v105
	v_div_scale_f32 v107, vcc, v65, v56, v65
	v_mul_f32_e32 v108, v107, v105
	v_fma_f32 v109, -v103, v108, v107
	v_fmac_f32_e32 v108, v109, v105
	v_fma_f32 v103, -v103, v108, v107
	v_div_fmas_f32 v103, v103, v105, v108
	v_div_fixup_f32 v56, v103, v56, v65
	v_pk_add_f32 v[64:65], v[66:67], v[64:65] op_sel_hi:[1,0] neg_lo:[0,1] neg_hi:[0,1]
	v_add_f32_e32 v68, v114, v68
	v_pk_mul_f32 v[66:67], v[64:65], v[64:65]
	v_add_f32_e32 v68, v115, v68
	v_add_f32_e32 v66, v66, v68
	v_pk_mul_f32 v[36:37], v[38:39], v[38:39]
	v_add_f32_e32 v66, v67, v66
	v_add_f32_e32 v36, v36, v66
	v_pk_mul_f32 v[58:59], v[34:35], v[34:35]
	v_add_f32_e32 v36, v37, v36
	v_add_f32_e32 v36, v58, v36
	v_pk_mul_f32 v[60:61], v[32:33], v[32:33]
	v_add_f32_e32 v36, v59, v36
	v_add_f32_e32 v36, v60, v36
	v_add_f32_e32 v36, v61, v36
	ds_bpermute_b32 v37, v116, v36
	s_mov_b32 s0, 0xf800000
	global_load_dwordx2 v[108:109], v[46:47], off offset:3136
	s_waitcnt lgkmcnt(0)
	v_add_f32_e32 v36, v36, v37
	ds_bpermute_b32 v37, v117, v36
	s_waitcnt lgkmcnt(0)
	v_add_f32_e32 v36, v36, v37
	v_fmamk_f32 v36, v36, 0x3c800000, v189
	v_cmp_gt_f32_e32 vcc, s0, v36
	v_mul_f32_e32 v37, 0x4f800000, v36
	s_nop 0
	v_cndmask_b32_e32 v36, v36, v37, vcc
	v_sqrt_f32_e32 v37, v36
	s_nop 0
	v_add_u32_e32 v58, -1, v37
	v_fma_f32 v59, -v58, v37, v36
	v_cmp_ge_f32_e64 s[0:1], 0, v59
	v_add_u32_e32 v59, 1, v37
	s_nop 0
	v_cndmask_b32_e64 v58, v37, v58, s[0:1]
	v_fma_f32 v37, -v59, v37, v36
	v_cmp_lt_f32_e64 s[0:1], 0, v37
	s_nop 1
	v_cndmask_b32_e64 v37, v58, v59, s[0:1]
	v_mul_f32_e32 v58, 0x37800000, v37
	v_cndmask_b32_e32 v37, v37, v58, vcc
	v_cmp_class_f32_e32 vcc, v36, v190
	s_nop 1
	v_cndmask_b32_e32 v36, v37, v36, vcc
	v_rcp_f32_e32 v36, v36
	s_nop 3
	v_pk_mul_f32 v[54:55], v[54:55], v[36:37] op_sel_hi:[1,0]
	v_pk_mul_f32 v[44:45], v[44:45], v[36:37] op_sel_hi:[1,0]
	v_pk_mul_f32 v[26:27], v[26:27], v[54:55]
	s_nop 0
	v_pk_mul_f32 v[26:27], v[50:51], v[26:27]
	v_pk_mul_f32 v[50:51], v[52:53], v[36:37] op_sel_hi:[1,0]
	v_cvt_pk_bf16_f32 v26, v26, v27
	v_pk_mul_f32 v[28:29], v[28:29], v[50:51]
	s_nop 0
	v_pk_mul_f32 v[28:29], v[48:49], v[28:29]
	s_nop 0
	v_cvt_pk_bf16_f32 v27, v28, v29
	global_store_dwordx2 v[30:31], v[26:27], off
	global_load_dwordx4 v[26:29], v[62:63], off offset:64
	s_waitcnt vmcnt(0)
	v_pk_mul_f32 v[26:27], v[26:27], v[44:45]
	s_nop 0
	v_pk_mul_f32 v[26:27], v[40:41], v[26:27]
	v_pk_mul_f32 v[40:41], v[42:43], v[36:37] op_sel_hi:[1,0]
	v_cvt_pk_bf16_f32 v26, v26, v27
	v_pk_mul_f32 v[28:29], v[28:29], v[40:41]
	v_lshlrev_b32_e32 v37, 16, v108
	v_pk_mul_f32 v[28:29], v[56:57], v[28:29]
	v_mul_f32_e32 v40, 0xbfb8aa3b, v37
	v_cvt_pk_bf16_f32 v27, v28, v29
	global_store_dwordx2 v[30:31], v[26:27], off offset:32
	global_load_dwordx4 v[26:29], v[62:63], off offset:128
	v_fma_f32 v41, v37, s91, -v40
	v_rndne_f32_e32 v43, v40
	v_fmac_f32_e32 v41, 0xb2a5705f, v37
	v_sub_f32_e32 v40, v40, v43
	v_add_f32_e32 v40, v40, v41
	v_exp_f32_e32 v40, v40
	v_cvt_i32_f32_e32 v41, v43
	v_and_b32_e32 v42, 0xffff0000, v108
	v_cmp_nlt_f32_e32 vcc, s89, v37
	v_ldexp_f32 v40, v40, v41
	v_mul_f32_e32 v41, 0xbfb8aa3b, v42
	v_fma_f32 v43, v42, s91, -v41
	v_rndne_f32_e32 v44, v41
	v_fmac_f32_e32 v43, 0xb2a5705f, v42
	v_sub_f32_e32 v41, v41, v44
	v_add_f32_e32 v41, v41, v43
	v_exp_f32_e32 v41, v41
	v_cvt_i32_f32_e32 v43, v44
	v_cndmask_b32_e32 v40, 0, v40, vcc
	v_cmp_ngt_f32_e32 vcc, s88, v37
	v_ldexp_f32 v41, v41, v43
	s_nop 0
	v_cndmask_b32_e32 v40, v191, v40, vcc
	v_cmp_nlt_f32_e32 vcc, s89, v42
	s_nop 1
	v_cndmask_b32_e32 v41, 0, v41, vcc
	v_cmp_ngt_f32_e32 vcc, s88, v42
	s_nop 1
	v_cndmask_b32_e32 v41, v191, v41, vcc
	v_pk_add_f32 v[40:41], v[40:41], 1.0 op_sel_hi:[1,0]
	s_nop 0
	v_rcp_f32_e32 v43, v41
	s_nop 3
	v_mul_f32_e32 v41, v42, v43
	s_nop 1
	v_rcp_f32_e32 v42, v40
	s_nop 3
	v_mul_f32_e32 v40, v37, v42
	s_nop 1
	v_pk_mul_f32 v[42:43], v[64:65], v[36:37] op_sel_hi:[1,0]
	v_lshlrev_b32_e32 v37, 16, v109
	v_cmp_nlt_f32_e32 vcc, s89, v37
	v_pk_mul_f32 v[38:39], v[38:39], v[36:37] op_sel_hi:[1,0]
	s_waitcnt vmcnt(0)
	v_pk_mul_f32 v[26:27], v[26:27], v[42:43]
	s_nop 0
	v_pk_mul_f32 v[26:27], v[40:41], v[26:27]
	v_mul_f32_e32 v40, 0xbfb8aa3b, v37
	v_fma_f32 v41, v37, s91, -v40
	v_rndne_f32_e32 v43, v40
	v_fmac_f32_e32 v41, 0xb2a5705f, v37
	v_sub_f32_e32 v40, v40, v43
	v_add_f32_e32 v40, v40, v41
	v_exp_f32_e32 v40, v40
	v_cvt_i32_f32_e32 v41, v43
	v_and_b32_e32 v42, 0xffff0000, v109
	v_pk_mul_f32 v[28:29], v[28:29], v[38:39]
	v_cvt_pk_bf16_f32 v26, v26, v27
	v_ldexp_f32 v40, v40, v41
	v_mul_f32_e32 v41, 0xbfb8aa3b, v42
	v_fma_f32 v43, v42, s91, -v41
	v_rndne_f32_e32 v44, v41
	v_fmac_f32_e32 v43, 0xb2a5705f, v42
	v_sub_f32_e32 v41, v41, v44
	v_add_f32_e32 v41, v41, v43
	v_exp_f32_e32 v41, v41
	v_cvt_i32_f32_e32 v43, v44
	v_cndmask_b32_e32 v40, 0, v40, vcc
	v_cmp_ngt_f32_e32 vcc, s88, v37
	v_ldexp_f32 v41, v41, v43
	s_nop 0
	v_cndmask_b32_e32 v40, v191, v40, vcc
	v_cmp_nlt_f32_e32 vcc, s89, v42
	s_nop 1
	v_cndmask_b32_e32 v41, 0, v41, vcc
	v_cmp_ngt_f32_e32 vcc, s88, v42
	s_nop 1
	v_cndmask_b32_e32 v41, v191, v41, vcc
	v_pk_add_f32 v[40:41], v[40:41], 1.0 op_sel_hi:[1,0]
	s_nop 0
	v_rcp_f32_e32 v43, v41
	s_nop 3
	v_mul_f32_e32 v41, v42, v43
	s_nop 1
	v_rcp_f32_e32 v42, v40
	s_nop 3
	v_mul_f32_e32 v40, v37, v42
	s_nop 1
	v_pk_mul_f32 v[28:29], v[40:41], v[28:29]
	s_nop 0
	v_cvt_pk_bf16_f32 v27, v28, v29
	global_store_dwordx2 v[30:31], v[26:27], off offset:64
	global_load_dwordx2 v[38:39], v[46:47], off offset:3168
	s_nop 0
	global_load_dwordx4 v[26:29], v[62:63], off offset:192
	s_waitcnt vmcnt(1)
	v_lshlrev_b32_e32 v37, 16, v38
	v_mul_f32_e32 v40, 0xbfb8aa3b, v37
	v_fma_f32 v41, v37, s91, -v40
	v_rndne_f32_e32 v42, v40
	v_fmac_f32_e32 v41, 0xb2a5705f, v37
	v_sub_f32_e32 v40, v40, v42
	v_add_f32_e32 v40, v40, v41
	v_exp_f32_e32 v40, v40
	v_cvt_i32_f32_e32 v41, v42
	v_and_b32_e32 v38, 0xffff0000, v38
	v_cmp_nlt_f32_e32 vcc, s89, v37
	v_pk_mul_f32 v[34:35], v[34:35], v[36:37] op_sel_hi:[1,0]
	v_ldexp_f32 v40, v40, v41
	v_mul_f32_e32 v41, 0xbfb8aa3b, v38
	v_fma_f32 v42, v38, s91, -v41
	v_rndne_f32_e32 v43, v41
	v_fmac_f32_e32 v42, 0xb2a5705f, v38
	v_sub_f32_e32 v41, v41, v43
	v_add_f32_e32 v41, v41, v42
	v_exp_f32_e32 v41, v41
	v_cvt_i32_f32_e32 v42, v43
	v_cndmask_b32_e32 v40, 0, v40, vcc
	v_cmp_ngt_f32_e32 vcc, s88, v37
	s_waitcnt vmcnt(0)
	v_pk_mul_f32 v[26:27], v[26:27], v[34:35]
	v_ldexp_f32 v41, v41, v42
	v_cndmask_b32_e32 v40, v191, v40, vcc
	v_cmp_nlt_f32_e32 vcc, s89, v38
	s_nop 1
	v_cndmask_b32_e32 v41, 0, v41, vcc
	v_cmp_ngt_f32_e32 vcc, s88, v38
	s_nop 1
	v_cndmask_b32_e32 v41, v191, v41, vcc
	v_pk_add_f32 v[40:41], v[40:41], 1.0 op_sel_hi:[1,0]
	s_nop 0
	v_rcp_f32_e32 v42, v41
	s_nop 3
	v_mul_f32_e32 v41, v38, v42
	s_nop 1
	v_rcp_f32_e32 v38, v40
	s_nop 3
	v_mul_f32_e32 v40, v37, v38
	s_nop 1
	v_lshlrev_b32_e32 v37, 16, v39
	v_mul_f32_e32 v34, 0xbfb8aa3b, v37
	v_and_b32_e32 v38, 0xffff0000, v39
	v_fma_f32 v35, v37, s91, -v34
	v_rndne_f32_e32 v39, v34
	v_fmac_f32_e32 v35, 0xb2a5705f, v37
	v_sub_f32_e32 v34, v34, v39
	v_add_f32_e32 v34, v34, v35
	v_exp_f32_e32 v34, v34
	v_cvt_i32_f32_e32 v35, v39
	v_pk_mul_f32 v[26:27], v[40:41], v[26:27]
	v_cmp_nlt_f32_e32 vcc, s89, v37
	v_pk_mul_f32 v[32:33], v[32:33], v[36:37] op_sel_hi:[1,0]
	v_ldexp_f32 v34, v34, v35
	v_mul_f32_e32 v35, 0xbfb8aa3b, v38
	v_fma_f32 v39, v38, s91, -v35
	v_rndne_f32_e32 v40, v35
	v_fmac_f32_e32 v39, 0xb2a5705f, v38
	v_sub_f32_e32 v35, v35, v40
	v_add_f32_e32 v35, v35, v39
	v_exp_f32_e32 v35, v35
	v_cvt_i32_f32_e32 v39, v40
	v_cndmask_b32_e32 v34, 0, v34, vcc
	v_cmp_ngt_f32_e32 vcc, s88, v37
	v_pk_mul_f32 v[28:29], v[28:29], v[32:33]
	v_ldexp_f32 v35, v35, v39
	v_cndmask_b32_e32 v34, v191, v34, vcc
	v_cmp_nlt_f32_e32 vcc, s89, v38
	v_cvt_pk_bf16_f32 v26, v26, v27
	s_nop 0
	v_cndmask_b32_e32 v35, 0, v35, vcc
	v_cmp_ngt_f32_e32 vcc, s88, v38
	s_nop 1
	v_cndmask_b32_e32 v35, v191, v35, vcc
	v_pk_add_f32 v[34:35], v[34:35], 1.0 op_sel_hi:[1,0]
	s_nop 0
	v_rcp_f32_e32 v39, v35
	s_nop 3
	v_mul_f32_e32 v35, v38, v39
	s_nop 1
	v_rcp_f32_e32 v38, v34
	s_nop 3
	v_mul_f32_e32 v34, v37, v38
	s_nop 1
	v_pk_mul_f32 v[28:29], v[34:35], v[28:29]
	s_andn2_b64 vcc, exec, s[84:85]
	v_cvt_pk_bf16_f32 v27, v28, v29
	global_store_dwordx2 v[30:31], v[26:27], off offset:96
	s_cbranch_vccz .LBB0_1286

.LBB0_1289:
	v_lshl_add_u64 v[56:57], v[38:39], 0, s[20:21]
	v_cmp_gt_i64_e64 s[10:11], s[12:13], v[56:57]
	s_nop 1
	v_cndmask_b32_e64 v2, v38, v56, s[10:11]
	v_cndmask_b32_e64 v3, v39, v57, s[10:11]
	v_and_b32_e32 v54, 56, v2
	v_ashrrev_i64 v[4:5], 6, v[2:3]
	v_lshl_add_u64 v[6:7], s[18:19], 0, v[54:55]
	s_waitcnt vmcnt(0)
	v_lshlrev_b32_e32 v1, 4, v2
	v_and_b32_e32 v2, 0xffffffc0, v2
	v_and_b32_e32 v54, 0x3f0, v1
	v_lshl_add_u64 v[2:3], v[6:7], 0, v[2:3]
	v_lshl_add_u64 v[8:9], s[16:17], 0, v[54:55]
	global_load_dwordx2 v[62:63], v[2:3], off
	v_lshlrev_b64 v[2:3], 10, v[4:5]
	v_lshl_add_u64 v[2:3], v[8:9], 0, v[2:3]
	global_load_dwordx4 v[22:25], v[2:3], off
	v_lshl_add_u64 v[2:3], v[4:5], 0, s[36:37]
	v_lshlrev_b64 v[10:11], 6, v[2:3]
	v_lshlrev_b64 v[2:3], 10, v[2:3]
	v_lshl_add_u64 v[10:11], v[6:7], 0, v[10:11]
	v_lshl_add_u64 v[2:3], v[8:9], 0, v[2:3]
	global_load_dwordx2 v[68:69], v[10:11], off
	global_load_dwordx4 v[30:33], v[2:3], off
	v_lshl_add_u64 v[2:3], v[4:5], 0, s[38:39]
	v_lshlrev_b64 v[4:5], 6, v[2:3]
	v_lshlrev_b64 v[2:3], 10, v[2:3]
	v_lshl_add_u64 v[4:5], v[6:7], 0, v[4:5]
	v_lshl_add_u64 v[2:3], v[8:9], 0, v[2:3]
	global_load_dwordx2 v[76:77], v[4:5], off
	global_load_dwordx4 v[34:37], v[2:3], off
	v_lshl_add_u64 v[2:3], s[26:27], 0, v[38:39]
	v_cmp_gt_i64_e64 s[8:9], s[12:13], v[2:3]
	s_nop 1
	v_cndmask_b32_e64 v2, v38, v2, s[8:9]
	v_cndmask_b32_e64 v3, v39, v3, s[8:9]
	v_and_b32_e32 v54, 56, v2
	v_ashrrev_i64 v[4:5], 6, v[2:3]
	v_lshl_add_u64 v[6:7], s[18:19], 0, v[54:55]
	v_lshlrev_b32_e32 v1, 4, v2
	v_and_b32_e32 v2, 0xffffffc0, v2
	v_and_b32_e32 v54, 0x3f0, v1
	v_lshl_add_u64 v[2:3], v[6:7], 0, v[2:3]
	v_lshl_add_u64 v[8:9], s[16:17], 0, v[54:55]
	global_load_dwordx2 v[60:61], v[2:3], off
	v_lshlrev_b64 v[2:3], 10, v[4:5]
	v_lshl_add_u64 v[2:3], v[8:9], 0, v[2:3]
	global_load_dwordx4 v[14:17], v[2:3], off
	v_lshl_add_u64 v[2:3], v[4:5], 0, s[36:37]
	v_lshlrev_b64 v[10:11], 6, v[2:3]
	v_lshlrev_b64 v[2:3], 10, v[2:3]
	v_lshl_add_u64 v[10:11], v[6:7], 0, v[10:11]
	v_lshl_add_u64 v[2:3], v[8:9], 0, v[2:3]
	global_load_dwordx2 v[66:67], v[10:11], off
	global_load_dwordx4 v[18:21], v[2:3], off
	v_lshl_add_u64 v[2:3], v[4:5], 0, s[38:39]
	v_lshlrev_b64 v[4:5], 6, v[2:3]
	v_lshlrev_b64 v[2:3], 10, v[2:3]
	v_lshl_add_u64 v[4:5], v[6:7], 0, v[4:5]
	v_lshl_add_u64 v[2:3], v[8:9], 0, v[2:3]
	global_load_dwordx2 v[74:75], v[4:5], off
	global_load_dwordx4 v[26:29], v[2:3], off
	v_lshl_add_u64 v[2:3], s[30:31], 0, v[38:39]
	v_cmp_gt_i64_e64 s[0:1], s[12:13], v[2:3]
	s_nop 1
	v_cndmask_b32_e64 v3, v39, v3, s[0:1]
	v_cndmask_b32_e64 v2, v38, v2, s[0:1]
	v_ashrrev_i64 v[10:11], 6, v[2:3]
	v_and_b32_e32 v54, 56, v2
	v_lshlrev_b32_e32 v1, 4, v2
	v_lshl_add_u64 v[12:13], s[18:19], 0, v[54:55]
	v_and_b32_e32 v54, 0x3f0, v1
	v_lshl_add_u64 v[6:7], v[10:11], 0, s[36:37]
	v_lshl_add_u64 v[40:41], s[16:17], 0, v[54:55]
	v_and_b32_e32 v2, 0xffffffc0, v2
	v_lshlrev_b64 v[8:9], 6, v[6:7]
	v_lshlrev_b64 v[6:7], 10, v[6:7]
	v_lshl_add_u64 v[2:3], v[12:13], 0, v[2:3]
	v_lshl_add_u64 v[8:9], v[12:13], 0, v[8:9]
	v_lshl_add_u64 v[6:7], v[40:41], 0, v[6:7]
	global_load_dwordx2 v[58:59], v[2:3], off
	global_load_dwordx2 v[64:65], v[8:9], off
	v_and_b32_e32 v54, 56, v38
	global_load_dwordx4 v[6:9], v[6:7], off
	v_lshlrev_b64 v[2:3], 10, v[10:11]
	v_lshl_add_u64 v[10:11], v[10:11], 0, s[38:39]
	v_lshlrev_b64 v[42:43], 6, v[10:11]
	v_lshlrev_b64 v[10:11], 10, v[10:11]
	v_lshl_add_u64 v[2:3], v[40:41], 0, v[2:3]
	v_lshl_add_u64 v[12:13], v[12:13], 0, v[42:43]
	v_lshl_add_u64 v[10:11], v[40:41], 0, v[10:11]
	v_lshl_add_u64 v[40:41], s[18:19], 0, v[54:55]
	v_and_b32_e32 v42, 0xffffffc0, v38
	v_mov_b32_e32 v43, v39
	v_lshl_add_u64 v[42:43], v[40:41], 0, v[42:43]
	v_ashrrev_i64 v[38:39], 6, v[38:39]
	global_load_dwordx2 v[44:45], v[42:43], off
	v_lshl_add_u64 v[42:43], v[38:39], 0, s[36:37]
	v_lshlrev_b64 v[46:47], 6, v[42:43]
	v_lshl_add_u64 v[46:47], v[40:41], 0, v[46:47]
	global_load_dwordx2 v[48:49], v[46:47], off
	v_lshl_add_u64 v[46:47], v[38:39], 0, s[38:39]
	v_lshlrev_b64 v[78:79], 6, v[46:47]
	v_lshl_add_u64 v[40:41], v[40:41], 0, v[78:79]
	global_load_dwordx2 v[40:41], v[40:41], off
	v_lshlrev_b64 v[38:39], 10, v[38:39]
	v_lshlrev_b64 v[42:43], 10, v[42:43]
	global_load_dwordx2 v[72:73], v[12:13], off
	v_lshlrev_b64 v[46:47], 10, v[46:47]
	global_load_dwordx4 v[2:5], v[2:3], off
	s_waitcnt vmcnt(2)
	v_max3_f32 v1, v44, v48, v40
	v_sub_f32_e32 v44, v44, v1
	v_mul_f32_e32 v44, 0x3fb8aa3b, v44
	v_exp_f32_e32 v44, v44
	s_nop 0
	v_mul_f32_e32 v54, v45, v44
	v_fma_f32 v71, v45, v44, 0
	v_sub_f32_e32 v44, v48, v1
	v_sub_f32_e32 v1, v40, v1
	v_mul_f32_e32 v44, 0x3fb8aa3b, v44
	v_mul_f32_e32 v1, 0x3fb8aa3b, v1
	v_exp_f32_e32 v45, v44
	v_exp_f32_e32 v44, v1
	v_mov_b32_e32 v48, v41
	v_pk_mul_f32 v[48:49], v[48:49], v[44:45]
	s_nop 0
	v_add_f32_e32 v1, v49, v71
	v_add_f32_e32 v1, v48, v1
	v_rcp_f32_e32 v1, v1
	s_nop 3
	v_and_b32_e32 v40, 0x1f8, v52
	v_mul_f32_e32 v78, v54, v1
	v_lshlrev_b32_e32 v54, 1, v40
	v_lshl_add_u64 v[84:85], s[16:17], 0, v[54:55]
	v_lshl_add_u64 v[38:39], v[84:85], 0, v[38:39]
	global_load_dwordx4 v[38:41], v[38:39], off
	v_lshl_add_u64 v[42:43], v[84:85], 0, v[42:43]
	global_load_dwordx4 v[42:45], v[42:43], off
	v_lshl_add_u64 v[46:47], v[84:85], 0, v[46:47]
	v_mul_f32_e32 v80, v49, v1
	v_mul_f32_e32 v82, v48, v1
	global_load_dwordx4 v[46:49], v[46:47], off
	s_waitcnt vmcnt(2)
	v_lshlrev_b32_e32 v84, 16, v38
	global_load_dwordx4 v[10:13], v[10:11], off
	v_and_b32_e32 v85, 0xffff0000, v38
	v_lshlrev_b32_e32 v38, 16, v39
	v_and_b32_e32 v39, 0xffff0000, v39
	s_waitcnt vmcnt(2)
	v_lshlrev_b32_e32 v86, 16, v42
	v_and_b32_e32 v87, 0xffff0000, v42
	v_pk_fma_f32 v[38:39], v[78:79], v[38:39], 0 op_sel_hi:[0,1,0]
	v_lshlrev_b32_e32 v42, 16, v43
	v_and_b32_e32 v43, 0xffff0000, v43
	v_pk_fma_f32 v[38:39], v[80:81], v[42:43], v[38:39] op_sel_hi:[0,1,1]
	s_waitcnt vmcnt(1)
	v_lshlrev_b32_e32 v42, 16, v47
	v_and_b32_e32 v43, 0xffff0000, v47
	v_pk_fma_f32 v[84:85], v[78:79], v[84:85], 0 op_sel_hi:[0,1,0]
	v_pk_fma_f32 v[42:43], v[82:83], v[42:43], v[38:39] op_sel_hi:[0,1,1]
	v_lshlrev_b32_e32 v38, 16, v40
	v_and_b32_e32 v39, 0xffff0000, v40
	v_pk_fma_f32 v[84:85], v[80:81], v[86:87], v[84:85] op_sel_hi:[0,1,1]
	v_lshlrev_b32_e32 v86, 16, v46
	v_and_b32_e32 v87, 0xffff0000, v46
	v_pk_fma_f32 v[38:39], v[78:79], v[38:39], 0 op_sel_hi:[0,1,0]
	v_lshlrev_b32_e32 v46, 16, v44
	v_and_b32_e32 v47, 0xffff0000, v44
	v_pk_fma_f32 v[38:39], v[80:81], v[46:47], v[38:39] op_sel_hi:[0,1,1]
	v_lshlrev_b32_e32 v46, 16, v48
	v_and_b32_e32 v47, 0xffff0000, v48
	v_pk_fma_f32 v[46:47], v[82:83], v[46:47], v[38:39] op_sel_hi:[0,1,1]
	v_lshlrev_b32_e32 v38, 16, v41
	v_and_b32_e32 v39, 0xffff0000, v41
	v_pk_fma_f32 v[38:39], v[78:79], v[38:39], 0 op_sel_hi:[0,1,0]
	v_lshlrev_b32_e32 v40, 16, v45
	v_and_b32_e32 v41, 0xffff0000, v45
	v_pk_fma_f32 v[38:39], v[80:81], v[40:41], v[38:39] op_sel_hi:[0,1,1]
	v_lshlrev_b32_e32 v40, 16, v49
	v_and_b32_e32 v41, 0xffff0000, v49
	v_pk_fma_f32 v[44:45], v[82:83], v[40:41], v[38:39] op_sel_hi:[0,1,1]
	v_and_b32_e32 v39, 0x7fffffff, v51
	v_and_b32_e32 v38, 0xfffff800, v50
	v_pk_fma_f32 v[84:85], v[82:83], v[86:87], v[84:85] op_sel_hi:[0,1,1]
	v_lshl_add_u64 v[38:39], v[38:39], 1, s[92:93]
	v_lshl_add_u64 v[48:49], v[38:39], 0, v[54:55]
	v_cvt_pk_bf16_f32 v38, v84, v85
	v_cvt_pk_bf16_f32 v39, v42, v43
	v_cvt_pk_bf16_f32 v40, v46, v47
	v_cvt_pk_bf16_f32 v41, v44, v45
	global_store_dwordx4 v[48:49], v[38:41], off offset:3072
	s_and_saveexec_b64 s[40:41], s[10:11]
	s_cbranch_execnz .LBB0_1292
	s_or_b64 exec, exec, s[40:41]
	s_and_saveexec_b64 s[10:11], s[8:9]
	s_cbranch_execnz .LBB0_1293

.LBB0_2690:
	s_or_b64 exec, exec, s[4:5]
	v_lshlrev_b64 v[132:133], 2, v[130:131]
	v_lshl_add_u64 v[126:127], s[28:29], 0, v[132:133]
	global_load_dwordx4 v[168:171], v[126:127], off offset:16
	s_nop 0
	global_load_dwordx4 v[126:129], v[126:127], off
	v_lshl_add_u64 v[132:133], s[36:37], 0, v[132:133]
	global_load_dwordx4 v[172:175], v[132:133], off offset:16
	global_load_dwordx4 v[176:179], v[132:133], off
	s_waitcnt vmcnt(4)
	v_lshlrev_b32_e32 v132, 16, v114
	v_and_b32_e32 v133, 0xffff0000, v114
	v_lshlrev_b32_e32 v180, 16, v118
	v_and_b32_e32 v181, 0xffff0000, v118
	v_lshlrev_b32_e32 v114, 16, v115
	v_and_b32_e32 v115, 0xffff0000, v115
	v_lshlrev_b32_e32 v118, 16, v119
	v_and_b32_e32 v119, 0xffff0000, v119
	v_lshlrev_b32_e32 v182, 16, v122
	v_and_b32_e32 v183, 0xffff0000, v122
	v_lshlrev_b32_e32 v122, 16, v123
	v_and_b32_e32 v123, 0xffff0000, v123
	v_pk_add_f32 v[118:119], v[118:119], v[114:115] neg_lo:[0,1] neg_hi:[0,1]
	v_pk_add_f32 v[180:181], v[180:181], v[132:133] neg_lo:[0,1] neg_hi:[0,1]
	v_cmp_lt_u32_e32 vcc, s76, v130
	s_waitcnt vmcnt(2)
	v_pk_fma_f32 v[118:119], v[118:119], v[128:129], v[114:115]
	v_pk_add_f32 v[114:115], v[122:123], v[114:115] neg_lo:[0,1] neg_hi:[0,1]
	v_lshlrev_b32_e32 v122, 16, v120
	s_waitcnt vmcnt(0)
	v_pk_fma_f32 v[114:115], v[114:115], v[178:179], v[118:119]
	v_lshlrev_b32_e32 v118, 16, v116
	v_and_b32_e32 v119, 0xffff0000, v116
	v_and_b32_e32 v123, 0xffff0000, v120
	v_lshlrev_b32_e32 v128, 16, v124
	v_and_b32_e32 v129, 0xffff0000, v124
	v_pk_add_f32 v[122:123], v[122:123], v[118:119] neg_lo:[0,1] neg_hi:[0,1]
	v_lshlrev_b32_e32 v116, 16, v117
	v_pk_fma_f32 v[122:123], v[122:123], v[168:169], v[118:119]
	v_pk_add_f32 v[118:119], v[128:129], v[118:119] neg_lo:[0,1] neg_hi:[0,1]
	v_and_b32_e32 v117, 0xffff0000, v117
	v_lshlrev_b32_e32 v120, 16, v121
	v_and_b32_e32 v121, 0xffff0000, v121
	v_pk_fma_f32 v[118:119], v[118:119], v[172:173], v[122:123]
	v_lshlrev_b32_e32 v122, 16, v125
	v_and_b32_e32 v123, 0xffff0000, v125
	v_pk_add_f32 v[120:121], v[120:121], v[116:117] neg_lo:[0,1] neg_hi:[0,1]
	v_pk_fma_f32 v[126:127], v[180:181], v[126:127], v[132:133]
	v_pk_add_f32 v[132:133], v[182:183], v[132:133] neg_lo:[0,1] neg_hi:[0,1]
	v_pk_fma_f32 v[120:121], v[120:121], v[170:171], v[116:117]
	v_pk_add_f32 v[116:117], v[122:123], v[116:117] neg_lo:[0,1] neg_hi:[0,1]
	v_pk_fma_f32 v[126:127], v[132:133], v[176:177], v[126:127]
	v_pk_fma_f32 v[116:117], v[116:117], v[174:175], v[120:121]
	s_and_saveexec_b64 s[2:3], vcc
	s_xor_b64 s[4:5], exec, s[2:3]
	s_cbranch_execz .LBB0_2738
	v_cmp_lt_u32_e32 vcc, s77, v130
	s_and_saveexec_b64 s[2:3], vcc
	s_xor_b64 s[46:47], exec, s[2:3]
	s_cbranch_execz .LBB0_2735
	v_cmp_lt_u32_e32 vcc, s78, v130
	s_and_saveexec_b64 s[2:3], vcc
	s_xor_b64 s[48:49], exec, s[2:3]
	s_cbranch_execz .LBB0_2732
	v_cmp_lt_u32_e32 vcc, s79, v130
	s_and_saveexec_b64 s[2:3], vcc
	s_xor_b64 s[50:51], exec, s[2:3]
	s_cbranch_execz .LBB0_2697
	v_cmp_lt_u32_e32 vcc, s80, v130
	s_and_saveexec_b64 s[52:53], vcc
	s_cbranch_execz .LBB0_2696
	v_mul_f32_e32 v120, 0xbfb8aa3b, v126
	v_rndne_f32_e32 v121, v120
	v_sub_f32_e32 v122, v120, v121
	v_fma_f32 v120, v126, s81, -v120
	v_fmac_f32_e32 v120, 0xb2a5705f, v126
	v_add_f32_e32 v120, v122, v120
	v_exp_f32_e32 v120, v120
	v_cvt_i32_f32_e32 v121, v121
	v_cmp_nlt_f32_e32 vcc, s82, v126
	v_ldexp_f32 v120, v120, v121
	v_mul_f32_e32 v121, 0xbfb8aa3b, v127
	v_rndne_f32_e32 v122, v121
	v_sub_f32_e32 v123, v121, v122
	v_fma_f32 v121, v127, s81, -v121
	v_fmac_f32_e32 v121, 0xb2a5705f, v127
	v_add_f32_e32 v121, v123, v121
	v_exp_f32_e32 v121, v121
	v_cvt_i32_f32_e32 v122, v122
	v_cndmask_b32_e32 v120, 0, v120, vcc
	v_cmp_ngt_f32_e32 vcc, s83, v126
	v_ldexp_f32 v121, v121, v122
	v_mul_f32_e32 v122, 0xbfb8aa3b, v114
	v_rndne_f32_e32 v123, v122
	v_sub_f32_e32 v124, v122, v123
	v_fma_f32 v122, v114, s81, -v122
	v_fmac_f32_e32 v122, 0xb2a5705f, v114
	v_add_f32_e32 v122, v124, v122
	v_exp_f32_e32 v122, v122
	v_cvt_i32_f32_e32 v123, v123
	v_cndmask_b32_e32 v120, v143, v120, vcc
	v_cmp_nlt_f32_e32 vcc, s82, v127
	v_ldexp_f32 v122, v122, v123
	s_nop 0
	v_cndmask_b32_e32 v121, 0, v121, vcc
	v_cmp_ngt_f32_e32 vcc, s83, v127
	s_nop 1
	v_cndmask_b32_e32 v121, v143, v121, vcc
	v_cmp_nlt_f32_e32 vcc, s82, v114
	v_pk_add_f32 v[120:121], v[120:121], 1.0 op_sel_hi:[1,0]
	s_nop 0
	v_cndmask_b32_e32 v122, 0, v122, vcc
	v_cmp_ngt_f32_e32 vcc, s83, v114
	s_nop 1
	v_cndmask_b32_e32 v114, v143, v122, vcc
	v_mul_f32_e32 v122, 0xbfb8aa3b, v115
	v_rndne_f32_e32 v123, v122
	v_sub_f32_e32 v124, v122, v123
	v_fma_f32 v122, v115, s81, -v122
	v_fmac_f32_e32 v122, 0xb2a5705f, v115
	v_add_f32_e32 v122, v124, v122
	v_exp_f32_e32 v122, v122
	v_cvt_i32_f32_e32 v123, v123
	v_cmp_nlt_f32_e32 vcc, s82, v115
	v_ldexp_f32 v122, v122, v123
	s_nop 0
	v_cndmask_b32_e32 v122, 0, v122, vcc
	v_cmp_ngt_f32_e32 vcc, s83, v115
	s_nop 1
	v_cndmask_b32_e32 v115, v143, v122, vcc
	v_mul_f32_e32 v122, 0xbfb8aa3b, v118
	v_rndne_f32_e32 v123, v122
	v_sub_f32_e32 v124, v122, v123
	v_fma_f32 v122, v118, s81, -v122
	v_fmac_f32_e32 v122, 0xb2a5705f, v118
	v_add_f32_e32 v122, v124, v122
	v_exp_f32_e32 v122, v122
	v_cvt_i32_f32_e32 v123, v123
	v_cmp_nlt_f32_e32 vcc, s82, v118
	v_pk_add_f32 v[114:115], v[114:115], 1.0 op_sel_hi:[1,0]
	v_ldexp_f32 v122, v122, v123
	v_cndmask_b32_e32 v122, 0, v122, vcc
	v_cmp_ngt_f32_e32 vcc, s83, v118
	s_nop 1
	v_cndmask_b32_e32 v118, v143, v122, vcc
	v_mul_f32_e32 v122, 0xbfb8aa3b, v119
	v_rndne_f32_e32 v123, v122
	v_sub_f32_e32 v124, v122, v123
	v_fma_f32 v122, v119, s81, -v122
	v_fmac_f32_e32 v122, 0xb2a5705f, v119
	v_add_f32_e32 v122, v124, v122
	v_exp_f32_e32 v122, v122
	v_cvt_i32_f32_e32 v123, v123
	v_cmp_nlt_f32_e32 vcc, s82, v119
	v_ldexp_f32 v122, v122, v123
	s_nop 0
	v_cndmask_b32_e32 v122, 0, v122, vcc
	v_cmp_ngt_f32_e32 vcc, s83, v119
	s_nop 1
	v_cndmask_b32_e32 v119, v143, v122, vcc
	v_mul_f32_e32 v122, 0xbfb8aa3b, v116
	v_rndne_f32_e32 v123, v122
	v_sub_f32_e32 v124, v122, v123
	v_fma_f32 v122, v116, s81, -v122
	v_fmac_f32_e32 v122, 0xb2a5705f, v116
	v_add_f32_e32 v122, v124, v122
	v_exp_f32_e32 v122, v122
	v_cvt_i32_f32_e32 v123, v123
	v_cmp_nlt_f32_e32 vcc, s82, v116
	v_pk_add_f32 v[118:119], v[118:119], 1.0 op_sel_hi:[1,0]
	v_ldexp_f32 v122, v122, v123
	v_cndmask_b32_e32 v122, 0, v122, vcc
	v_cmp_ngt_f32_e32 vcc, s83, v116
	s_nop 1
	v_cndmask_b32_e32 v116, v143, v122, vcc
	v_mul_f32_e32 v122, 0xbfb8aa3b, v117
	v_rndne_f32_e32 v123, v122
	v_sub_f32_e32 v124, v122, v123
	v_fma_f32 v122, v117, s81, -v122
	v_fmac_f32_e32 v122, 0xb2a5705f, v117
	v_add_f32_e32 v122, v124, v122
	v_exp_f32_e32 v122, v122
	v_cvt_i32_f32_e32 v123, v123
	v_cmp_nlt_f32_e32 vcc, s82, v117
	v_ldexp_f32 v122, v122, v123
	s_nop 0
	v_cndmask_b32_e32 v122, 0, v122, vcc
	v_cmp_ngt_f32_e32 vcc, s83, v117
	s_nop 1
	v_cndmask_b32_e32 v117, v143, v122, vcc
	v_div_scale_f32 v122, s[2:3], v120, v120, 1.0
	v_rcp_f32_e32 v123, v122
	v_pk_add_f32 v[116:117], v[116:117], 1.0 op_sel_hi:[1,0]
	v_fma_f32 v124, -v122, v123, 1.0
	v_fmac_f32_e32 v123, v124, v123
	v_div_scale_f32 v124, vcc, 1.0, v120, 1.0
	v_mul_f32_e32 v125, v124, v123
	v_fma_f32 v126, -v122, v125, v124
	v_fmac_f32_e32 v125, v126, v123
	v_fma_f32 v122, -v122, v125, v124
	v_div_fmas_f32 v122, v122, v123, v125
	v_div_fixup_f32 v126, v122, v120, 1.0
	v_rcp_f32_e32 v127, v121
	s_nop 3
	v_rcp_f32_e32 v114, v114
	s_nop 3
	v_rcp_f32_e32 v115, v115
	s_nop 3
	v_rcp_f32_e32 v118, v118
	s_nop 3
	v_rcp_f32_e32 v119, v119
	s_nop 3
	v_rcp_f32_e32 v116, v116
	s_nop 3
	v_div_scale_f32 v120, s[2:3], v117, v117, 1.0
	v_rcp_f32_e32 v121, v120
	s_nop 0
	v_fma_f32 v122, -v120, v121, 1.0
	v_fmac_f32_e32 v121, v122, v121
	v_div_scale_f32 v122, vcc, 1.0, v117, 1.0
	v_mul_f32_e32 v123, v122, v121
	v_fma_f32 v124, -v120, v123, v122
	v_fmac_f32_e32 v123, v124, v121
	v_fma_f32 v120, -v120, v123, v122
	v_div_fmas_f32 v120, v120, v121, v123
	v_div_fixup_f32 v117, v120, v117, 1.0

.LBB0_2747:
	v_add_u32_e32 v130, v120, v165
	v_lshlrev_b64 v[114:115], 2, v[130:131]
	v_lshl_add_u64 v[122:123], s[28:29], 0, v[114:115]
	global_load_dwordx4 v[116:119], v[122:123], off offset:16
	s_nop 0
	global_load_dwordx4 v[122:125], v[122:123], off
	v_lshl_add_u64 v[114:115], s[36:37], 0, v[114:115]
	v_lshrrev_b32_e32 v121, 2, v166
	global_load_dwordx4 v[126:129], v[114:115], off offset:16
	global_load_dwordx4 v[164:167], v[114:115], off
	v_lshlrev_b32_e32 v114, 16, v10
	v_and_b32_e32 v115, 0xffff0000, v10
	v_lshlrev_b32_e32 v132, 16, v110
	v_and_b32_e32 v133, 0xffff0000, v110
	v_lshlrev_b32_e32 v168, 16, v38
	v_and_b32_e32 v169, 0xffff0000, v38
	v_pk_add_f32 v[132:133], v[132:133], v[114:115] neg_lo:[0,1] neg_hi:[0,1]
	v_lshlrev_b32_e32 v110, 16, v111
	v_and_b32_e32 v111, 0xffff0000, v111
	v_cmp_lt_u32_e32 vcc, s76, v130
	s_waitcnt vmcnt(2)
	v_pk_fma_f32 v[122:123], v[132:133], v[122:123], v[114:115]
	v_pk_add_f32 v[114:115], v[168:169], v[114:115] neg_lo:[0,1] neg_hi:[0,1]
	v_lshlrev_b32_e32 v132, 16, v39
	s_waitcnt vmcnt(0)
	v_pk_fma_f32 v[114:115], v[114:115], v[164:165], v[122:123]
	v_lshlrev_b32_e32 v122, 16, v11
	v_and_b32_e32 v123, 0xffff0000, v11
	v_and_b32_e32 v133, 0xffff0000, v39
	v_pk_add_f32 v[110:111], v[110:111], v[122:123] neg_lo:[0,1] neg_hi:[0,1]
	s_nop 0
	v_pk_fma_f32 v[110:111], v[110:111], v[124:125], v[122:123]
	v_pk_add_f32 v[122:123], v[132:133], v[122:123] neg_lo:[0,1] neg_hi:[0,1]
	v_lshlrev_b32_e32 v124, 16, v112
	v_pk_fma_f32 v[110:111], v[122:123], v[166:167], v[110:111]
	v_lshlrev_b32_e32 v122, 16, v12
	v_and_b32_e32 v123, 0xffff0000, v12
	v_and_b32_e32 v125, 0xffff0000, v112
	v_lshlrev_b32_e32 v132, 16, v40
	v_and_b32_e32 v133, 0xffff0000, v40
	v_pk_add_f32 v[124:125], v[124:125], v[122:123] neg_lo:[0,1] neg_hi:[0,1]
	v_lshlrev_b32_e32 v112, 16, v113
	v_pk_fma_f32 v[116:117], v[124:125], v[116:117], v[122:123]
	v_pk_add_f32 v[122:123], v[132:133], v[122:123] neg_lo:[0,1] neg_hi:[0,1]
	v_and_b32_e32 v113, 0xffff0000, v113
	v_pk_fma_f32 v[116:117], v[122:123], v[126:127], v[116:117]
	v_lshlrev_b32_e32 v122, 16, v13
	v_and_b32_e32 v123, 0xffff0000, v13
	v_lshlrev_b32_e32 v124, 16, v41
	v_and_b32_e32 v125, 0xffff0000, v41
	v_pk_add_f32 v[112:113], v[112:113], v[122:123] neg_lo:[0,1] neg_hi:[0,1]
	s_nop 0
	v_pk_fma_f32 v[112:113], v[112:113], v[118:119], v[122:123]
	v_pk_add_f32 v[118:119], v[124:125], v[122:123] neg_lo:[0,1] neg_hi:[0,1]
	s_nop 0
	v_pk_fma_f32 v[112:113], v[118:119], v[128:129], v[112:113]
	s_and_saveexec_b64 s[2:3], vcc
	s_xor_b64 s[22:23], exec, s[2:3]
	s_cbranch_execz .LBB0_2795
	v_cmp_lt_u32_e32 vcc, s77, v130
	s_and_saveexec_b64 s[2:3], vcc
	s_xor_b64 s[46:47], exec, s[2:3]
	s_cbranch_execz .LBB0_2792
	v_cmp_lt_u32_e32 vcc, s78, v130
	s_and_saveexec_b64 s[2:3], vcc
	s_xor_b64 s[48:49], exec, s[2:3]
	s_cbranch_execz .LBB0_2789
	v_cmp_lt_u32_e32 vcc, s79, v130
	s_and_saveexec_b64 s[2:3], vcc
	s_xor_b64 s[50:51], exec, s[2:3]
	s_cbranch_execz .LBB0_2754
	v_cmp_lt_u32_e32 vcc, s80, v130
	s_and_saveexec_b64 s[52:53], vcc
	s_cbranch_execz .LBB0_2753
	v_mul_f32_e32 v118, 0xbfb8aa3b, v114
	v_rndne_f32_e32 v119, v118
	v_sub_f32_e32 v122, v118, v119
	v_fma_f32 v118, v114, s81, -v118
	v_fmac_f32_e32 v118, 0xb2a5705f, v114
	v_add_f32_e32 v118, v122, v118
	v_exp_f32_e32 v118, v118
	v_cvt_i32_f32_e32 v119, v119
	v_cmp_nlt_f32_e32 vcc, s82, v114
	v_ldexp_f32 v118, v118, v119
	s_nop 0
	v_cndmask_b32_e32 v118, 0, v118, vcc
	v_cmp_ngt_f32_e32 vcc, s83, v114
	s_nop 1
	v_cndmask_b32_e32 v114, v143, v118, vcc
	v_mul_f32_e32 v118, 0xbfb8aa3b, v115
	v_rndne_f32_e32 v119, v118
	v_sub_f32_e32 v122, v118, v119
	v_fma_f32 v118, v115, s81, -v118
	v_fmac_f32_e32 v118, 0xb2a5705f, v115
	v_add_f32_e32 v118, v122, v118
	v_exp_f32_e32 v118, v118
	v_cvt_i32_f32_e32 v119, v119
	v_cmp_nlt_f32_e32 vcc, s82, v115
	v_ldexp_f32 v118, v118, v119
	s_nop 0
	v_cndmask_b32_e32 v118, 0, v118, vcc
	v_cmp_ngt_f32_e32 vcc, s83, v115
	s_nop 1
	v_cndmask_b32_e32 v115, v143, v118, vcc
	v_mul_f32_e32 v118, 0xbfb8aa3b, v110
	v_rndne_f32_e32 v119, v118
	v_sub_f32_e32 v122, v118, v119
	v_fma_f32 v118, v110, s81, -v118
	v_fmac_f32_e32 v118, 0xb2a5705f, v110
	v_add_f32_e32 v118, v122, v118
	v_exp_f32_e32 v118, v118
	v_cvt_i32_f32_e32 v119, v119
	v_cmp_nlt_f32_e32 vcc, s82, v110
	v_pk_add_f32 v[114:115], v[114:115], 1.0 op_sel_hi:[1,0]
	v_ldexp_f32 v118, v118, v119
	v_cndmask_b32_e32 v118, 0, v118, vcc
	v_cmp_ngt_f32_e32 vcc, s83, v110
	s_nop 1
	v_cndmask_b32_e32 v110, v143, v118, vcc
	v_mul_f32_e32 v118, 0xbfb8aa3b, v111
	v_rndne_f32_e32 v119, v118
	v_sub_f32_e32 v122, v118, v119
	v_fma_f32 v118, v111, s81, -v118
	v_fmac_f32_e32 v118, 0xb2a5705f, v111
	v_add_f32_e32 v118, v122, v118
	v_exp_f32_e32 v118, v118
	v_cvt_i32_f32_e32 v119, v119
	v_cmp_nlt_f32_e32 vcc, s82, v111
	v_ldexp_f32 v118, v118, v119
	s_nop 0
	v_cndmask_b32_e32 v118, 0, v118, vcc
	v_cmp_ngt_f32_e32 vcc, s83, v111
	s_nop 1
	v_cndmask_b32_e32 v111, v143, v118, vcc
	v_mul_f32_e32 v118, 0xbfb8aa3b, v116
	v_rndne_f32_e32 v119, v118
	v_sub_f32_e32 v122, v118, v119
	v_fma_f32 v118, v116, s81, -v118
	v_fmac_f32_e32 v118, 0xb2a5705f, v116
	v_add_f32_e32 v118, v122, v118
	v_exp_f32_e32 v118, v118
	v_cvt_i32_f32_e32 v119, v119
	v_cmp_nlt_f32_e32 vcc, s82, v116
	v_pk_add_f32 v[110:111], v[110:111], 1.0 op_sel_hi:[1,0]
	v_ldexp_f32 v118, v118, v119
	v_cndmask_b32_e32 v118, 0, v118, vcc
	v_cmp_ngt_f32_e32 vcc, s83, v116
	s_nop 1
	v_cndmask_b32_e32 v116, v143, v118, vcc
	v_mul_f32_e32 v118, 0xbfb8aa3b, v117
	v_rndne_f32_e32 v119, v118
	v_sub_f32_e32 v122, v118, v119
	v_fma_f32 v118, v117, s81, -v118
	v_fmac_f32_e32 v118, 0xb2a5705f, v117
	v_add_f32_e32 v118, v122, v118
	v_exp_f32_e32 v118, v118
	v_cvt_i32_f32_e32 v119, v119
	v_cmp_nlt_f32_e32 vcc, s82, v117
	v_ldexp_f32 v118, v118, v119
	s_nop 0
	v_cndmask_b32_e32 v118, 0, v118, vcc
	v_cmp_ngt_f32_e32 vcc, s83, v117
	s_nop 1
	v_cndmask_b32_e32 v117, v143, v118, vcc
	v_mul_f32_e32 v118, 0xbfb8aa3b, v112
	v_rndne_f32_e32 v119, v118
	v_sub_f32_e32 v122, v118, v119
	v_fma_f32 v118, v112, s81, -v118
	v_fmac_f32_e32 v118, 0xb2a5705f, v112
	v_add_f32_e32 v118, v122, v118
	v_exp_f32_e32 v118, v118
	v_cvt_i32_f32_e32 v119, v119
	v_cmp_nlt_f32_e32 vcc, s82, v112
	v_pk_add_f32 v[116:117], v[116:117], 1.0 op_sel_hi:[1,0]
	v_ldexp_f32 v118, v118, v119
	v_cndmask_b32_e32 v118, 0, v118, vcc
	v_cmp_ngt_f32_e32 vcc, s83, v112
	s_nop 1
	v_cndmask_b32_e32 v112, v143, v118, vcc
	v_mul_f32_e32 v118, 0xbfb8aa3b, v113
	v_rndne_f32_e32 v119, v118
	v_sub_f32_e32 v122, v118, v119
	v_fma_f32 v118, v113, s81, -v118
	v_fmac_f32_e32 v118, 0xb2a5705f, v113
	v_add_f32_e32 v118, v122, v118
	v_exp_f32_e32 v118, v118
	v_cvt_i32_f32_e32 v119, v119
	v_cmp_nlt_f32_e32 vcc, s82, v113
	v_ldexp_f32 v118, v118, v119
	s_nop 0
	v_cndmask_b32_e32 v118, 0, v118, vcc
	v_cmp_ngt_f32_e32 vcc, s83, v113
	s_nop 1
	v_cndmask_b32_e32 v113, v143, v118, vcc
	v_div_scale_f32 v118, s[2:3], v114, v114, 1.0
	v_rcp_f32_e32 v119, v118
	v_pk_add_f32 v[112:113], v[112:113], 1.0 op_sel_hi:[1,0]
	v_fma_f32 v122, -v118, v119, 1.0
	v_fmac_f32_e32 v119, v122, v119
	v_div_scale_f32 v122, vcc, 1.0, v114, 1.0
	v_mul_f32_e32 v123, v122, v119
	v_fma_f32 v124, -v118, v123, v122
	v_fmac_f32_e32 v123, v124, v119
	v_fma_f32 v118, -v118, v123, v122
	v_div_fmas_f32 v118, v118, v119, v123
	v_div_fixup_f32 v114, v118, v114, 1.0
	v_rcp_f32_e32 v115, v115
	s_nop 3
	v_rcp_f32_e32 v110, v110
	s_nop 3
	v_rcp_f32_e32 v111, v111
	s_nop 3
	v_rcp_f32_e32 v116, v116
	s_nop 3
	v_rcp_f32_e32 v117, v117
	s_nop 3
	v_rcp_f32_e32 v112, v112
	s_nop 3
	v_div_scale_f32 v118, s[2:3], v113, v113, 1.0
	v_rcp_f32_e32 v119, v118
	s_nop 0
	v_fma_f32 v122, -v118, v119, 1.0
	v_fmac_f32_e32 v119, v122, v119
	v_div_scale_f32 v122, vcc, 1.0, v113, 1.0
	v_mul_f32_e32 v123, v122, v119
	v_fma_f32 v124, -v118, v123, v122
	v_fmac_f32_e32 v123, v124, v119
	v_fma_f32 v118, -v118, v123, v122
	v_div_fmas_f32 v118, v118, v119, v123
	v_div_fixup_f32 v113, v118, v113, 1.0

.LBB0_2798:
	v_add_u32_e32 v130, v120, v162
	v_lshlrev_b64 v[110:111], 2, v[130:131]
	v_lshl_add_u64 v[118:119], s[28:29], 0, v[110:111]
	global_load_dwordx4 v[112:115], v[118:119], off offset:16
	global_load_dwordx4 v[122:125], v[118:119], off
	v_lshl_add_u64 v[110:111], s[36:37], 0, v[110:111]
	v_lshrrev_b32_e32 v116, 2, v163
	global_load_dwordx4 v[126:129], v[110:111], off offset:16
	global_load_dwordx4 v[162:165], v[110:111], off
	v_lshlrev_b32_e32 v110, 16, v6
	v_and_b32_e32 v111, 0xffff0000, v6
	v_lshlrev_b32_e32 v118, 16, v106
	v_and_b32_e32 v119, 0xffff0000, v106
	v_lshlrev_b32_e32 v132, 16, v34
	v_and_b32_e32 v133, 0xffff0000, v34
	v_pk_add_f32 v[118:119], v[118:119], v[110:111] neg_lo:[0,1] neg_hi:[0,1]
	v_lshlrev_b32_e32 v106, 16, v107
	v_and_b32_e32 v107, 0xffff0000, v107
	v_cmp_lt_u32_e32 vcc, s76, v130
	s_waitcnt vmcnt(2)
	v_pk_fma_f32 v[118:119], v[118:119], v[122:123], v[110:111]
	v_pk_add_f32 v[110:111], v[132:133], v[110:111] neg_lo:[0,1] neg_hi:[0,1]
	v_lshlrev_b32_e32 v122, 16, v35
	s_waitcnt vmcnt(0)
	v_pk_fma_f32 v[110:111], v[110:111], v[162:163], v[118:119]
	v_lshlrev_b32_e32 v118, 16, v7
	v_and_b32_e32 v119, 0xffff0000, v7
	v_and_b32_e32 v123, 0xffff0000, v35
	v_pk_add_f32 v[106:107], v[106:107], v[118:119] neg_lo:[0,1] neg_hi:[0,1]
	s_nop 0
	v_pk_fma_f32 v[106:107], v[106:107], v[124:125], v[118:119]
	v_pk_add_f32 v[118:119], v[122:123], v[118:119] neg_lo:[0,1] neg_hi:[0,1]
	v_lshlrev_b32_e32 v122, 16, v108
	v_pk_fma_f32 v[106:107], v[118:119], v[164:165], v[106:107]
	v_lshlrev_b32_e32 v118, 16, v8
	v_and_b32_e32 v119, 0xffff0000, v8
	v_and_b32_e32 v123, 0xffff0000, v108
	v_lshlrev_b32_e32 v124, 16, v36
	v_and_b32_e32 v125, 0xffff0000, v36
	v_pk_add_f32 v[122:123], v[122:123], v[118:119] neg_lo:[0,1] neg_hi:[0,1]
	v_lshlrev_b32_e32 v108, 16, v109
	v_pk_fma_f32 v[112:113], v[122:123], v[112:113], v[118:119]
	v_pk_add_f32 v[118:119], v[124:125], v[118:119] neg_lo:[0,1] neg_hi:[0,1]
	v_and_b32_e32 v109, 0xffff0000, v109
	v_pk_fma_f32 v[112:113], v[118:119], v[126:127], v[112:113]
	v_lshlrev_b32_e32 v118, 16, v9
	v_and_b32_e32 v119, 0xffff0000, v9
	v_lshlrev_b32_e32 v122, 16, v37
	v_and_b32_e32 v123, 0xffff0000, v37
	v_pk_add_f32 v[108:109], v[108:109], v[118:119] neg_lo:[0,1] neg_hi:[0,1]
	s_nop 0
	v_pk_fma_f32 v[108:109], v[108:109], v[114:115], v[118:119]
	v_pk_add_f32 v[114:115], v[122:123], v[118:119] neg_lo:[0,1] neg_hi:[0,1]
	s_nop 0
	v_pk_fma_f32 v[108:109], v[114:115], v[128:129], v[108:109]
	s_and_saveexec_b64 s[2:3], vcc
	s_xor_b64 s[20:21], exec, s[2:3]
	s_cbranch_execz .LBB0_2846
	v_cmp_lt_u32_e32 vcc, s77, v130
	s_and_saveexec_b64 s[2:3], vcc
	s_xor_b64 s[22:23], exec, s[2:3]
	s_cbranch_execz .LBB0_2843
	v_cmp_lt_u32_e32 vcc, s78, v130
	s_and_saveexec_b64 s[2:3], vcc
	s_xor_b64 s[46:47], exec, s[2:3]
	s_cbranch_execz .LBB0_2840
	v_cmp_lt_u32_e32 vcc, s79, v130
	s_and_saveexec_b64 s[2:3], vcc
	s_xor_b64 s[48:49], exec, s[2:3]
	s_cbranch_execz .LBB0_2805
	v_cmp_lt_u32_e32 vcc, s80, v130
	s_and_saveexec_b64 s[50:51], vcc
	s_cbranch_execz .LBB0_2804
	v_mul_f32_e32 v114, 0xbfb8aa3b, v110
	v_rndne_f32_e32 v115, v114
	v_sub_f32_e32 v117, v114, v115
	v_fma_f32 v114, v110, s81, -v114
	v_fmac_f32_e32 v114, 0xb2a5705f, v110
	v_add_f32_e32 v114, v117, v114
	v_exp_f32_e32 v114, v114
	v_cvt_i32_f32_e32 v115, v115
	v_cmp_nlt_f32_e32 vcc, s82, v110
	v_ldexp_f32 v114, v114, v115
	s_nop 0
	v_cndmask_b32_e32 v114, 0, v114, vcc
	v_cmp_ngt_f32_e32 vcc, s83, v110
	s_nop 1
	v_cndmask_b32_e32 v110, v143, v114, vcc
	v_mul_f32_e32 v114, 0xbfb8aa3b, v111
	v_rndne_f32_e32 v115, v114
	v_sub_f32_e32 v117, v114, v115
	v_fma_f32 v114, v111, s81, -v114
	v_fmac_f32_e32 v114, 0xb2a5705f, v111
	v_add_f32_e32 v114, v117, v114
	v_exp_f32_e32 v114, v114
	v_cvt_i32_f32_e32 v115, v115
	v_cmp_nlt_f32_e32 vcc, s82, v111
	v_ldexp_f32 v114, v114, v115
	s_nop 0
	v_cndmask_b32_e32 v114, 0, v114, vcc
	v_cmp_ngt_f32_e32 vcc, s83, v111
	s_nop 1
	v_cndmask_b32_e32 v111, v143, v114, vcc
	v_mul_f32_e32 v114, 0xbfb8aa3b, v106
	v_rndne_f32_e32 v115, v114
	v_sub_f32_e32 v117, v114, v115
	v_fma_f32 v114, v106, s81, -v114
	v_fmac_f32_e32 v114, 0xb2a5705f, v106
	v_add_f32_e32 v114, v117, v114
	v_exp_f32_e32 v114, v114
	v_cvt_i32_f32_e32 v115, v115
	v_cmp_nlt_f32_e32 vcc, s82, v106
	v_pk_add_f32 v[110:111], v[110:111], 1.0 op_sel_hi:[1,0]
	v_ldexp_f32 v114, v114, v115
	v_cndmask_b32_e32 v114, 0, v114, vcc
	v_cmp_ngt_f32_e32 vcc, s83, v106
	s_nop 1
	v_cndmask_b32_e32 v106, v143, v114, vcc
	v_mul_f32_e32 v114, 0xbfb8aa3b, v107
	v_rndne_f32_e32 v115, v114
	v_sub_f32_e32 v117, v114, v115
	v_fma_f32 v114, v107, s81, -v114
	v_fmac_f32_e32 v114, 0xb2a5705f, v107
	v_add_f32_e32 v114, v117, v114
	v_exp_f32_e32 v114, v114
	v_cvt_i32_f32_e32 v115, v115
	v_cmp_nlt_f32_e32 vcc, s82, v107
	v_ldexp_f32 v114, v114, v115
	s_nop 0
	v_cndmask_b32_e32 v114, 0, v114, vcc
	v_cmp_ngt_f32_e32 vcc, s83, v107
	s_nop 1
	v_cndmask_b32_e32 v107, v143, v114, vcc
	v_mul_f32_e32 v114, 0xbfb8aa3b, v112
	v_rndne_f32_e32 v115, v114
	v_sub_f32_e32 v117, v114, v115
	v_fma_f32 v114, v112, s81, -v114
	v_fmac_f32_e32 v114, 0xb2a5705f, v112
	v_add_f32_e32 v114, v117, v114
	v_exp_f32_e32 v114, v114
	v_cvt_i32_f32_e32 v115, v115
	v_cmp_nlt_f32_e32 vcc, s82, v112
	v_pk_add_f32 v[106:107], v[106:107], 1.0 op_sel_hi:[1,0]
	v_ldexp_f32 v114, v114, v115
	v_cndmask_b32_e32 v114, 0, v114, vcc
	v_cmp_ngt_f32_e32 vcc, s83, v112
	s_nop 1
	v_cndmask_b32_e32 v112, v143, v114, vcc
	v_mul_f32_e32 v114, 0xbfb8aa3b, v113
	v_rndne_f32_e32 v115, v114
	v_sub_f32_e32 v117, v114, v115
	v_fma_f32 v114, v113, s81, -v114
	v_fmac_f32_e32 v114, 0xb2a5705f, v113
	v_add_f32_e32 v114, v117, v114
	v_exp_f32_e32 v114, v114
	v_cvt_i32_f32_e32 v115, v115
	v_cmp_nlt_f32_e32 vcc, s82, v113
	v_ldexp_f32 v114, v114, v115
	s_nop 0
	v_cndmask_b32_e32 v114, 0, v114, vcc
	v_cmp_ngt_f32_e32 vcc, s83, v113
	s_nop 1
	v_cndmask_b32_e32 v113, v143, v114, vcc
	v_mul_f32_e32 v114, 0xbfb8aa3b, v108
	v_rndne_f32_e32 v115, v114
	v_sub_f32_e32 v117, v114, v115
	v_fma_f32 v114, v108, s81, -v114
	v_fmac_f32_e32 v114, 0xb2a5705f, v108
	v_add_f32_e32 v114, v117, v114
	v_exp_f32_e32 v114, v114
	v_cvt_i32_f32_e32 v115, v115
	v_cmp_nlt_f32_e32 vcc, s82, v108
	v_pk_add_f32 v[112:113], v[112:113], 1.0 op_sel_hi:[1,0]
	v_ldexp_f32 v114, v114, v115
	v_cndmask_b32_e32 v114, 0, v114, vcc
	v_cmp_ngt_f32_e32 vcc, s83, v108
	s_nop 1
	v_cndmask_b32_e32 v108, v143, v114, vcc
	v_mul_f32_e32 v114, 0xbfb8aa3b, v109
	v_rndne_f32_e32 v115, v114
	v_sub_f32_e32 v117, v114, v115
	v_fma_f32 v114, v109, s81, -v114
	v_fmac_f32_e32 v114, 0xb2a5705f, v109
	v_add_f32_e32 v114, v117, v114
	v_exp_f32_e32 v114, v114
	v_cvt_i32_f32_e32 v115, v115
	v_cmp_nlt_f32_e32 vcc, s82, v109
	v_ldexp_f32 v114, v114, v115
	s_nop 0
	v_cndmask_b32_e32 v114, 0, v114, vcc
	v_cmp_ngt_f32_e32 vcc, s83, v109
	s_nop 1
	v_cndmask_b32_e32 v109, v143, v114, vcc
	v_div_scale_f32 v114, s[2:3], v110, v110, 1.0
	v_rcp_f32_e32 v115, v114
	v_pk_add_f32 v[108:109], v[108:109], 1.0 op_sel_hi:[1,0]
	v_fma_f32 v117, -v114, v115, 1.0
	v_fmac_f32_e32 v115, v117, v115
	v_div_scale_f32 v117, vcc, 1.0, v110, 1.0
	v_mul_f32_e32 v118, v117, v115
	v_fma_f32 v119, -v114, v118, v117
	v_fmac_f32_e32 v118, v119, v115
	v_fma_f32 v114, -v114, v118, v117
	v_div_fmas_f32 v114, v114, v115, v118
	v_div_fixup_f32 v110, v114, v110, 1.0
	v_rcp_f32_e32 v111, v111
	s_nop 3
	v_rcp_f32_e32 v106, v106
	s_nop 3
	v_rcp_f32_e32 v107, v107
	s_nop 3
	v_rcp_f32_e32 v112, v112
	s_nop 3
	v_rcp_f32_e32 v113, v113
	s_nop 3
	v_rcp_f32_e32 v108, v108
	s_nop 3
	v_div_scale_f32 v114, s[2:3], v109, v109, 1.0
	v_rcp_f32_e32 v115, v114
	s_nop 0
	v_fma_f32 v117, -v114, v115, 1.0
	v_fmac_f32_e32 v115, v117, v115
	v_div_scale_f32 v117, vcc, 1.0, v109, 1.0
	v_mul_f32_e32 v118, v117, v115
	v_fma_f32 v119, -v114, v118, v117
	v_fmac_f32_e32 v118, v119, v115
	v_fma_f32 v114, -v114, v118, v117
	v_div_fmas_f32 v114, v114, v115, v118
	v_div_fixup_f32 v109, v114, v109, 1.0

.LBB0_2849:
	v_add_u32_e32 v130, v120, v159
	v_lshlrev_b64 v[106:107], 2, v[130:131]
	v_lshl_add_u64 v[114:115], s[28:29], 0, v[106:107]
	global_load_dwordx4 v[108:111], v[114:115], off offset:16
	s_nop 0
	global_load_dwordx4 v[114:117], v[114:115], off
	v_lshl_add_u64 v[106:107], s[36:37], 0, v[106:107]
	global_load_dwordx4 v[122:125], v[106:107], off offset:16
	global_load_dwordx4 v[126:129], v[106:107], off
	v_lshlrev_b32_e32 v106, 16, v2
	v_and_b32_e32 v107, 0xffff0000, v2
	v_lshlrev_b32_e32 v118, 16, v102
	v_and_b32_e32 v119, 0xffff0000, v102
	v_lshlrev_b32_e32 v132, 16, v30
	v_and_b32_e32 v133, 0xffff0000, v30
	v_pk_add_f32 v[118:119], v[118:119], v[106:107] neg_lo:[0,1] neg_hi:[0,1]
	v_lshlrev_b32_e32 v102, 16, v103
	v_and_b32_e32 v103, 0xffff0000, v103
	v_lshrrev_b32_e32 v112, 2, v160
	v_cmp_lt_u32_e32 vcc, s76, v130
	s_waitcnt vmcnt(2)
	v_pk_fma_f32 v[114:115], v[118:119], v[114:115], v[106:107]
	v_pk_add_f32 v[106:107], v[132:133], v[106:107] neg_lo:[0,1] neg_hi:[0,1]
	v_lshlrev_b32_e32 v118, 16, v31
	s_waitcnt vmcnt(0)
	v_pk_fma_f32 v[106:107], v[106:107], v[126:127], v[114:115]
	v_lshlrev_b32_e32 v114, 16, v3
	v_and_b32_e32 v115, 0xffff0000, v3
	v_and_b32_e32 v119, 0xffff0000, v31
	v_pk_add_f32 v[102:103], v[102:103], v[114:115] neg_lo:[0,1] neg_hi:[0,1]
	s_nop 0
	v_pk_fma_f32 v[102:103], v[102:103], v[116:117], v[114:115]
	v_pk_add_f32 v[114:115], v[118:119], v[114:115] neg_lo:[0,1] neg_hi:[0,1]
	v_lshlrev_b32_e32 v116, 16, v104
	v_pk_fma_f32 v[102:103], v[114:115], v[128:129], v[102:103]
	v_lshlrev_b32_e32 v114, 16, v4
	v_and_b32_e32 v115, 0xffff0000, v4
	v_and_b32_e32 v117, 0xffff0000, v104
	v_lshlrev_b32_e32 v118, 16, v32
	v_and_b32_e32 v119, 0xffff0000, v32
	v_pk_add_f32 v[116:117], v[116:117], v[114:115] neg_lo:[0,1] neg_hi:[0,1]
	v_lshlrev_b32_e32 v104, 16, v105
	v_pk_fma_f32 v[108:109], v[116:117], v[108:109], v[114:115]
	v_pk_add_f32 v[114:115], v[118:119], v[114:115] neg_lo:[0,1] neg_hi:[0,1]
	v_and_b32_e32 v105, 0xffff0000, v105
	v_pk_fma_f32 v[108:109], v[114:115], v[122:123], v[108:109]
	v_lshlrev_b32_e32 v114, 16, v5
	v_and_b32_e32 v115, 0xffff0000, v5
	v_lshlrev_b32_e32 v116, 16, v33
	v_and_b32_e32 v117, 0xffff0000, v33
	v_pk_add_f32 v[104:105], v[104:105], v[114:115] neg_lo:[0,1] neg_hi:[0,1]
	s_nop 0
	v_pk_fma_f32 v[104:105], v[104:105], v[110:111], v[114:115]
	v_pk_add_f32 v[110:111], v[116:117], v[114:115] neg_lo:[0,1] neg_hi:[0,1]
	s_nop 0
	v_pk_fma_f32 v[104:105], v[110:111], v[124:125], v[104:105]
	s_and_saveexec_b64 s[2:3], vcc
	s_xor_b64 s[18:19], exec, s[2:3]
	s_cbranch_execz .LBB0_2897
	v_cmp_lt_u32_e32 vcc, s77, v130
	s_and_saveexec_b64 s[2:3], vcc
	s_xor_b64 s[20:21], exec, s[2:3]
	s_cbranch_execz .LBB0_2894
	v_cmp_lt_u32_e32 vcc, s78, v130
	s_and_saveexec_b64 s[2:3], vcc
	s_xor_b64 s[22:23], exec, s[2:3]
	s_cbranch_execz .LBB0_2891
	v_cmp_lt_u32_e32 vcc, s79, v130
	s_and_saveexec_b64 s[2:3], vcc
	s_xor_b64 s[46:47], exec, s[2:3]
	s_cbranch_execz .LBB0_2856
	v_cmp_lt_u32_e32 vcc, s80, v130
	s_and_saveexec_b64 s[48:49], vcc
	s_cbranch_execz .LBB0_2855
	v_mul_f32_e32 v110, 0xbfb8aa3b, v106
	v_rndne_f32_e32 v111, v110
	v_sub_f32_e32 v113, v110, v111
	v_fma_f32 v110, v106, s81, -v110
	v_fmac_f32_e32 v110, 0xb2a5705f, v106
	v_add_f32_e32 v110, v113, v110
	v_exp_f32_e32 v110, v110
	v_cvt_i32_f32_e32 v111, v111
	v_cmp_nlt_f32_e32 vcc, s82, v106
	v_ldexp_f32 v110, v110, v111
	s_nop 0
	v_cndmask_b32_e32 v110, 0, v110, vcc
	v_cmp_ngt_f32_e32 vcc, s83, v106
	s_nop 1
	v_cndmask_b32_e32 v106, v143, v110, vcc
	v_mul_f32_e32 v110, 0xbfb8aa3b, v107
	v_rndne_f32_e32 v111, v110
	v_sub_f32_e32 v113, v110, v111
	v_fma_f32 v110, v107, s81, -v110
	v_fmac_f32_e32 v110, 0xb2a5705f, v107
	v_add_f32_e32 v110, v113, v110
	v_exp_f32_e32 v110, v110
	v_cvt_i32_f32_e32 v111, v111
	v_cmp_nlt_f32_e32 vcc, s82, v107
	v_ldexp_f32 v110, v110, v111
	s_nop 0
	v_cndmask_b32_e32 v110, 0, v110, vcc
	v_cmp_ngt_f32_e32 vcc, s83, v107
	s_nop 1
	v_cndmask_b32_e32 v107, v143, v110, vcc
	v_mul_f32_e32 v110, 0xbfb8aa3b, v102
	v_rndne_f32_e32 v111, v110
	v_sub_f32_e32 v113, v110, v111
	v_fma_f32 v110, v102, s81, -v110
	v_fmac_f32_e32 v110, 0xb2a5705f, v102
	v_add_f32_e32 v110, v113, v110
	v_exp_f32_e32 v110, v110
	v_cvt_i32_f32_e32 v111, v111
	v_cmp_nlt_f32_e32 vcc, s82, v102
	v_pk_add_f32 v[106:107], v[106:107], 1.0 op_sel_hi:[1,0]
	v_ldexp_f32 v110, v110, v111
	v_cndmask_b32_e32 v110, 0, v110, vcc
	v_cmp_ngt_f32_e32 vcc, s83, v102
	s_nop 1
	v_cndmask_b32_e32 v102, v143, v110, vcc
	v_mul_f32_e32 v110, 0xbfb8aa3b, v103
	v_rndne_f32_e32 v111, v110
	v_sub_f32_e32 v113, v110, v111
	v_fma_f32 v110, v103, s81, -v110
	v_fmac_f32_e32 v110, 0xb2a5705f, v103
	v_add_f32_e32 v110, v113, v110
	v_exp_f32_e32 v110, v110
	v_cvt_i32_f32_e32 v111, v111
	v_cmp_nlt_f32_e32 vcc, s82, v103
	v_ldexp_f32 v110, v110, v111
	s_nop 0
	v_cndmask_b32_e32 v110, 0, v110, vcc
	v_cmp_ngt_f32_e32 vcc, s83, v103
	s_nop 1
	v_cndmask_b32_e32 v103, v143, v110, vcc
	v_mul_f32_e32 v110, 0xbfb8aa3b, v108
	v_rndne_f32_e32 v111, v110
	v_sub_f32_e32 v113, v110, v111
	v_fma_f32 v110, v108, s81, -v110
	v_fmac_f32_e32 v110, 0xb2a5705f, v108
	v_add_f32_e32 v110, v113, v110
	v_exp_f32_e32 v110, v110
	v_cvt_i32_f32_e32 v111, v111
	v_cmp_nlt_f32_e32 vcc, s82, v108
	v_pk_add_f32 v[102:103], v[102:103], 1.0 op_sel_hi:[1,0]
	v_ldexp_f32 v110, v110, v111
	v_cndmask_b32_e32 v110, 0, v110, vcc
	v_cmp_ngt_f32_e32 vcc, s83, v108
	s_nop 1
	v_cndmask_b32_e32 v108, v143, v110, vcc
	v_mul_f32_e32 v110, 0xbfb8aa3b, v109
	v_rndne_f32_e32 v111, v110
	v_sub_f32_e32 v113, v110, v111
	v_fma_f32 v110, v109, s81, -v110
	v_fmac_f32_e32 v110, 0xb2a5705f, v109
	v_add_f32_e32 v110, v113, v110
	v_exp_f32_e32 v110, v110
	v_cvt_i32_f32_e32 v111, v111
	v_cmp_nlt_f32_e32 vcc, s82, v109
	v_ldexp_f32 v110, v110, v111
	s_nop 0
	v_cndmask_b32_e32 v110, 0, v110, vcc
	v_cmp_ngt_f32_e32 vcc, s83, v109
	s_nop 1
	v_cndmask_b32_e32 v109, v143, v110, vcc
	v_mul_f32_e32 v110, 0xbfb8aa3b, v104
	v_rndne_f32_e32 v111, v110
	v_sub_f32_e32 v113, v110, v111
	v_fma_f32 v110, v104, s81, -v110
	v_fmac_f32_e32 v110, 0xb2a5705f, v104
	v_add_f32_e32 v110, v113, v110
	v_exp_f32_e32 v110, v110
	v_cvt_i32_f32_e32 v111, v111
	v_cmp_nlt_f32_e32 vcc, s82, v104
	v_pk_add_f32 v[108:109], v[108:109], 1.0 op_sel_hi:[1,0]
	v_ldexp_f32 v110, v110, v111
	v_cndmask_b32_e32 v110, 0, v110, vcc
	v_cmp_ngt_f32_e32 vcc, s83, v104
	s_nop 1
	v_cndmask_b32_e32 v104, v143, v110, vcc
	v_mul_f32_e32 v110, 0xbfb8aa3b, v105
	v_rndne_f32_e32 v111, v110
	v_sub_f32_e32 v113, v110, v111
	v_fma_f32 v110, v105, s81, -v110
	v_fmac_f32_e32 v110, 0xb2a5705f, v105
	v_add_f32_e32 v110, v113, v110
	v_exp_f32_e32 v110, v110
	v_cvt_i32_f32_e32 v111, v111
	v_cmp_nlt_f32_e32 vcc, s82, v105
	v_ldexp_f32 v110, v110, v111
	s_nop 0
	v_cndmask_b32_e32 v110, 0, v110, vcc
	v_cmp_ngt_f32_e32 vcc, s83, v105
	s_nop 1
	v_cndmask_b32_e32 v105, v143, v110, vcc
	v_div_scale_f32 v110, s[2:3], v106, v106, 1.0
	v_rcp_f32_e32 v111, v110
	v_pk_add_f32 v[104:105], v[104:105], 1.0 op_sel_hi:[1,0]
	v_fma_f32 v113, -v110, v111, 1.0
	v_fmac_f32_e32 v111, v113, v111
	v_div_scale_f32 v113, vcc, 1.0, v106, 1.0
	v_mul_f32_e32 v114, v113, v111
	v_fma_f32 v115, -v110, v114, v113
	v_fmac_f32_e32 v114, v115, v111
	v_fma_f32 v110, -v110, v114, v113
	v_div_fmas_f32 v110, v110, v111, v114
	v_div_fixup_f32 v106, v110, v106, 1.0
	v_rcp_f32_e32 v107, v107
	s_nop 3
	v_rcp_f32_e32 v102, v102
	s_nop 3
	v_rcp_f32_e32 v103, v103
	s_nop 3
	v_rcp_f32_e32 v108, v108
	s_nop 3
	v_rcp_f32_e32 v109, v109
	s_nop 3
	v_rcp_f32_e32 v104, v104
	s_nop 3
	v_div_scale_f32 v110, s[2:3], v105, v105, 1.0
	v_rcp_f32_e32 v111, v110
	s_nop 0
	v_fma_f32 v113, -v110, v111, 1.0
	v_fmac_f32_e32 v111, v113, v111
	v_div_scale_f32 v113, vcc, 1.0, v105, 1.0
	v_mul_f32_e32 v114, v113, v111
	v_fma_f32 v115, -v110, v114, v113
	v_fmac_f32_e32 v114, v115, v111
	v_fma_f32 v110, -v110, v114, v113
	v_div_fmas_f32 v110, v110, v111, v114
	v_div_fixup_f32 v105, v110, v105, 1.0

.LBB0_2900:
	v_add_u32_e32 v130, v120, v156
	v_lshlrev_b64 v[102:103], 2, v[130:131]
	v_lshl_add_u64 v[110:111], s[28:29], 0, v[102:103]
	global_load_dwordx4 v[104:107], v[110:111], off offset:16
	s_nop 0
	global_load_dwordx4 v[110:113], v[110:111], off
	v_lshl_add_u64 v[102:103], s[36:37], 0, v[102:103]
	global_load_dwordx4 v[114:117], v[102:103], off offset:16
	global_load_dwordx4 v[122:125], v[102:103], off
	v_lshlrev_b32_e32 v102, 16, v14
	v_and_b32_e32 v103, 0xffff0000, v14
	v_lshlrev_b32_e32 v118, 16, v98
	v_and_b32_e32 v119, 0xffff0000, v98
	v_lshlrev_b32_e32 v126, 16, v46
	v_and_b32_e32 v127, 0xffff0000, v46
	v_pk_add_f32 v[118:119], v[118:119], v[102:103] neg_lo:[0,1] neg_hi:[0,1]
	v_lshlrev_b32_e32 v98, 16, v99
	v_and_b32_e32 v99, 0xffff0000, v99
	v_lshrrev_b32_e32 v108, 2, v157
	v_cmp_lt_u32_e32 vcc, s76, v130
	s_waitcnt vmcnt(2)
	v_pk_fma_f32 v[110:111], v[118:119], v[110:111], v[102:103]
	v_pk_add_f32 v[102:103], v[126:127], v[102:103] neg_lo:[0,1] neg_hi:[0,1]
	v_lshlrev_b32_e32 v118, 16, v47
	s_waitcnt vmcnt(0)
	v_pk_fma_f32 v[102:103], v[102:103], v[122:123], v[110:111]
	v_lshlrev_b32_e32 v110, 16, v15
	v_and_b32_e32 v111, 0xffff0000, v15
	v_and_b32_e32 v119, 0xffff0000, v47
	v_pk_add_f32 v[98:99], v[98:99], v[110:111] neg_lo:[0,1] neg_hi:[0,1]
	s_nop 0
	v_pk_fma_f32 v[98:99], v[98:99], v[112:113], v[110:111]
	v_pk_add_f32 v[110:111], v[118:119], v[110:111] neg_lo:[0,1] neg_hi:[0,1]
	v_lshlrev_b32_e32 v112, 16, v100
	v_pk_fma_f32 v[98:99], v[110:111], v[124:125], v[98:99]
	v_lshlrev_b32_e32 v110, 16, v16
	v_and_b32_e32 v111, 0xffff0000, v16
	v_and_b32_e32 v113, 0xffff0000, v100
	v_lshlrev_b32_e32 v118, 16, v48
	v_and_b32_e32 v119, 0xffff0000, v48
	v_pk_add_f32 v[112:113], v[112:113], v[110:111] neg_lo:[0,1] neg_hi:[0,1]
	v_lshlrev_b32_e32 v100, 16, v101
	v_pk_fma_f32 v[104:105], v[112:113], v[104:105], v[110:111]
	v_pk_add_f32 v[110:111], v[118:119], v[110:111] neg_lo:[0,1] neg_hi:[0,1]
	v_and_b32_e32 v101, 0xffff0000, v101
	v_pk_fma_f32 v[104:105], v[110:111], v[114:115], v[104:105]
	v_lshlrev_b32_e32 v110, 16, v17
	v_and_b32_e32 v111, 0xffff0000, v17
	v_lshlrev_b32_e32 v112, 16, v49
	v_and_b32_e32 v113, 0xffff0000, v49
	v_pk_add_f32 v[100:101], v[100:101], v[110:111] neg_lo:[0,1] neg_hi:[0,1]
	s_nop 0
	v_pk_fma_f32 v[100:101], v[100:101], v[106:107], v[110:111]
	v_pk_add_f32 v[106:107], v[112:113], v[110:111] neg_lo:[0,1] neg_hi:[0,1]
	s_nop 0
	v_pk_fma_f32 v[100:101], v[106:107], v[116:117], v[100:101]
	s_and_saveexec_b64 s[2:3], vcc
	s_xor_b64 s[16:17], exec, s[2:3]
	s_cbranch_execz .LBB0_2948
	v_cmp_lt_u32_e32 vcc, s77, v130
	s_and_saveexec_b64 s[2:3], vcc
	s_xor_b64 s[18:19], exec, s[2:3]
	s_cbranch_execz .LBB0_2945
	v_cmp_lt_u32_e32 vcc, s78, v130
	s_and_saveexec_b64 s[2:3], vcc
	s_xor_b64 s[20:21], exec, s[2:3]
	s_cbranch_execz .LBB0_2942
	v_cmp_lt_u32_e32 vcc, s79, v130
	s_and_saveexec_b64 s[2:3], vcc
	s_xor_b64 s[22:23], exec, s[2:3]
	s_cbranch_execz .LBB0_2907
	v_cmp_lt_u32_e32 vcc, s80, v130
	s_and_saveexec_b64 s[46:47], vcc
	s_cbranch_execz .LBB0_2906
	v_mul_f32_e32 v106, 0xbfb8aa3b, v102
	v_rndne_f32_e32 v107, v106
	v_sub_f32_e32 v109, v106, v107
	v_fma_f32 v106, v102, s81, -v106
	v_fmac_f32_e32 v106, 0xb2a5705f, v102
	v_add_f32_e32 v106, v109, v106
	v_exp_f32_e32 v106, v106
	v_cvt_i32_f32_e32 v107, v107
	v_cmp_nlt_f32_e32 vcc, s82, v102
	v_ldexp_f32 v106, v106, v107
	s_nop 0
	v_cndmask_b32_e32 v106, 0, v106, vcc
	v_cmp_ngt_f32_e32 vcc, s83, v102
	s_nop 1
	v_cndmask_b32_e32 v102, v143, v106, vcc
	v_mul_f32_e32 v106, 0xbfb8aa3b, v103
	v_rndne_f32_e32 v107, v106
	v_sub_f32_e32 v109, v106, v107
	v_fma_f32 v106, v103, s81, -v106
	v_fmac_f32_e32 v106, 0xb2a5705f, v103
	v_add_f32_e32 v106, v109, v106
	v_exp_f32_e32 v106, v106
	v_cvt_i32_f32_e32 v107, v107
	v_cmp_nlt_f32_e32 vcc, s82, v103
	v_ldexp_f32 v106, v106, v107
	s_nop 0
	v_cndmask_b32_e32 v106, 0, v106, vcc
	v_cmp_ngt_f32_e32 vcc, s83, v103
	s_nop 1
	v_cndmask_b32_e32 v103, v143, v106, vcc
	v_mul_f32_e32 v106, 0xbfb8aa3b, v98
	v_rndne_f32_e32 v107, v106
	v_sub_f32_e32 v109, v106, v107
	v_fma_f32 v106, v98, s81, -v106
	v_fmac_f32_e32 v106, 0xb2a5705f, v98
	v_add_f32_e32 v106, v109, v106
	v_exp_f32_e32 v106, v106
	v_cvt_i32_f32_e32 v107, v107
	v_cmp_nlt_f32_e32 vcc, s82, v98
	v_pk_add_f32 v[102:103], v[102:103], 1.0 op_sel_hi:[1,0]
	v_ldexp_f32 v106, v106, v107
	v_cndmask_b32_e32 v106, 0, v106, vcc
	v_cmp_ngt_f32_e32 vcc, s83, v98
	s_nop 1
	v_cndmask_b32_e32 v98, v143, v106, vcc
	v_mul_f32_e32 v106, 0xbfb8aa3b, v99
	v_rndne_f32_e32 v107, v106
	v_sub_f32_e32 v109, v106, v107
	v_fma_f32 v106, v99, s81, -v106
	v_fmac_f32_e32 v106, 0xb2a5705f, v99
	v_add_f32_e32 v106, v109, v106
	v_exp_f32_e32 v106, v106
	v_cvt_i32_f32_e32 v107, v107
	v_cmp_nlt_f32_e32 vcc, s82, v99
	v_ldexp_f32 v106, v106, v107
	s_nop 0
	v_cndmask_b32_e32 v106, 0, v106, vcc
	v_cmp_ngt_f32_e32 vcc, s83, v99
	s_nop 1
	v_cndmask_b32_e32 v99, v143, v106, vcc
	v_mul_f32_e32 v106, 0xbfb8aa3b, v104
	v_rndne_f32_e32 v107, v106
	v_sub_f32_e32 v109, v106, v107
	v_fma_f32 v106, v104, s81, -v106
	v_fmac_f32_e32 v106, 0xb2a5705f, v104
	v_add_f32_e32 v106, v109, v106
	v_exp_f32_e32 v106, v106
	v_cvt_i32_f32_e32 v107, v107
	v_cmp_nlt_f32_e32 vcc, s82, v104
	v_pk_add_f32 v[98:99], v[98:99], 1.0 op_sel_hi:[1,0]
	v_ldexp_f32 v106, v106, v107
	v_cndmask_b32_e32 v106, 0, v106, vcc
	v_cmp_ngt_f32_e32 vcc, s83, v104
	s_nop 1
	v_cndmask_b32_e32 v104, v143, v106, vcc
	v_mul_f32_e32 v106, 0xbfb8aa3b, v105
	v_rndne_f32_e32 v107, v106
	v_sub_f32_e32 v109, v106, v107
	v_fma_f32 v106, v105, s81, -v106
	v_fmac_f32_e32 v106, 0xb2a5705f, v105
	v_add_f32_e32 v106, v109, v106
	v_exp_f32_e32 v106, v106
	v_cvt_i32_f32_e32 v107, v107
	v_cmp_nlt_f32_e32 vcc, s82, v105
	v_ldexp_f32 v106, v106, v107
	s_nop 0
	v_cndmask_b32_e32 v106, 0, v106, vcc
	v_cmp_ngt_f32_e32 vcc, s83, v105
	s_nop 1
	v_cndmask_b32_e32 v105, v143, v106, vcc
	v_mul_f32_e32 v106, 0xbfb8aa3b, v100
	v_rndne_f32_e32 v107, v106
	v_sub_f32_e32 v109, v106, v107
	v_fma_f32 v106, v100, s81, -v106
	v_fmac_f32_e32 v106, 0xb2a5705f, v100
	v_add_f32_e32 v106, v109, v106
	v_exp_f32_e32 v106, v106
	v_cvt_i32_f32_e32 v107, v107
	v_cmp_nlt_f32_e32 vcc, s82, v100
	v_pk_add_f32 v[104:105], v[104:105], 1.0 op_sel_hi:[1,0]
	v_ldexp_f32 v106, v106, v107
	v_cndmask_b32_e32 v106, 0, v106, vcc
	v_cmp_ngt_f32_e32 vcc, s83, v100
	s_nop 1
	v_cndmask_b32_e32 v100, v143, v106, vcc
	v_mul_f32_e32 v106, 0xbfb8aa3b, v101
	v_rndne_f32_e32 v107, v106
	v_sub_f32_e32 v109, v106, v107
	v_fma_f32 v106, v101, s81, -v106
	v_fmac_f32_e32 v106, 0xb2a5705f, v101
	v_add_f32_e32 v106, v109, v106
	v_exp_f32_e32 v106, v106
	v_cvt_i32_f32_e32 v107, v107
	v_cmp_nlt_f32_e32 vcc, s82, v101
	v_ldexp_f32 v106, v106, v107
	s_nop 0
	v_cndmask_b32_e32 v106, 0, v106, vcc
	v_cmp_ngt_f32_e32 vcc, s83, v101
	s_nop 1
	v_cndmask_b32_e32 v101, v143, v106, vcc
	v_div_scale_f32 v106, s[2:3], v102, v102, 1.0
	v_rcp_f32_e32 v107, v106
	v_pk_add_f32 v[100:101], v[100:101], 1.0 op_sel_hi:[1,0]
	v_fma_f32 v109, -v106, v107, 1.0
	v_fmac_f32_e32 v107, v109, v107
	v_div_scale_f32 v109, vcc, 1.0, v102, 1.0
	v_mul_f32_e32 v110, v109, v107
	v_fma_f32 v111, -v106, v110, v109
	v_fmac_f32_e32 v110, v111, v107
	v_fma_f32 v106, -v106, v110, v109
	v_div_fmas_f32 v106, v106, v107, v110
	v_div_fixup_f32 v102, v106, v102, 1.0
	v_rcp_f32_e32 v103, v103
	s_nop 3
	v_rcp_f32_e32 v98, v98
	s_nop 3
	v_rcp_f32_e32 v99, v99
	s_nop 3
	v_rcp_f32_e32 v104, v104
	s_nop 3
	v_rcp_f32_e32 v105, v105
	s_nop 3
	v_rcp_f32_e32 v100, v100
	s_nop 3
	v_div_scale_f32 v106, s[2:3], v101, v101, 1.0
	v_rcp_f32_e32 v107, v106
	s_nop 0
	v_fma_f32 v109, -v106, v107, 1.0
	v_fmac_f32_e32 v107, v109, v107
	v_div_scale_f32 v109, vcc, 1.0, v101, 1.0
	v_mul_f32_e32 v110, v109, v107
	v_fma_f32 v111, -v106, v110, v109
	v_fmac_f32_e32 v110, v111, v107
	v_fma_f32 v106, -v106, v110, v109
	v_div_fmas_f32 v106, v106, v107, v110
	v_div_fixup_f32 v101, v106, v101, 1.0

.LBB0_2951:
	v_add_u32_e32 v130, v120, v153
	v_lshlrev_b64 v[98:99], 2, v[130:131]
	v_lshl_add_u64 v[106:107], s[28:29], 0, v[98:99]
	global_load_dwordx4 v[100:103], v[106:107], off offset:16
	s_nop 0
	global_load_dwordx4 v[106:109], v[106:107], off
	v_lshl_add_u64 v[98:99], s[36:37], 0, v[98:99]
	global_load_dwordx4 v[110:113], v[98:99], off offset:16
	global_load_dwordx4 v[114:117], v[98:99], off
	v_lshlrev_b32_e32 v98, 16, v18
	v_and_b32_e32 v99, 0xffff0000, v18
	v_lshlrev_b32_e32 v118, 16, v94
	v_and_b32_e32 v119, 0xffff0000, v94
	v_lshlrev_b32_e32 v122, 16, v54
	v_and_b32_e32 v123, 0xffff0000, v54
	v_pk_add_f32 v[118:119], v[118:119], v[98:99] neg_lo:[0,1] neg_hi:[0,1]
	v_lshlrev_b32_e32 v94, 16, v95
	v_and_b32_e32 v95, 0xffff0000, v95
	v_lshrrev_b32_e32 v104, 2, v154
	v_cmp_lt_u32_e32 vcc, s76, v130
	s_waitcnt vmcnt(2)
	v_pk_fma_f32 v[106:107], v[118:119], v[106:107], v[98:99]
	v_pk_add_f32 v[98:99], v[122:123], v[98:99] neg_lo:[0,1] neg_hi:[0,1]
	s_waitcnt vmcnt(0)
	v_pk_fma_f32 v[98:99], v[98:99], v[114:115], v[106:107]
	v_lshlrev_b32_e32 v106, 16, v19
	v_and_b32_e32 v107, 0xffff0000, v19
	v_lshlrev_b32_e32 v114, 16, v55
	v_and_b32_e32 v115, 0xffff0000, v55
	v_pk_add_f32 v[94:95], v[94:95], v[106:107] neg_lo:[0,1] neg_hi:[0,1]
	s_nop 0
	v_pk_fma_f32 v[94:95], v[94:95], v[108:109], v[106:107]
	v_pk_add_f32 v[106:107], v[114:115], v[106:107] neg_lo:[0,1] neg_hi:[0,1]
	v_lshlrev_b32_e32 v108, 16, v96
	v_pk_fma_f32 v[94:95], v[106:107], v[116:117], v[94:95]
	v_lshlrev_b32_e32 v106, 16, v20
	v_and_b32_e32 v107, 0xffff0000, v20
	v_and_b32_e32 v109, 0xffff0000, v96
	v_lshlrev_b32_e32 v114, 16, v56
	v_and_b32_e32 v115, 0xffff0000, v56
	v_pk_add_f32 v[108:109], v[108:109], v[106:107] neg_lo:[0,1] neg_hi:[0,1]
	v_lshlrev_b32_e32 v96, 16, v97
	v_pk_fma_f32 v[100:101], v[108:109], v[100:101], v[106:107]
	v_pk_add_f32 v[106:107], v[114:115], v[106:107] neg_lo:[0,1] neg_hi:[0,1]
	v_and_b32_e32 v97, 0xffff0000, v97
	v_pk_fma_f32 v[100:101], v[106:107], v[110:111], v[100:101]
	v_lshlrev_b32_e32 v106, 16, v21
	v_and_b32_e32 v107, 0xffff0000, v21
	v_lshlrev_b32_e32 v108, 16, v57
	v_and_b32_e32 v109, 0xffff0000, v57
	v_pk_add_f32 v[96:97], v[96:97], v[106:107] neg_lo:[0,1] neg_hi:[0,1]
	s_nop 0
	v_pk_fma_f32 v[96:97], v[96:97], v[102:103], v[106:107]
	v_pk_add_f32 v[102:103], v[108:109], v[106:107] neg_lo:[0,1] neg_hi:[0,1]
	s_nop 0
	v_pk_fma_f32 v[96:97], v[102:103], v[112:113], v[96:97]
	s_and_saveexec_b64 s[2:3], vcc
	s_xor_b64 s[14:15], exec, s[2:3]
	s_cbranch_execz .LBB0_2999
	v_cmp_lt_u32_e32 vcc, s77, v130
	s_and_saveexec_b64 s[2:3], vcc
	s_xor_b64 s[16:17], exec, s[2:3]
	s_cbranch_execz .LBB0_2996
	v_cmp_lt_u32_e32 vcc, s78, v130
	s_and_saveexec_b64 s[2:3], vcc
	s_xor_b64 s[18:19], exec, s[2:3]
	s_cbranch_execz .LBB0_2993
	v_cmp_lt_u32_e32 vcc, s79, v130
	s_and_saveexec_b64 s[2:3], vcc
	s_xor_b64 s[20:21], exec, s[2:3]
	s_cbranch_execz .LBB0_2958
	v_cmp_lt_u32_e32 vcc, s80, v130
	s_and_saveexec_b64 s[22:23], vcc
	s_cbranch_execz .LBB0_2957
	v_mul_f32_e32 v102, 0xbfb8aa3b, v98
	v_rndne_f32_e32 v103, v102
	v_sub_f32_e32 v105, v102, v103
	v_fma_f32 v102, v98, s81, -v102
	v_fmac_f32_e32 v102, 0xb2a5705f, v98
	v_add_f32_e32 v102, v105, v102
	v_exp_f32_e32 v102, v102
	v_cvt_i32_f32_e32 v103, v103
	v_cmp_nlt_f32_e32 vcc, s82, v98
	v_ldexp_f32 v102, v102, v103
	s_nop 0
	v_cndmask_b32_e32 v102, 0, v102, vcc
	v_cmp_ngt_f32_e32 vcc, s83, v98
	s_nop 1
	v_cndmask_b32_e32 v98, v143, v102, vcc
	v_mul_f32_e32 v102, 0xbfb8aa3b, v99
	v_rndne_f32_e32 v103, v102
	v_sub_f32_e32 v105, v102, v103
	v_fma_f32 v102, v99, s81, -v102
	v_fmac_f32_e32 v102, 0xb2a5705f, v99
	v_add_f32_e32 v102, v105, v102
	v_exp_f32_e32 v102, v102
	v_cvt_i32_f32_e32 v103, v103
	v_cmp_nlt_f32_e32 vcc, s82, v99
	v_ldexp_f32 v102, v102, v103
	s_nop 0
	v_cndmask_b32_e32 v102, 0, v102, vcc
	v_cmp_ngt_f32_e32 vcc, s83, v99
	s_nop 1
	v_cndmask_b32_e32 v99, v143, v102, vcc
	v_mul_f32_e32 v102, 0xbfb8aa3b, v94
	v_rndne_f32_e32 v103, v102
	v_sub_f32_e32 v105, v102, v103
	v_fma_f32 v102, v94, s81, -v102
	v_fmac_f32_e32 v102, 0xb2a5705f, v94
	v_add_f32_e32 v102, v105, v102
	v_exp_f32_e32 v102, v102
	v_cvt_i32_f32_e32 v103, v103
	v_cmp_nlt_f32_e32 vcc, s82, v94
	v_pk_add_f32 v[98:99], v[98:99], 1.0 op_sel_hi:[1,0]
	v_ldexp_f32 v102, v102, v103
	v_cndmask_b32_e32 v102, 0, v102, vcc
	v_cmp_ngt_f32_e32 vcc, s83, v94
	s_nop 1
	v_cndmask_b32_e32 v94, v143, v102, vcc
	v_mul_f32_e32 v102, 0xbfb8aa3b, v95
	v_rndne_f32_e32 v103, v102
	v_sub_f32_e32 v105, v102, v103
	v_fma_f32 v102, v95, s81, -v102
	v_fmac_f32_e32 v102, 0xb2a5705f, v95
	v_add_f32_e32 v102, v105, v102
	v_exp_f32_e32 v102, v102
	v_cvt_i32_f32_e32 v103, v103
	v_cmp_nlt_f32_e32 vcc, s82, v95
	v_ldexp_f32 v102, v102, v103
	s_nop 0
	v_cndmask_b32_e32 v102, 0, v102, vcc
	v_cmp_ngt_f32_e32 vcc, s83, v95
	s_nop 1
	v_cndmask_b32_e32 v95, v143, v102, vcc
	v_mul_f32_e32 v102, 0xbfb8aa3b, v100
	v_rndne_f32_e32 v103, v102
	v_sub_f32_e32 v105, v102, v103
	v_fma_f32 v102, v100, s81, -v102
	v_fmac_f32_e32 v102, 0xb2a5705f, v100
	v_add_f32_e32 v102, v105, v102
	v_exp_f32_e32 v102, v102
	v_cvt_i32_f32_e32 v103, v103
	v_cmp_nlt_f32_e32 vcc, s82, v100
	v_pk_add_f32 v[94:95], v[94:95], 1.0 op_sel_hi:[1,0]
	v_ldexp_f32 v102, v102, v103
	v_cndmask_b32_e32 v102, 0, v102, vcc
	v_cmp_ngt_f32_e32 vcc, s83, v100
	s_nop 1
	v_cndmask_b32_e32 v100, v143, v102, vcc
	v_mul_f32_e32 v102, 0xbfb8aa3b, v101
	v_rndne_f32_e32 v103, v102
	v_sub_f32_e32 v105, v102, v103
	v_fma_f32 v102, v101, s81, -v102
	v_fmac_f32_e32 v102, 0xb2a5705f, v101
	v_add_f32_e32 v102, v105, v102
	v_exp_f32_e32 v102, v102
	v_cvt_i32_f32_e32 v103, v103
	v_cmp_nlt_f32_e32 vcc, s82, v101
	v_ldexp_f32 v102, v102, v103
	s_nop 0
	v_cndmask_b32_e32 v102, 0, v102, vcc
	v_cmp_ngt_f32_e32 vcc, s83, v101
	s_nop 1
	v_cndmask_b32_e32 v101, v143, v102, vcc
	v_mul_f32_e32 v102, 0xbfb8aa3b, v96
	v_rndne_f32_e32 v103, v102
	v_sub_f32_e32 v105, v102, v103
	v_fma_f32 v102, v96, s81, -v102
	v_fmac_f32_e32 v102, 0xb2a5705f, v96
	v_add_f32_e32 v102, v105, v102
	v_exp_f32_e32 v102, v102
	v_cvt_i32_f32_e32 v103, v103
	v_cmp_nlt_f32_e32 vcc, s82, v96
	v_pk_add_f32 v[100:101], v[100:101], 1.0 op_sel_hi:[1,0]
	v_ldexp_f32 v102, v102, v103
	v_cndmask_b32_e32 v102, 0, v102, vcc
	v_cmp_ngt_f32_e32 vcc, s83, v96
	s_nop 1
	v_cndmask_b32_e32 v96, v143, v102, vcc
	v_mul_f32_e32 v102, 0xbfb8aa3b, v97
	v_rndne_f32_e32 v103, v102
	v_sub_f32_e32 v105, v102, v103
	v_fma_f32 v102, v97, s81, -v102
	v_fmac_f32_e32 v102, 0xb2a5705f, v97
	v_add_f32_e32 v102, v105, v102
	v_exp_f32_e32 v102, v102
	v_cvt_i32_f32_e32 v103, v103
	v_cmp_nlt_f32_e32 vcc, s82, v97
	v_ldexp_f32 v102, v102, v103
	s_nop 0
	v_cndmask_b32_e32 v102, 0, v102, vcc
	v_cmp_ngt_f32_e32 vcc, s83, v97
	s_nop 1
	v_cndmask_b32_e32 v97, v143, v102, vcc
	v_div_scale_f32 v102, s[2:3], v98, v98, 1.0
	v_rcp_f32_e32 v103, v102
	v_pk_add_f32 v[96:97], v[96:97], 1.0 op_sel_hi:[1,0]
	v_fma_f32 v105, -v102, v103, 1.0
	v_fmac_f32_e32 v103, v105, v103
	v_div_scale_f32 v105, vcc, 1.0, v98, 1.0
	v_mul_f32_e32 v106, v105, v103
	v_fma_f32 v107, -v102, v106, v105
	v_fmac_f32_e32 v106, v107, v103
	v_fma_f32 v102, -v102, v106, v105
	v_div_fmas_f32 v102, v102, v103, v106
	v_div_fixup_f32 v98, v102, v98, 1.0
	v_rcp_f32_e32 v99, v99
	s_nop 3
	v_rcp_f32_e32 v94, v94
	s_nop 3
	v_rcp_f32_e32 v95, v95
	s_nop 3
	v_rcp_f32_e32 v100, v100
	s_nop 3
	v_rcp_f32_e32 v101, v101
	s_nop 3
	v_rcp_f32_e32 v96, v96
	s_nop 3
	v_div_scale_f32 v102, s[2:3], v97, v97, 1.0
	v_rcp_f32_e32 v103, v102
	s_nop 0
	v_fma_f32 v105, -v102, v103, 1.0
	v_fmac_f32_e32 v103, v105, v103
	v_div_scale_f32 v105, vcc, 1.0, v97, 1.0
	v_mul_f32_e32 v106, v105, v103
	v_fma_f32 v107, -v102, v106, v105
	v_fmac_f32_e32 v106, v107, v103
	v_fma_f32 v102, -v102, v106, v105
	v_div_fmas_f32 v102, v102, v103, v106
	v_div_fixup_f32 v97, v102, v97, 1.0

.LBB0_3002:
	v_add_u32_e32 v130, v120, v150
	v_lshlrev_b64 v[94:95], 2, v[130:131]
	v_lshl_add_u64 v[102:103], s[28:29], 0, v[94:95]
	global_load_dwordx4 v[96:99], v[102:103], off offset:16
	s_nop 0
	global_load_dwordx4 v[102:105], v[102:103], off
	v_lshl_add_u64 v[94:95], s[36:37], 0, v[94:95]
	global_load_dwordx4 v[106:109], v[94:95], off offset:16
	global_load_dwordx4 v[110:113], v[94:95], off
	v_lshlrev_b32_e32 v94, 16, v22
	v_and_b32_e32 v95, 0xffff0000, v22
	v_lshlrev_b32_e32 v114, 16, v90
	v_and_b32_e32 v115, 0xffff0000, v90
	v_lshlrev_b32_e32 v116, 16, v62
	v_and_b32_e32 v117, 0xffff0000, v62
	v_pk_add_f32 v[114:115], v[114:115], v[94:95] neg_lo:[0,1] neg_hi:[0,1]
	v_lshlrev_b32_e32 v90, 16, v91
	v_and_b32_e32 v91, 0xffff0000, v91
	v_lshrrev_b32_e32 v100, 2, v151
	v_cmp_lt_u32_e32 vcc, s76, v130
	s_waitcnt vmcnt(2)
	v_pk_fma_f32 v[102:103], v[114:115], v[102:103], v[94:95]
	v_pk_add_f32 v[94:95], v[116:117], v[94:95] neg_lo:[0,1] neg_hi:[0,1]
	s_waitcnt vmcnt(0)
	v_pk_fma_f32 v[94:95], v[94:95], v[110:111], v[102:103]
	v_lshlrev_b32_e32 v102, 16, v23
	v_and_b32_e32 v103, 0xffff0000, v23
	v_lshlrev_b32_e32 v110, 16, v63
	v_and_b32_e32 v111, 0xffff0000, v63
	v_pk_add_f32 v[90:91], v[90:91], v[102:103] neg_lo:[0,1] neg_hi:[0,1]
	s_nop 0
	v_pk_fma_f32 v[90:91], v[90:91], v[104:105], v[102:103]
	v_pk_add_f32 v[102:103], v[110:111], v[102:103] neg_lo:[0,1] neg_hi:[0,1]
	v_lshlrev_b32_e32 v104, 16, v92
	v_pk_fma_f32 v[90:91], v[102:103], v[112:113], v[90:91]
	v_lshlrev_b32_e32 v102, 16, v24
	v_and_b32_e32 v103, 0xffff0000, v24
	v_and_b32_e32 v105, 0xffff0000, v92
	v_lshlrev_b32_e32 v110, 16, v64
	v_and_b32_e32 v111, 0xffff0000, v64
	v_pk_add_f32 v[104:105], v[104:105], v[102:103] neg_lo:[0,1] neg_hi:[0,1]
	v_lshlrev_b32_e32 v92, 16, v93
	v_pk_fma_f32 v[96:97], v[104:105], v[96:97], v[102:103]
	v_pk_add_f32 v[102:103], v[110:111], v[102:103] neg_lo:[0,1] neg_hi:[0,1]
	v_and_b32_e32 v93, 0xffff0000, v93
	v_pk_fma_f32 v[96:97], v[102:103], v[106:107], v[96:97]
	v_lshlrev_b32_e32 v102, 16, v25
	v_and_b32_e32 v103, 0xffff0000, v25
	v_lshlrev_b32_e32 v104, 16, v65
	v_and_b32_e32 v105, 0xffff0000, v65
	v_pk_add_f32 v[92:93], v[92:93], v[102:103] neg_lo:[0,1] neg_hi:[0,1]
	s_nop 0
	v_pk_fma_f32 v[92:93], v[92:93], v[98:99], v[102:103]
	v_pk_add_f32 v[98:99], v[104:105], v[102:103] neg_lo:[0,1] neg_hi:[0,1]
	s_nop 0
	v_pk_fma_f32 v[92:93], v[98:99], v[108:109], v[92:93]
	s_and_saveexec_b64 s[2:3], vcc
	s_xor_b64 s[12:13], exec, s[2:3]
	s_cbranch_execz .LBB0_3050
	v_cmp_lt_u32_e32 vcc, s77, v130
	s_and_saveexec_b64 s[2:3], vcc
	s_xor_b64 s[14:15], exec, s[2:3]
	s_cbranch_execz .LBB0_3047
	v_cmp_lt_u32_e32 vcc, s78, v130
	s_and_saveexec_b64 s[2:3], vcc
	s_xor_b64 s[16:17], exec, s[2:3]
	s_cbranch_execz .LBB0_3044
	v_cmp_lt_u32_e32 vcc, s79, v130
	s_and_saveexec_b64 s[2:3], vcc
	s_xor_b64 s[18:19], exec, s[2:3]
	s_cbranch_execz .LBB0_3009
	v_cmp_lt_u32_e32 vcc, s80, v130
	s_and_saveexec_b64 s[20:21], vcc
	s_cbranch_execz .LBB0_3008
	v_mul_f32_e32 v98, 0xbfb8aa3b, v94
	v_rndne_f32_e32 v99, v98
	v_sub_f32_e32 v101, v98, v99
	v_fma_f32 v98, v94, s81, -v98
	v_fmac_f32_e32 v98, 0xb2a5705f, v94
	v_add_f32_e32 v98, v101, v98
	v_exp_f32_e32 v98, v98
	v_cvt_i32_f32_e32 v99, v99
	v_cmp_nlt_f32_e32 vcc, s82, v94
	v_ldexp_f32 v98, v98, v99
	s_nop 0
	v_cndmask_b32_e32 v98, 0, v98, vcc
	v_cmp_ngt_f32_e32 vcc, s83, v94
	s_nop 1
	v_cndmask_b32_e32 v94, v143, v98, vcc
	v_mul_f32_e32 v98, 0xbfb8aa3b, v95
	v_rndne_f32_e32 v99, v98
	v_sub_f32_e32 v101, v98, v99
	v_fma_f32 v98, v95, s81, -v98
	v_fmac_f32_e32 v98, 0xb2a5705f, v95
	v_add_f32_e32 v98, v101, v98
	v_exp_f32_e32 v98, v98
	v_cvt_i32_f32_e32 v99, v99
	v_cmp_nlt_f32_e32 vcc, s82, v95
	v_ldexp_f32 v98, v98, v99
	s_nop 0
	v_cndmask_b32_e32 v98, 0, v98, vcc
	v_cmp_ngt_f32_e32 vcc, s83, v95
	s_nop 1
	v_cndmask_b32_e32 v95, v143, v98, vcc
	v_mul_f32_e32 v98, 0xbfb8aa3b, v90
	v_rndne_f32_e32 v99, v98
	v_sub_f32_e32 v101, v98, v99
	v_fma_f32 v98, v90, s81, -v98
	v_fmac_f32_e32 v98, 0xb2a5705f, v90
	v_add_f32_e32 v98, v101, v98
	v_exp_f32_e32 v98, v98
	v_cvt_i32_f32_e32 v99, v99
	v_cmp_nlt_f32_e32 vcc, s82, v90
	v_pk_add_f32 v[94:95], v[94:95], 1.0 op_sel_hi:[1,0]
	v_ldexp_f32 v98, v98, v99
	v_cndmask_b32_e32 v98, 0, v98, vcc
	v_cmp_ngt_f32_e32 vcc, s83, v90
	s_nop 1
	v_cndmask_b32_e32 v90, v143, v98, vcc
	v_mul_f32_e32 v98, 0xbfb8aa3b, v91
	v_rndne_f32_e32 v99, v98
	v_sub_f32_e32 v101, v98, v99
	v_fma_f32 v98, v91, s81, -v98
	v_fmac_f32_e32 v98, 0xb2a5705f, v91
	v_add_f32_e32 v98, v101, v98
	v_exp_f32_e32 v98, v98
	v_cvt_i32_f32_e32 v99, v99
	v_cmp_nlt_f32_e32 vcc, s82, v91
	v_ldexp_f32 v98, v98, v99
	s_nop 0
	v_cndmask_b32_e32 v98, 0, v98, vcc
	v_cmp_ngt_f32_e32 vcc, s83, v91
	s_nop 1
	v_cndmask_b32_e32 v91, v143, v98, vcc
	v_mul_f32_e32 v98, 0xbfb8aa3b, v96
	v_rndne_f32_e32 v99, v98
	v_sub_f32_e32 v101, v98, v99
	v_fma_f32 v98, v96, s81, -v98
	v_fmac_f32_e32 v98, 0xb2a5705f, v96
	v_add_f32_e32 v98, v101, v98
	v_exp_f32_e32 v98, v98
	v_cvt_i32_f32_e32 v99, v99
	v_cmp_nlt_f32_e32 vcc, s82, v96
	v_pk_add_f32 v[90:91], v[90:91], 1.0 op_sel_hi:[1,0]
	v_ldexp_f32 v98, v98, v99
	v_cndmask_b32_e32 v98, 0, v98, vcc
	v_cmp_ngt_f32_e32 vcc, s83, v96
	s_nop 1
	v_cndmask_b32_e32 v96, v143, v98, vcc
	v_mul_f32_e32 v98, 0xbfb8aa3b, v97
	v_rndne_f32_e32 v99, v98
	v_sub_f32_e32 v101, v98, v99
	v_fma_f32 v98, v97, s81, -v98
	v_fmac_f32_e32 v98, 0xb2a5705f, v97
	v_add_f32_e32 v98, v101, v98
	v_exp_f32_e32 v98, v98
	v_cvt_i32_f32_e32 v99, v99
	v_cmp_nlt_f32_e32 vcc, s82, v97
	v_ldexp_f32 v98, v98, v99
	s_nop 0
	v_cndmask_b32_e32 v98, 0, v98, vcc
	v_cmp_ngt_f32_e32 vcc, s83, v97
	s_nop 1
	v_cndmask_b32_e32 v97, v143, v98, vcc
	v_mul_f32_e32 v98, 0xbfb8aa3b, v92
	v_rndne_f32_e32 v99, v98
	v_sub_f32_e32 v101, v98, v99
	v_fma_f32 v98, v92, s81, -v98
	v_fmac_f32_e32 v98, 0xb2a5705f, v92
	v_add_f32_e32 v98, v101, v98
	v_exp_f32_e32 v98, v98
	v_cvt_i32_f32_e32 v99, v99
	v_cmp_nlt_f32_e32 vcc, s82, v92
	v_pk_add_f32 v[96:97], v[96:97], 1.0 op_sel_hi:[1,0]
	v_ldexp_f32 v98, v98, v99
	v_cndmask_b32_e32 v98, 0, v98, vcc
	v_cmp_ngt_f32_e32 vcc, s83, v92
	s_nop 1
	v_cndmask_b32_e32 v92, v143, v98, vcc
	v_mul_f32_e32 v98, 0xbfb8aa3b, v93
	v_rndne_f32_e32 v99, v98
	v_sub_f32_e32 v101, v98, v99
	v_fma_f32 v98, v93, s81, -v98
	v_fmac_f32_e32 v98, 0xb2a5705f, v93
	v_add_f32_e32 v98, v101, v98
	v_exp_f32_e32 v98, v98
	v_cvt_i32_f32_e32 v99, v99
	v_cmp_nlt_f32_e32 vcc, s82, v93
	v_ldexp_f32 v98, v98, v99
	s_nop 0
	v_cndmask_b32_e32 v98, 0, v98, vcc
	v_cmp_ngt_f32_e32 vcc, s83, v93
	s_nop 1
	v_cndmask_b32_e32 v93, v143, v98, vcc
	v_div_scale_f32 v98, s[2:3], v94, v94, 1.0
	v_rcp_f32_e32 v99, v98
	v_pk_add_f32 v[92:93], v[92:93], 1.0 op_sel_hi:[1,0]
	v_fma_f32 v101, -v98, v99, 1.0
	v_fmac_f32_e32 v99, v101, v99
	v_div_scale_f32 v101, vcc, 1.0, v94, 1.0
	v_mul_f32_e32 v102, v101, v99
	v_fma_f32 v103, -v98, v102, v101
	v_fmac_f32_e32 v102, v103, v99
	v_fma_f32 v98, -v98, v102, v101
	v_div_fmas_f32 v98, v98, v99, v102
	v_div_fixup_f32 v94, v98, v94, 1.0
	v_rcp_f32_e32 v95, v95
	s_nop 3
	v_rcp_f32_e32 v90, v90
	s_nop 3
	v_rcp_f32_e32 v91, v91
	s_nop 3
	v_rcp_f32_e32 v96, v96
	s_nop 3
	v_rcp_f32_e32 v97, v97
	s_nop 3
	v_rcp_f32_e32 v92, v92
	s_nop 3
	v_div_scale_f32 v98, s[2:3], v93, v93, 1.0
	v_rcp_f32_e32 v99, v98
	s_nop 0
	v_fma_f32 v101, -v98, v99, 1.0
	v_fmac_f32_e32 v99, v101, v99
	v_div_scale_f32 v101, vcc, 1.0, v93, 1.0
	v_mul_f32_e32 v102, v101, v99
	v_fma_f32 v103, -v98, v102, v101
	v_fmac_f32_e32 v102, v103, v99
	v_fma_f32 v98, -v98, v102, v101
	v_div_fmas_f32 v98, v98, v99, v102
	v_div_fixup_f32 v93, v98, v93, 1.0

.LBB0_3053:
	v_add_u32_e32 v130, v120, v147
	v_lshlrev_b64 v[90:91], 2, v[130:131]
	v_lshl_add_u64 v[98:99], s[28:29], 0, v[90:91]
	global_load_dwordx4 v[92:95], v[98:99], off offset:16
	s_nop 0
	global_load_dwordx4 v[98:101], v[98:99], off
	v_lshl_add_u64 v[90:91], s[36:37], 0, v[90:91]
	global_load_dwordx4 v[102:105], v[90:91], off offset:16
	global_load_dwordx4 v[106:109], v[90:91], off
	v_lshlrev_b32_e32 v90, 16, v26
	v_and_b32_e32 v91, 0xffff0000, v26
	v_lshlrev_b32_e32 v110, 16, v86
	v_and_b32_e32 v111, 0xffff0000, v86
	v_lshlrev_b32_e32 v112, 16, v70
	v_and_b32_e32 v113, 0xffff0000, v70
	v_pk_add_f32 v[110:111], v[110:111], v[90:91] neg_lo:[0,1] neg_hi:[0,1]
	v_lshlrev_b32_e32 v86, 16, v87
	v_and_b32_e32 v87, 0xffff0000, v87
	v_lshrrev_b32_e32 v96, 2, v148
	v_cmp_lt_u32_e32 vcc, s76, v130
	s_waitcnt vmcnt(2)
	v_pk_fma_f32 v[98:99], v[110:111], v[98:99], v[90:91]
	v_pk_add_f32 v[90:91], v[112:113], v[90:91] neg_lo:[0,1] neg_hi:[0,1]
	s_waitcnt vmcnt(0)
	v_pk_fma_f32 v[90:91], v[90:91], v[106:107], v[98:99]
	v_lshlrev_b32_e32 v98, 16, v27
	v_and_b32_e32 v99, 0xffff0000, v27
	v_lshlrev_b32_e32 v106, 16, v71
	v_and_b32_e32 v107, 0xffff0000, v71
	v_pk_add_f32 v[86:87], v[86:87], v[98:99] neg_lo:[0,1] neg_hi:[0,1]
	s_nop 0
	v_pk_fma_f32 v[86:87], v[86:87], v[100:101], v[98:99]
	v_pk_add_f32 v[98:99], v[106:107], v[98:99] neg_lo:[0,1] neg_hi:[0,1]
	v_lshlrev_b32_e32 v100, 16, v88
	v_pk_fma_f32 v[86:87], v[98:99], v[108:109], v[86:87]
	v_lshlrev_b32_e32 v98, 16, v28
	v_and_b32_e32 v99, 0xffff0000, v28
	v_and_b32_e32 v101, 0xffff0000, v88
	v_lshlrev_b32_e32 v106, 16, v72
	v_and_b32_e32 v107, 0xffff0000, v72
	v_pk_add_f32 v[100:101], v[100:101], v[98:99] neg_lo:[0,1] neg_hi:[0,1]
	v_lshlrev_b32_e32 v88, 16, v89
	v_pk_fma_f32 v[92:93], v[100:101], v[92:93], v[98:99]
	v_pk_add_f32 v[98:99], v[106:107], v[98:99] neg_lo:[0,1] neg_hi:[0,1]
	v_and_b32_e32 v89, 0xffff0000, v89
	v_pk_fma_f32 v[92:93], v[98:99], v[102:103], v[92:93]
	v_lshlrev_b32_e32 v98, 16, v29
	v_and_b32_e32 v99, 0xffff0000, v29
	v_lshlrev_b32_e32 v100, 16, v73
	v_and_b32_e32 v101, 0xffff0000, v73
	v_pk_add_f32 v[88:89], v[88:89], v[98:99] neg_lo:[0,1] neg_hi:[0,1]
	s_nop 0
	v_pk_fma_f32 v[88:89], v[88:89], v[94:95], v[98:99]
	v_pk_add_f32 v[94:95], v[100:101], v[98:99] neg_lo:[0,1] neg_hi:[0,1]
	s_nop 0
	v_pk_fma_f32 v[88:89], v[94:95], v[104:105], v[88:89]
	s_and_saveexec_b64 s[2:3], vcc
	s_xor_b64 s[6:7], exec, s[2:3]
	s_cbranch_execz .LBB0_3101
	v_cmp_lt_u32_e32 vcc, s77, v130
	s_and_saveexec_b64 s[2:3], vcc
	s_xor_b64 s[12:13], exec, s[2:3]
	s_cbranch_execz .LBB0_3098
	v_cmp_lt_u32_e32 vcc, s78, v130
	s_and_saveexec_b64 s[2:3], vcc
	s_xor_b64 s[14:15], exec, s[2:3]
	s_cbranch_execz .LBB0_3095
	v_cmp_lt_u32_e32 vcc, s79, v130
	s_and_saveexec_b64 s[2:3], vcc
	s_xor_b64 s[16:17], exec, s[2:3]
	s_cbranch_execz .LBB0_3060
	v_cmp_lt_u32_e32 vcc, s80, v130
	s_and_saveexec_b64 s[18:19], vcc
	s_cbranch_execz .LBB0_3059
	v_mul_f32_e32 v94, 0xbfb8aa3b, v90
	v_rndne_f32_e32 v95, v94
	v_sub_f32_e32 v97, v94, v95
	v_fma_f32 v94, v90, s81, -v94
	v_fmac_f32_e32 v94, 0xb2a5705f, v90
	v_add_f32_e32 v94, v97, v94
	v_exp_f32_e32 v94, v94
	v_cvt_i32_f32_e32 v95, v95
	v_cmp_nlt_f32_e32 vcc, s82, v90
	v_ldexp_f32 v94, v94, v95
	s_nop 0
	v_cndmask_b32_e32 v94, 0, v94, vcc
	v_cmp_ngt_f32_e32 vcc, s83, v90
	s_nop 1
	v_cndmask_b32_e32 v90, v143, v94, vcc
	v_mul_f32_e32 v94, 0xbfb8aa3b, v91
	v_rndne_f32_e32 v95, v94
	v_sub_f32_e32 v97, v94, v95
	v_fma_f32 v94, v91, s81, -v94
	v_fmac_f32_e32 v94, 0xb2a5705f, v91
	v_add_f32_e32 v94, v97, v94
	v_exp_f32_e32 v94, v94
	v_cvt_i32_f32_e32 v95, v95
	v_cmp_nlt_f32_e32 vcc, s82, v91
	v_ldexp_f32 v94, v94, v95
	s_nop 0
	v_cndmask_b32_e32 v94, 0, v94, vcc
	v_cmp_ngt_f32_e32 vcc, s83, v91
	s_nop 1
	v_cndmask_b32_e32 v91, v143, v94, vcc
	v_mul_f32_e32 v94, 0xbfb8aa3b, v86
	v_rndne_f32_e32 v95, v94
	v_sub_f32_e32 v97, v94, v95
	v_fma_f32 v94, v86, s81, -v94
	v_fmac_f32_e32 v94, 0xb2a5705f, v86
	v_add_f32_e32 v94, v97, v94
	v_exp_f32_e32 v94, v94
	v_cvt_i32_f32_e32 v95, v95
	v_cmp_nlt_f32_e32 vcc, s82, v86
	v_pk_add_f32 v[90:91], v[90:91], 1.0 op_sel_hi:[1,0]
	v_ldexp_f32 v94, v94, v95
	v_cndmask_b32_e32 v94, 0, v94, vcc
	v_cmp_ngt_f32_e32 vcc, s83, v86
	s_nop 1
	v_cndmask_b32_e32 v86, v143, v94, vcc
	v_mul_f32_e32 v94, 0xbfb8aa3b, v87
	v_rndne_f32_e32 v95, v94
	v_sub_f32_e32 v97, v94, v95
	v_fma_f32 v94, v87, s81, -v94
	v_fmac_f32_e32 v94, 0xb2a5705f, v87
	v_add_f32_e32 v94, v97, v94
	v_exp_f32_e32 v94, v94
	v_cvt_i32_f32_e32 v95, v95
	v_cmp_nlt_f32_e32 vcc, s82, v87
	v_ldexp_f32 v94, v94, v95
	s_nop 0
	v_cndmask_b32_e32 v94, 0, v94, vcc
	v_cmp_ngt_f32_e32 vcc, s83, v87
	s_nop 1
	v_cndmask_b32_e32 v87, v143, v94, vcc
	v_mul_f32_e32 v94, 0xbfb8aa3b, v92
	v_rndne_f32_e32 v95, v94
	v_sub_f32_e32 v97, v94, v95
	v_fma_f32 v94, v92, s81, -v94
	v_fmac_f32_e32 v94, 0xb2a5705f, v92
	v_add_f32_e32 v94, v97, v94
	v_exp_f32_e32 v94, v94
	v_cvt_i32_f32_e32 v95, v95
	v_cmp_nlt_f32_e32 vcc, s82, v92
	v_pk_add_f32 v[86:87], v[86:87], 1.0 op_sel_hi:[1,0]
	v_ldexp_f32 v94, v94, v95
	v_cndmask_b32_e32 v94, 0, v94, vcc
	v_cmp_ngt_f32_e32 vcc, s83, v92
	s_nop 1
	v_cndmask_b32_e32 v92, v143, v94, vcc
	v_mul_f32_e32 v94, 0xbfb8aa3b, v93
	v_rndne_f32_e32 v95, v94
	v_sub_f32_e32 v97, v94, v95
	v_fma_f32 v94, v93, s81, -v94
	v_fmac_f32_e32 v94, 0xb2a5705f, v93
	v_add_f32_e32 v94, v97, v94
	v_exp_f32_e32 v94, v94
	v_cvt_i32_f32_e32 v95, v95
	v_cmp_nlt_f32_e32 vcc, s82, v93
	v_ldexp_f32 v94, v94, v95
	s_nop 0
	v_cndmask_b32_e32 v94, 0, v94, vcc
	v_cmp_ngt_f32_e32 vcc, s83, v93
	s_nop 1
	v_cndmask_b32_e32 v93, v143, v94, vcc
	v_mul_f32_e32 v94, 0xbfb8aa3b, v88
	v_rndne_f32_e32 v95, v94
	v_sub_f32_e32 v97, v94, v95
	v_fma_f32 v94, v88, s81, -v94
	v_fmac_f32_e32 v94, 0xb2a5705f, v88
	v_add_f32_e32 v94, v97, v94
	v_exp_f32_e32 v94, v94
	v_cvt_i32_f32_e32 v95, v95
	v_cmp_nlt_f32_e32 vcc, s82, v88
	v_pk_add_f32 v[92:93], v[92:93], 1.0 op_sel_hi:[1,0]
	v_ldexp_f32 v94, v94, v95
	v_cndmask_b32_e32 v94, 0, v94, vcc
	v_cmp_ngt_f32_e32 vcc, s83, v88
	s_nop 1
	v_cndmask_b32_e32 v88, v143, v94, vcc
	v_mul_f32_e32 v94, 0xbfb8aa3b, v89
	v_rndne_f32_e32 v95, v94
	v_sub_f32_e32 v97, v94, v95
	v_fma_f32 v94, v89, s81, -v94
	v_fmac_f32_e32 v94, 0xb2a5705f, v89
	v_add_f32_e32 v94, v97, v94
	v_exp_f32_e32 v94, v94
	v_cvt_i32_f32_e32 v95, v95
	v_cmp_nlt_f32_e32 vcc, s82, v89
	v_ldexp_f32 v94, v94, v95
	s_nop 0
	v_cndmask_b32_e32 v94, 0, v94, vcc
	v_cmp_ngt_f32_e32 vcc, s83, v89
	s_nop 1
	v_cndmask_b32_e32 v89, v143, v94, vcc
	v_div_scale_f32 v94, s[2:3], v90, v90, 1.0
	v_rcp_f32_e32 v95, v94
	v_pk_add_f32 v[88:89], v[88:89], 1.0 op_sel_hi:[1,0]
	v_fma_f32 v97, -v94, v95, 1.0
	v_fmac_f32_e32 v95, v97, v95
	v_div_scale_f32 v97, vcc, 1.0, v90, 1.0
	v_mul_f32_e32 v98, v97, v95
	v_fma_f32 v99, -v94, v98, v97
	v_fmac_f32_e32 v98, v99, v95
	v_fma_f32 v94, -v94, v98, v97
	v_div_fmas_f32 v94, v94, v95, v98
	v_div_fixup_f32 v90, v94, v90, 1.0
	v_rcp_f32_e32 v91, v91
	s_nop 3
	v_rcp_f32_e32 v86, v86
	s_nop 3
	v_rcp_f32_e32 v87, v87
	s_nop 3
	v_rcp_f32_e32 v92, v92
	s_nop 3
	v_rcp_f32_e32 v93, v93
	s_nop 3
	v_rcp_f32_e32 v88, v88
	s_nop 3
	v_div_scale_f32 v94, s[2:3], v89, v89, 1.0
	v_rcp_f32_e32 v95, v94
	s_nop 0
	v_fma_f32 v97, -v94, v95, 1.0
	v_fmac_f32_e32 v95, v97, v95
	v_div_scale_f32 v97, vcc, 1.0, v89, 1.0
	v_mul_f32_e32 v98, v97, v95
	v_fma_f32 v99, -v94, v98, v97
	v_fmac_f32_e32 v98, v99, v95
	v_fma_f32 v94, -v94, v98, v97
	v_div_fmas_f32 v94, v94, v95, v98
	v_div_fixup_f32 v89, v94, v89, 1.0

.LBB0_3593:
	ds_read_b128 v[30:33], v183
	ds_read_b128 v[26:29], v183 offset:64
	ds_read_b128 v[34:37], v184 offset:18432
	ds_read_b128 v[38:41], v184 offset:18496
	s_lshl_b32 s0, s93, 5
	s_sub_i32 s2, s86, s0
	s_lshr_b32 s0, s92, 24
	s_waitcnt lgkmcnt(1)
	v_mfma_f32_16x16x32_bf16 v[34:37], v[34:37], v[30:33], 0
	s_add_i32 s0, s86, s0
	s_ashr_i32 s0, s0, 8
	s_ashr_i32 s1, s0, 31
	s_waitcnt lgkmcnt(0)
	v_mfma_f32_16x16x32_bf16 v[54:57], v[38:41], v[26:29], v[34:37]
	ds_read_b128 v[38:41], v184 offset:20800
	s_ashr_i32 s3, s2, 31
	s_nop 0
	ds_read_b128 v[34:37], v184 offset:20736
	s_lshl_b64 s[0:1], s[0:1], 12
	s_lshl_b64 s[92:93], s[2:3], 7
	s_add_u32 s0, s0, s92
	s_addc_u32 s1, s1, s93
	s_waitcnt lgkmcnt(0)
	v_mfma_f32_16x16x32_bf16 v[34:37], v[34:37], v[30:33], 0
	s_lshl_b32 s86, s97, 7
	ds_read_b128 v[58:61], v184 offset:34624
	v_mfma_f32_16x16x32_bf16 v[62:65], v[38:41], v[26:29], v[34:37]
	ds_read_b128 v[38:41], v184 offset:23104
	s_nop 3
	ds_read_b128 v[34:37], v184 offset:23040
	s_waitcnt lgkmcnt(0)
	v_mfma_f32_16x16x32_bf16 v[34:37], v[34:37], v[30:33], 0
	v_mfma_f32_16x16x32_bf16 v[66:69], v[38:41], v[26:29], v[34:37]
	ds_read_b128 v[38:41], v184 offset:25408
	s_nop 5
	ds_read_b128 v[34:37], v184 offset:25344
	s_waitcnt lgkmcnt(0)
	v_mfma_f32_16x16x32_bf16 v[34:37], v[34:37], v[30:33], 0
	v_mfma_f32_16x16x32_bf16 v[50:53], v[38:41], v[26:29], v[34:37]
	ds_read_b128 v[38:41], v184 offset:27712
	s_nop 5
	ds_read_b128 v[34:37], v184 offset:27648
	s_waitcnt lgkmcnt(0)
	v_mfma_f32_16x16x32_bf16 v[34:37], v[34:37], v[30:33], 0
	v_mfma_f32_16x16x32_bf16 v[46:49], v[38:41], v[26:29], v[34:37]
	ds_read_b128 v[38:41], v184 offset:30016
	s_nop 5
	ds_read_b128 v[34:37], v184 offset:29952
	s_waitcnt lgkmcnt(0)
	v_mfma_f32_16x16x32_bf16 v[34:37], v[34:37], v[30:33], 0
	v_mfma_f32_16x16x32_bf16 v[42:45], v[38:41], v[26:29], v[34:37]
	ds_read_b128 v[38:41], v184 offset:32320
	s_nop 5
	ds_read_b128 v[34:37], v184 offset:32256
	s_waitcnt lgkmcnt(0)
	v_mfma_f32_16x16x32_bf16 v[34:37], v[34:37], v[30:33], 0
	v_mfma_f32_16x16x32_bf16 v[38:41], v[38:41], v[26:29], v[34:37]
	s_nop 6
	ds_read_b128 v[34:37], v184 offset:34560
	s_waitcnt lgkmcnt(0)
	v_mfma_f32_16x16x32_bf16 v[34:37], v[34:37], v[30:33], 0
	v_mfma_f32_16x16x32_bf16 v[34:37], v[58:61], v[26:29], v[34:37]
	v_mul_f32_e32 v58, v107, v89
	v_mul_f32_e32 v59, v108, v87
	v_cndmask_b32_e64 v58, v59, v58, s[6:7]
	v_mul_f32_e32 v59, v107, v91
	v_mul_f32_e32 v60, v108, v93
	v_cndmask_b32_e64 v59, v59, v60, s[12:13]
	v_mul_f32_e32 v58, 0x3fb8aa3b, v58
	v_mul_f32_e32 v59, 0x3fb8aa3b, v59
	v_exp_f32_e32 v58, v58
	v_exp_f32_e32 v59, v59
	v_mul_f32_e32 v60, v108, v120
	v_pk_mul_f32 v[58:59], v[58:59], v[54:55]
	v_mul_f32_e32 v54, v107, v119
	v_mul_f32_e32 v55, v108, v118
	v_cndmask_b32_e64 v54, v55, v54, s[14:15]
	v_mul_f32_e32 v55, v107, v121
	v_cndmask_b32_e64 v55, v60, v55, s[16:17]
	v_mul_f32_e32 v54, 0x3fb8aa3b, v54
	v_mul_f32_e32 v55, 0x3fb8aa3b, v55
	v_exp_f32_e32 v54, v54
	v_exp_f32_e32 v55, v55
	v_cvt_pk_bf16_f32 v58, v58, v59
	v_pk_mul_f32 v[60:61], v[54:55], v[56:57]
	v_mul_f32_e32 v54, v107, v123
	v_mul_f32_e32 v55, v108, v122
	v_cndmask_b32_e64 v54, v55, v54, s[18:19]
	v_mul_f32_e32 v55, v107, v125
	v_mul_f32_e32 v56, v108, v124
	v_cndmask_b32_e64 v55, v56, v55, s[20:21]
	v_mul_f32_e32 v54, 0x3fb8aa3b, v54
	v_mul_f32_e32 v55, 0x3fb8aa3b, v55
	v_exp_f32_e32 v54, v54
	v_exp_f32_e32 v55, v55
	v_mul_f32_e32 v56, v108, v128
	v_mul_f32_e32 v57, v108, v134
	v_cvt_pk_bf16_f32 v59, v60, v61
	v_pk_mul_f32 v[62:63], v[54:55], v[62:63]
	v_mul_f32_e32 v54, v107, v127
	v_mul_f32_e32 v55, v108, v126
	v_cndmask_b32_e64 v54, v55, v54, s[22:23]
	v_mul_f32_e32 v55, v107, v129
	v_cndmask_b32_e64 v55, v56, v55, s[24:25]
	v_mul_f32_e32 v54, 0x3fb8aa3b, v54
	v_mul_f32_e32 v55, 0x3fb8aa3b, v55
	v_exp_f32_e32 v54, v54
	v_exp_f32_e32 v55, v55
	v_mul_f32_e32 v56, v108, v132
	v_cvt_pk_bf16_f32 v60, v62, v63
	v_pk_mul_f32 v[64:65], v[54:55], v[64:65]
	v_mul_f32_e32 v54, v107, v131
	v_mul_f32_e32 v55, v108, v130
	v_cndmask_b32_e64 v54, v55, v54, s[26:27]
	v_mul_f32_e32 v55, v107, v133
	v_cndmask_b32_e64 v55, v56, v55, s[28:29]
	v_mul_f32_e32 v54, 0x3fb8aa3b, v54
	v_mul_f32_e32 v55, 0x3fb8aa3b, v55
	v_exp_f32_e32 v54, v54
	v_exp_f32_e32 v55, v55
	v_mul_f32_e32 v56, v107, v135
	v_cndmask_b32_e64 v56, v57, v56, s[30:31]
	v_mul_f32_e32 v57, v107, v137
	v_pk_mul_f32 v[54:55], v[54:55], v[66:67]
	v_mul_f32_e32 v66, v108, v136
	v_cndmask_b32_e64 v57, v66, v57, s[34:35]
	v_mul_f32_e32 v56, 0x3fb8aa3b, v56
	v_mul_f32_e32 v57, 0x3fb8aa3b, v57
	v_exp_f32_e32 v56, v56
	v_exp_f32_e32 v57, v57
	v_mul_f32_e32 v66, v107, v139
	v_mul_f32_e32 v67, v108, v138
	v_cndmask_b32_e64 v66, v67, v66, s[36:37]
	v_pk_mul_f32 v[56:57], v[56:57], v[68:69]
	v_mul_f32_e32 v67, v107, v141
	v_mul_f32_e32 v68, v108, v140
	v_cndmask_b32_e64 v67, v68, v67, s[38:39]
	v_mul_f32_e32 v66, 0x3fb8aa3b, v66
	v_mul_f32_e32 v67, 0x3fb8aa3b, v67
	v_exp_f32_e32 v66, v66
	v_exp_f32_e32 v67, v67
	v_mul_f32_e32 v68, v108, v144
	v_cvt_pk_bf16_f32 v61, v64, v65
	v_cvt_pk_bf16_f32 v54, v54, v55
	v_pk_mul_f32 v[50:51], v[66:67], v[50:51]
	v_mul_f32_e32 v66, v107, v143
	v_mul_f32_e32 v67, v108, v142
	v_cndmask_b32_e64 v66, v67, v66, s[40:41]
	v_mul_f32_e32 v67, v107, v145
	v_cndmask_b32_e64 v67, v68, v67, s[42:43]
	v_mul_f32_e32 v66, 0x3fb8aa3b, v66
	v_mul_f32_e32 v67, 0x3fb8aa3b, v67
	v_exp_f32_e32 v66, v66
	v_exp_f32_e32 v67, v67
	v_mul_f32_e32 v68, v108, v148
	v_cvt_pk_bf16_f32 v55, v56, v57
	v_cvt_pk_bf16_f32 v56, v50, v51
	v_pk_mul_f32 v[52:53], v[66:67], v[52:53]
	v_mul_f32_e32 v66, v107, v147
	v_mul_f32_e32 v67, v108, v146
	v_cndmask_b32_e64 v66, v67, v66, s[44:45]
	v_mul_f32_e32 v67, v107, v149
	v_cndmask_b32_e64 v67, v68, v67, s[46:47]
	v_mul_f32_e32 v66, 0x3fb8aa3b, v66
	v_mul_f32_e32 v67, 0x3fb8aa3b, v67
	v_exp_f32_e32 v66, v66
	v_exp_f32_e32 v67, v67
	v_mul_f32_e32 v68, v108, v152
	v_cvt_pk_bf16_f32 v57, v52, v53
	v_pk_mul_f32 v[46:47], v[66:67], v[46:47]
	v_mul_f32_e32 v66, v107, v151
	v_mul_f32_e32 v67, v108, v150
	v_cndmask_b32_e64 v66, v67, v66, s[48:49]
	v_mul_f32_e32 v67, v107, v153
	v_cndmask_b32_e64 v67, v68, v67, s[50:51]
	v_mul_f32_e32 v66, 0x3fb8aa3b, v66
	v_mul_f32_e32 v67, 0x3fb8aa3b, v67
	v_exp_f32_e32 v66, v66
	v_exp_f32_e32 v67, v67
	v_mul_f32_e32 v68, v108, v156
	v_cvt_pk_bf16_f32 v46, v46, v47
	v_pk_mul_f32 v[48:49], v[66:67], v[48:49]
	v_mul_f32_e32 v66, v107, v155
	v_mul_f32_e32 v67, v108, v154
	v_cndmask_b32_e64 v66, v67, v66, s[52:53]
	v_mul_f32_e32 v67, v107, v157
	v_cndmask_b32_e64 v67, v68, v67, s[54:55]
	v_mul_f32_e32 v66, 0x3fb8aa3b, v66
	v_mul_f32_e32 v67, 0x3fb8aa3b, v67
	v_exp_f32_e32 v66, v66
	v_exp_f32_e32 v67, v67
	v_mul_f32_e32 v68, v108, v160
	v_cvt_pk_bf16_f32 v47, v48, v49
	v_pk_mul_f32 v[42:43], v[66:67], v[42:43]
	v_mul_f32_e32 v66, v107, v159
	v_mul_f32_e32 v67, v108, v158
	v_cndmask_b32_e64 v66, v67, v66, s[56:57]
	v_mul_f32_e32 v67, v107, v161
	v_cndmask_b32_e64 v67, v68, v67, s[58:59]
	v_mul_f32_e32 v66, 0x3fb8aa3b, v66
	v_mul_f32_e32 v67, 0x3fb8aa3b, v67
	v_exp_f32_e32 v66, v66
	v_exp_f32_e32 v67, v67
	v_mul_f32_e32 v68, v108, v164
	v_cvt_pk_bf16_f32 v48, v42, v43
	v_pk_mul_f32 v[44:45], v[66:67], v[44:45]
	v_mul_f32_e32 v66, v107, v163
	v_mul_f32_e32 v67, v108, v162
	v_cndmask_b32_e64 v66, v67, v66, s[60:61]
	v_mul_f32_e32 v67, v107, v165
	v_cndmask_b32_e64 v67, v68, v67, s[62:63]
	v_mul_f32_e32 v66, 0x3fb8aa3b, v66
	v_mul_f32_e32 v67, 0x3fb8aa3b, v67
	v_exp_f32_e32 v66, v66
	v_exp_f32_e32 v67, v67
	v_mul_f32_e32 v68, v108, v168
	v_cvt_pk_bf16_f32 v49, v44, v45
	v_pk_mul_f32 v[38:39], v[66:67], v[38:39]
	v_mul_f32_e32 v66, v107, v167
	v_mul_f32_e32 v67, v108, v166
	v_cndmask_b32_e64 v66, v67, v66, s[64:65]
	v_mul_f32_e32 v67, v107, v169
	v_cndmask_b32_e64 v67, v68, v67, s[66:67]
	v_mul_f32_e32 v66, 0x3fb8aa3b, v66
	v_mul_f32_e32 v67, 0x3fb8aa3b, v67
	v_exp_f32_e32 v66, v66
	v_exp_f32_e32 v67, v67
	v_mul_f32_e32 v68, v108, v172
	v_cvt_pk_bf16_f32 v38, v38, v39
	v_pk_mul_f32 v[40:41], v[66:67], v[40:41]
	v_mul_f32_e32 v66, v107, v171
	v_mul_f32_e32 v67, v108, v170
	v_cndmask_b32_e64 v66, v67, v66, s[68:69]
	v_mul_f32_e32 v67, v107, v173
	v_cndmask_b32_e64 v67, v68, v67, s[70:71]
	v_mul_f32_e32 v66, 0x3fb8aa3b, v66
	v_mul_f32_e32 v67, 0x3fb8aa3b, v67
	v_exp_f32_e32 v66, v66
	v_exp_f32_e32 v67, v67
	v_mul_f32_e32 v68, v108, v176
	v_cvt_pk_bf16_f32 v39, v40, v41
	v_pk_mul_f32 v[34:35], v[66:67], v[34:35]
	v_mul_f32_e32 v66, v107, v175
	v_mul_f32_e32 v67, v108, v174
	v_cndmask_b32_e64 v66, v67, v66, s[72:73]
	v_mul_f32_e32 v67, v107, v177
	v_cndmask_b32_e64 v67, v68, v67, s[74:75]
	v_mul_f32_e32 v66, 0x3fb8aa3b, v66
	v_mul_f32_e32 v67, 0x3fb8aa3b, v67
	v_exp_f32_e32 v66, v66
	v_exp_f32_e32 v67, v67
	v_cvt_pk_bf16_f32 v40, v34, v35
	v_pk_mul_f32 v[36:37], v[66:67], v[36:37]
	ds_read_b64_tr_b16 v[64:65], v185 offset:39168
	ds_read_b64_tr_b16 v[62:63], v185 offset:36864
	ds_read_b64_tr_b16 v[66:67], v185 offset:36896
	ds_read_b64_tr_b16 v[68:69], v185 offset:39200
	ds_read_b64_tr_b16 v[110:111], v185 offset:36928
	ds_read_b64_tr_b16 v[112:113], v185 offset:39232
	ds_read_b64_tr_b16 v[192:193], v185 offset:36960
	ds_read_b64_tr_b16 v[194:195], v185 offset:39264
	s_waitcnt lgkmcnt(6)
	v_mfma_f32_16x16x32_bf16 v[62:65], v[62:65], v[58:61], 0
	v_cvt_pk_bf16_f32 v41, v36, v37
	s_waitcnt lgkmcnt(4)
	v_mfma_f32_16x16x32_bf16 v[66:69], v[66:69], v[58:61], 0
	s_waitcnt lgkmcnt(2)
	v_mfma_f32_16x16x32_bf16 v[110:113], v[110:113], v[58:61], 0
	s_waitcnt lgkmcnt(0)
	v_mfma_f32_16x16x32_bf16 v[58:61], v[192:195], v[58:61], 0
	ds_read_b64_tr_b16 v[52:53], v186 offset:39168
	ds_read_b64_tr_b16 v[50:51], v186 offset:36864
	ds_read_b64_tr_b16 v[192:193], v186 offset:36896
	ds_read_b64_tr_b16 v[194:195], v186 offset:39200
	s_waitcnt lgkmcnt(2)
	v_mfma_f32_16x16x32_bf16 v[50:53], v[50:53], v[54:57], v[62:65]
	s_waitcnt lgkmcnt(0)
	v_mfma_f32_16x16x32_bf16 v[62:65], v[192:195], v[54:57], v[66:69]
	s_nop 2
	ds_read_b64_tr_b16 v[66:67], v186 offset:36928
	ds_read_b64_tr_b16 v[68:69], v186 offset:39232
	s_waitcnt lgkmcnt(0)
	v_mfma_f32_16x16x32_bf16 v[66:69], v[66:69], v[54:57], v[110:113]
	s_nop 2
	ds_read_b64_tr_b16 v[110:111], v186 offset:36960
	ds_read_b64_tr_b16 v[112:113], v186 offset:39264
	s_waitcnt lgkmcnt(0)
	v_mfma_f32_16x16x32_bf16 v[54:57], v[110:113], v[54:57], v[58:61]
	ds_read_b64_tr_b16 v[44:45], v187 offset:39168
	ds_read_b64_tr_b16 v[42:43], v187 offset:36864
	s_nop 0
	ds_read_b64_tr_b16 v[58:59], v187 offset:36896
	ds_read_b64_tr_b16 v[60:61], v187 offset:39200
	s_waitcnt lgkmcnt(2)
	v_mfma_f32_16x16x32_bf16 v[42:45], v[42:45], v[46:49], v[50:53]
	s_nop 2
	ds_read_b64_tr_b16 v[50:51], v187 offset:36928
	ds_read_b64_tr_b16 v[52:53], v187 offset:39232
	s_waitcnt lgkmcnt(2)
	v_mfma_f32_16x16x32_bf16 v[58:61], v[58:61], v[46:49], v[62:65]
	s_waitcnt lgkmcnt(0)
	v_mfma_f32_16x16x32_bf16 v[62:65], v[50:53], v[46:49], v[66:69]
	ds_read_b64_tr_b16 v[50:51], v187 offset:36960
	ds_read_b64_tr_b16 v[52:53], v187 offset:39264
	s_waitcnt lgkmcnt(0)
	v_mfma_f32_16x16x32_bf16 v[54:57], v[50:53], v[46:49], v[54:57]
	ds_read_b64_tr_b16 v[36:37], v188 offset:39168
	ds_read_b64_tr_b16 v[34:35], v188 offset:36864
	ds_read_b64_tr_b16 v[46:47], v188 offset:36896
	ds_read_b64_tr_b16 v[48:49], v188 offset:39200
	s_waitcnt lgkmcnt(2)
	v_mfma_f32_16x16x32_bf16 v[50:53], v[34:37], v[38:41], v[42:45]
	s_nop 2
	ds_read_b64_tr_b16 v[42:43], v188 offset:36928
	ds_read_b64_tr_b16 v[44:45], v188 offset:39232
	s_waitcnt lgkmcnt(2)
	v_mfma_f32_16x16x32_bf16 v[34:37], v[46:49], v[38:41], v[58:61]
	s_waitcnt lgkmcnt(0)
	v_mfma_f32_16x16x32_bf16 v[46:49], v[42:45], v[38:41], v[62:65]
	ds_read_b64_tr_b16 v[42:43], v188 offset:36960
	ds_read_b64_tr_b16 v[44:45], v188 offset:39264
	ds_read_b128 v[110:113], v178 offset:59968
	ds_read_b128 v[62:65], v178 offset:57664
	s_waitcnt lgkmcnt(2)
	v_mfma_f32_16x16x32_bf16 v[192:195], v[42:45], v[38:41], v[54:57]
	ds_read_b128 v[38:41], v178 offset:55296
	s_nop 1
	ds_read_b128 v[54:57], v178 offset:55360
	ds_read_b128 v[42:45], v178 offset:64512
	s_waitcnt lgkmcnt(2)
	v_mfma_f32_16x16x32_bf16 v[38:41], v[38:41], v[30:33], 0
	ds_read_b128 v[66:69], v180 offset:64512
	ds_read_b128 v[196:199], v181 offset:64512
	s_waitcnt lgkmcnt(3)
	v_mfma_f32_16x16x32_bf16 v[54:57], v[54:57], v[26:29], v[38:41]
	s_nop 3
	ds_read_b128 v[38:41], v178 offset:64576
	s_waitcnt lgkmcnt(3)
	v_mfma_f32_16x16x32_bf16 v[42:45], v[42:45], v[30:33], 0
	s_waitcnt lgkmcnt(0)
	v_mfma_f32_16x16x32_bf16 v[58:61], v[38:41], v[26:29], v[42:45]
	ds_read_b128 v[38:41], v178 offset:57600
	s_nop 4
	ds_read_b128 v[42:45], v179 offset:64512
	s_waitcnt lgkmcnt(1)
	v_mfma_f32_16x16x32_bf16 v[38:41], v[38:41], v[30:33], 0
	v_mfma_f32_16x16x32_bf16 v[38:41], v[62:65], v[26:29], v[38:41]
	ds_read_b128 v[62:65], v179 offset:64576
	s_waitcnt lgkmcnt(1)
	v_mfma_f32_16x16x32_bf16 v[42:45], v[42:45], v[30:33], 0
	s_waitcnt lgkmcnt(0)
	v_mfma_f32_16x16x32_bf16 v[42:45], v[62:65], v[26:29], v[42:45]
	ds_read_b128 v[62:65], v178 offset:59904
	s_waitcnt lgkmcnt(0)
	v_mfma_f32_16x16x32_bf16 v[62:65], v[62:65], v[30:33], 0
	v_mfma_f32_16x16x32_bf16 v[62:65], v[110:113], v[26:29], v[62:65]
	ds_read_b128 v[110:113], v180 offset:64576
	v_mfma_f32_16x16x32_bf16 v[66:69], v[66:69], v[30:33], 0
	s_waitcnt lgkmcnt(0)
	v_mfma_f32_16x16x32_bf16 v[66:69], v[110:113], v[26:29], v[66:69]
	ds_read_b128 v[110:113], v178 offset:62208
	s_waitcnt lgkmcnt(0)
	v_mfma_f32_16x16x32_bf16 v[110:113], v[110:113], v[30:33], 0
	v_mfma_f32_16x16x32_bf16 v[30:33], v[196:199], v[30:33], 0
	ds_read_b128 v[196:199], v178 offset:62272
	s_waitcnt lgkmcnt(0)
	v_mfma_f32_16x16x32_bf16 v[196:199], v[196:199], v[26:29], v[110:113]
	s_nop 3
	ds_read_b128 v[110:113], v181 offset:64576
	s_waitcnt lgkmcnt(0)
	v_mfma_f32_16x16x32_bf16 v[26:29], v[110:113], v[26:29], v[30:33]
	s_nop 2
	v_mul_f32_e32 v30, v108, v1
	v_mul_f32_e32 v30, 0x3fb8aa3b, v30
	v_exp_f32_e32 v110, v30
	v_mul_f32_e32 v30, v107, v71
	v_mul_f32_e32 v30, 0x3fb8aa3b, v30
	v_exp_f32_e32 v112, v30
	s_nop 0
	v_pk_mul_f32 v[26:27], v[112:113], v[26:27] op_sel_hi:[0,1]
	v_pk_fma_f32 v[26:27], v[110:111], v[196:197], v[26:27] op_sel_hi:[0,1,1]
	v_pk_add_f32 v[32:33], v[192:193], v[26:27]
	v_pk_mul_f32 v[26:27], v[112:113], v[28:29] op_sel_hi:[0,1]
	v_pk_fma_f32 v[26:27], v[110:111], v[198:199], v[26:27] op_sel_hi:[0,1,1]
	v_pk_add_f32 v[108:109], v[194:195], v[26:27]
	v_lshl_add_u64 v[26:27], s[0:1], 0, v[82:83]
	v_mov_b64_e32 v[28:29], s[84:85]
	v_mad_u64_u32 v[28:29], s[0:1], v26, s95, v[28:29]
	v_pk_mul_f32 v[30:31], v[112:113], v[66:67] op_sel_hi:[0,1]
	v_mad_i32_i24 v29, v27, s95, v29
	v_lshlrev_b64 v[26:27], 12, v[26:27]
	v_pk_fma_f32 v[30:31], v[110:111], v[62:63], v[30:31] op_sel_hi:[0,1,1]
	v_lshl_add_u64 v[28:29], v[28:29], 0, s[86:87]
	v_lshl_add_u64 v[26:27], s[80:81], 0, v[26:27]
	v_pk_add_f32 v[66:67], v[46:47], v[30:31]
	v_lshl_add_u64 v[46:47], v[28:29], 0, v[72:73]
	v_lshl_add_u64 v[26:27], v[26:27], 0, s[86:87]
	s_lshl_b32 s86, s97, 8
	v_lshl_add_u64 v[30:31], v[26:27], 0, v[72:73]
	v_lshl_add_u64 v[62:63], v[84:85], 0, s[86:87]
	global_load_dwordx2 v[114:115], v[46:47], off offset:3072
	global_load_dwordx4 v[26:29], v[62:63], off
	v_pk_mul_f32 v[60:61], v[112:113], v[60:61] op_sel_hi:[0,1]
	v_pk_fma_f32 v[56:57], v[110:111], v[56:57], v[60:61] op_sel_hi:[0,1,1]
	v_pk_add_f32 v[52:53], v[52:53], v[56:57]
	v_pk_mul_f32 v[56:57], v[112:113], v[58:59] op_sel_hi:[0,1]
	v_pk_fma_f32 v[54:55], v[110:111], v[54:55], v[56:57] op_sel_hi:[0,1,1]
	v_pk_add_f32 v[54:55], v[50:51], v[54:55]
	v_pk_mul_f32 v[44:45], v[112:113], v[44:45] op_sel_hi:[0,1]
	v_add_f32_e32 v50, 0, v54
	v_add_f32_e32 v56, v55, v50
	v_add_f32_e32 v56, v52, v56
	s_mov_b32 s86, s96
	s_waitcnt vmcnt(1)
	v_lshlrev_b32_e32 v57, 16, v114
	v_mul_f32_e32 v50, 0xbfb8aa3b, v57
	v_fma_f32 v51, v57, s8, -v50
	v_rndne_f32_e32 v59, v50
	v_fmac_f32_e32 v51, 0xb2a5705f, v57
	v_sub_f32_e32 v50, v50, v59
	v_add_f32_e32 v50, v50, v51
	v_exp_f32_e32 v50, v50
	v_cvt_i32_f32_e32 v51, v59
	v_and_b32_e32 v58, 0xffff0000, v114
	v_cmp_nlt_f32_e32 vcc, s9, v57
	v_lshlrev_b32_e32 v60, 16, v115
	v_ldexp_f32 v50, v50, v51
	v_mul_f32_e32 v51, 0xbfb8aa3b, v58
	v_fma_f32 v59, v58, s8, -v51
	v_rndne_f32_e32 v103, v51
	v_fmac_f32_e32 v59, 0xb2a5705f, v58
	v_sub_f32_e32 v51, v51, v103
	v_add_f32_e32 v51, v51, v59
	v_exp_f32_e32 v51, v51
	v_cvt_i32_f32_e32 v59, v103
	v_cndmask_b32_e32 v50, 0, v50, vcc
	v_cmp_ngt_f32_e32 vcc, s10, v57
	v_and_b32_e32 v61, 0xffff0000, v115
	v_ldexp_f32 v51, v51, v59
	v_cndmask_b32_e32 v50, v191, v50, vcc
	v_cmp_nlt_f32_e32 vcc, s9, v58
	s_nop 1
	v_cndmask_b32_e32 v51, 0, v51, vcc
	v_cmp_ngt_f32_e32 vcc, s10, v58
	s_nop 1
	v_cndmask_b32_e32 v51, v191, v51, vcc
	v_pk_add_f32 v[50:51], v[50:51], 1.0 op_sel_hi:[1,0]
	s_nop 0
	v_rcp_f32_e32 v59, v51
	s_nop 3
	v_mul_f32_e32 v51, v58, v59
	s_nop 1
	v_div_scale_f32 v58, s[0:1], v50, v50, v57
	v_rcp_f32_e32 v59, v58
	v_pk_fma_f32 v[40:41], v[110:111], v[40:41], v[44:45] op_sel_hi:[0,1,1]
	v_pk_add_f32 v[36:37], v[36:37], v[40:41]
	v_pk_mul_f32 v[40:41], v[112:113], v[42:43] op_sel_hi:[0,1]
	v_fma_f32 v103, -v58, v59, 1.0
	v_fmac_f32_e32 v59, v103, v59
	v_div_scale_f32 v103, vcc, v57, v50, v57
	v_mul_f32_e32 v105, v103, v59
	v_fma_f32 v107, -v58, v105, v103
	v_fmac_f32_e32 v105, v107, v59
	v_fma_f32 v58, -v58, v105, v103
	v_div_fmas_f32 v58, v58, v59, v105
	v_div_fixup_f32 v50, v58, v50, v57
	v_add_f32_e32 v58, v53, v56
	v_pk_mul_f32 v[56:57], v[112:113], v[68:69] op_sel_hi:[0,1]
	v_pk_fma_f32 v[56:57], v[110:111], v[64:65], v[56:57] op_sel_hi:[0,1,1]
	v_pk_add_f32 v[56:57], v[48:49], v[56:57]
	v_mul_f32_e32 v48, 0xbfb8aa3b, v60
	v_fma_f32 v49, v60, s8, -v48
	v_rndne_f32_e32 v59, v48
	v_fmac_f32_e32 v49, 0xb2a5705f, v60
	v_sub_f32_e32 v48, v48, v59
	v_add_f32_e32 v48, v48, v49
	v_exp_f32_e32 v48, v48
	v_cvt_i32_f32_e32 v49, v59
	v_cmp_nlt_f32_e32 vcc, s9, v60
	v_pk_fma_f32 v[38:39], v[110:111], v[38:39], v[40:41] op_sel_hi:[0,1,1]
	v_pk_add_f32 v[34:35], v[34:35], v[38:39]
	v_ldexp_f32 v48, v48, v49
	v_mul_f32_e32 v49, 0xbfb8aa3b, v61
	v_fma_f32 v59, v61, s8, -v49
	v_rndne_f32_e32 v64, v49
	v_fmac_f32_e32 v59, 0xb2a5705f, v61
	v_sub_f32_e32 v49, v49, v64
	v_add_f32_e32 v49, v49, v59
	v_exp_f32_e32 v49, v49
	v_cvt_i32_f32_e32 v59, v64
	v_cndmask_b32_e32 v48, 0, v48, vcc
	v_cmp_ngt_f32_e32 vcc, s10, v60
	v_add_f32_e32 v38, v58, v34
	v_ldexp_f32 v49, v49, v59
	v_cndmask_b32_e32 v48, v191, v48, vcc
	v_cmp_nlt_f32_e32 vcc, s9, v61
	v_add_f32_e32 v42, v35, v38
	s_nop 0
	v_cndmask_b32_e32 v49, 0, v49, vcc
	v_cmp_ngt_f32_e32 vcc, s10, v61
	s_nop 1
	v_cndmask_b32_e32 v49, v191, v49, vcc
	v_pk_add_f32 v[48:49], v[48:49], 1.0 op_sel_hi:[1,0]
	s_nop 0
	v_rcp_f32_e32 v59, v49
	s_nop 3
	v_mul_f32_e32 v49, v61, v59
	s_nop 1
	v_rcp_f32_e32 v59, v48
	s_nop 3
	v_mul_f32_e32 v48, v60, v59
	s_nop 1
	global_load_dwordx2 v[60:61], v[46:47], off offset:3104
	s_waitcnt vmcnt(0)
	v_lshlrev_b32_e32 v40, 16, v60
	v_mul_f32_e32 v38, 0xbfb8aa3b, v40
	v_fma_f32 v39, v40, s8, -v38
	v_rndne_f32_e32 v43, v38
	v_fmac_f32_e32 v39, 0xb2a5705f, v40
	v_sub_f32_e32 v38, v38, v43
	v_add_f32_e32 v38, v38, v39
	v_exp_f32_e32 v38, v38
	v_cvt_i32_f32_e32 v39, v43
	v_and_b32_e32 v41, 0xffff0000, v60
	v_cmp_nlt_f32_e32 vcc, s9, v40
	v_lshlrev_b32_e32 v65, 16, v61
	v_ldexp_f32 v38, v38, v39
	v_mul_f32_e32 v39, 0xbfb8aa3b, v41
	v_fma_f32 v43, v41, s8, -v39
	v_rndne_f32_e32 v44, v39
	v_fmac_f32_e32 v43, 0xb2a5705f, v41
	v_sub_f32_e32 v39, v39, v44
	v_add_f32_e32 v39, v39, v43
	v_exp_f32_e32 v39, v39
	v_cvt_i32_f32_e32 v43, v44
	v_cndmask_b32_e32 v38, 0, v38, vcc
	v_cmp_ngt_f32_e32 vcc, s10, v40
	v_and_b32_e32 v103, 0xffff0000, v61
	v_ldexp_f32 v39, v39, v43
	v_cndmask_b32_e32 v38, v191, v38, vcc
	v_cmp_nlt_f32_e32 vcc, s9, v41
	s_nop 1
	v_cndmask_b32_e32 v39, 0, v39, vcc
	v_cmp_ngt_f32_e32 vcc, s10, v41
	s_nop 1
	v_cndmask_b32_e32 v39, v191, v39, vcc
	v_pk_add_f32 v[38:39], v[38:39], 1.0 op_sel_hi:[1,0]
	s_nop 0
	v_rcp_f32_e32 v43, v39
	s_nop 3
	v_mul_f32_e32 v41, v41, v43
	s_nop 1
	v_rcp_f32_e32 v39, v38
	s_nop 3
	v_mul_f32_e32 v40, v40, v39
	s_nop 1
	v_add_f32_e32 v38, v36, v42
	v_add_f32_e32 v38, v37, v38
	v_add_f32_e32 v38, v38, v66
	v_add_f32_e32 v38, v67, v38
	v_add_f32_e32 v38, v56, v38
	v_add_f32_e32 v38, v57, v38
	v_add_f32_e32 v38, v38, v32
	v_add_f32_e32 v38, v33, v38
	v_add_f32_e32 v38, v108, v38
	v_add_f32_e32 v38, v109, v38
	ds_bpermute_b32 v39, v116, v38
	v_cmp_nlt_f32_e32 vcc, s9, v65
	s_waitcnt lgkmcnt(0)
	v_add_f32_e32 v38, v38, v39
	ds_bpermute_b32 v39, v117, v38
	s_waitcnt lgkmcnt(0)
	v_add_f32_e32 v38, v38, v39
	v_mul_f32_e32 v64, 0x3c800000, v38
	v_pk_add_f32 v[38:39], v[56:57], v[64:65] op_sel_hi:[1,0] neg_lo:[0,1] neg_hi:[0,1]
	v_mul_f32_e32 v56, 0xbfb8aa3b, v65
	v_fma_f32 v57, v65, s8, -v56
	v_rndne_f32_e32 v105, v56
	v_fmac_f32_e32 v57, 0xb2a5705f, v65
	v_sub_f32_e32 v56, v56, v105
	v_add_f32_e32 v56, v56, v57
	v_exp_f32_e32 v56, v56
	v_cvt_i32_f32_e32 v57, v105
	v_pk_add_f32 v[44:45], v[34:35], v[64:65] op_sel_hi:[1,0] neg_lo:[0,1] neg_hi:[0,1]
	v_pk_add_f32 v[34:35], v[32:33], v[64:65] op_sel_hi:[1,0] neg_lo:[0,1] neg_hi:[0,1]
	v_pk_add_f32 v[32:33], v[108:109], v[64:65] op_sel_hi:[1,0] neg_lo:[0,1] neg_hi:[0,1]
	v_ldexp_f32 v56, v56, v57
	v_mul_f32_e32 v57, 0xbfb8aa3b, v103
	v_fma_f32 v105, v103, s8, -v57
	v_rndne_f32_e32 v107, v57
	v_fmac_f32_e32 v105, 0xb2a5705f, v103
	v_sub_f32_e32 v57, v57, v107
	v_add_f32_e32 v57, v57, v105
	v_exp_f32_e32 v57, v57
	v_cvt_i32_f32_e32 v105, v107
	v_cndmask_b32_e32 v56, 0, v56, vcc
	v_cmp_ngt_f32_e32 vcc, s10, v65
	v_pk_add_f32 v[54:55], v[54:55], v[64:65] op_sel_hi:[1,0] neg_lo:[0,1] neg_hi:[0,1]
	v_ldexp_f32 v57, v57, v105
	v_cndmask_b32_e32 v56, v191, v56, vcc
	v_cmp_nlt_f32_e32 vcc, s9, v103
	v_pk_mul_f32 v[68:69], v[54:55], v[54:55]
	v_pk_add_f32 v[52:53], v[52:53], v[64:65] op_sel_hi:[1,0] neg_lo:[0,1] neg_hi:[0,1]
	v_cndmask_b32_e32 v57, 0, v57, vcc
	v_cmp_ngt_f32_e32 vcc, s10, v103
	v_pk_mul_f32 v[110:111], v[52:53], v[52:53]
	v_add_f32_e32 v68, v68, v69
	v_cndmask_b32_e32 v57, v191, v57, vcc
	v_pk_add_f32 v[56:57], v[56:57], 1.0 op_sel_hi:[1,0]
	v_add_f32_e32 v68, v110, v68
	v_div_scale_f32 v105, s[0:1], v57, v57, v103
	v_rcp_f32_e32 v107, v105
	v_pk_mul_f32 v[112:113], v[44:45], v[44:45]
	v_add_f32_e32 v68, v111, v68
	v_pk_add_f32 v[42:43], v[36:37], v[64:65] op_sel_hi:[1,0] neg_lo:[0,1] neg_hi:[0,1]
	v_fma_f32 v108, -v105, v107, 1.0
	v_fmac_f32_e32 v107, v108, v107
	v_div_scale_f32 v108, vcc, v103, v57, v103
	v_mul_f32_e32 v109, v108, v107
	v_fma_f32 v192, -v105, v109, v108
	v_fmac_f32_e32 v109, v192, v107
	v_fma_f32 v105, -v105, v109, v108
	v_div_fmas_f32 v105, v105, v107, v109
	v_div_fixup_f32 v57, v105, v57, v103
	v_div_scale_f32 v103, s[0:1], v56, v56, v65
	v_rcp_f32_e32 v105, v103
	v_add_f32_e32 v68, v112, v68
	v_pk_mul_f32 v[114:115], v[42:43], v[42:43]
	v_add_f32_e32 v68, v113, v68
	v_fma_f32 v107, -v103, v105, 1.0
	v_fmac_f32_e32 v105, v107, v105
	v_div_scale_f32 v107, vcc, v65, v56, v65
	v_mul_f32_e32 v108, v107, v105
	v_fma_f32 v109, -v103, v108, v107
	v_fmac_f32_e32 v108, v109, v105
	v_fma_f32 v103, -v103, v108, v107
	v_div_fmas_f32 v103, v103, v105, v108
	v_div_fixup_f32 v56, v103, v56, v65
	v_pk_add_f32 v[64:65], v[66:67], v[64:65] op_sel_hi:[1,0] neg_lo:[0,1] neg_hi:[0,1]
	v_add_f32_e32 v68, v114, v68
	v_pk_mul_f32 v[66:67], v[64:65], v[64:65]
	v_add_f32_e32 v68, v115, v68
	v_add_f32_e32 v66, v66, v68
	v_pk_mul_f32 v[36:37], v[38:39], v[38:39]
	v_add_f32_e32 v66, v67, v66
	v_add_f32_e32 v36, v36, v66
	v_pk_mul_f32 v[58:59], v[34:35], v[34:35]
	v_add_f32_e32 v36, v37, v36
	v_add_f32_e32 v36, v58, v36
	v_pk_mul_f32 v[60:61], v[32:33], v[32:33]
	v_add_f32_e32 v36, v59, v36
	v_add_f32_e32 v36, v60, v36
	v_add_f32_e32 v36, v61, v36
	ds_bpermute_b32 v37, v116, v36
	s_mov_b32 s0, 0xf800000
	global_load_dwordx2 v[108:109], v[46:47], off offset:3136
	s_waitcnt lgkmcnt(0)
	v_add_f32_e32 v36, v36, v37
	ds_bpermute_b32 v37, v117, v36
	s_waitcnt lgkmcnt(0)
	v_add_f32_e32 v36, v36, v37
	v_fmamk_f32 v36, v36, 0x3c800000, v189
	v_cmp_gt_f32_e32 vcc, s0, v36
	v_mul_f32_e32 v37, 0x4f800000, v36
	s_nop 0
	v_cndmask_b32_e32 v36, v36, v37, vcc
	v_sqrt_f32_e32 v37, v36
	s_nop 0
	v_add_u32_e32 v58, -1, v37
	v_fma_f32 v59, -v58, v37, v36
	v_cmp_ge_f32_e64 s[0:1], 0, v59
	v_add_u32_e32 v59, 1, v37
	s_nop 0
	v_cndmask_b32_e64 v58, v37, v58, s[0:1]
	v_fma_f32 v37, -v59, v37, v36
	v_cmp_lt_f32_e64 s[0:1], 0, v37
	s_nop 1
	v_cndmask_b32_e64 v37, v58, v59, s[0:1]
	v_mul_f32_e32 v58, 0x37800000, v37
	v_cndmask_b32_e32 v37, v37, v58, vcc
	v_cmp_class_f32_e32 vcc, v36, v190
	s_nop 1
	v_cndmask_b32_e32 v36, v37, v36, vcc
	v_rcp_f32_e32 v36, v36
	s_nop 3
	v_pk_mul_f32 v[54:55], v[54:55], v[36:37] op_sel_hi:[1,0]
	v_pk_mul_f32 v[44:45], v[44:45], v[36:37] op_sel_hi:[1,0]
	v_pk_mul_f32 v[26:27], v[26:27], v[54:55]
	s_nop 0
	v_pk_mul_f32 v[26:27], v[50:51], v[26:27]
	v_pk_mul_f32 v[50:51], v[52:53], v[36:37] op_sel_hi:[1,0]
	v_cvt_pk_bf16_f32 v26, v26, v27
	v_pk_mul_f32 v[28:29], v[28:29], v[50:51]
	s_nop 0
	v_pk_mul_f32 v[28:29], v[48:49], v[28:29]
	s_nop 0
	v_cvt_pk_bf16_f32 v27, v28, v29
	global_store_dwordx2 v[30:31], v[26:27], off
	global_load_dwordx4 v[26:29], v[62:63], off offset:64
	s_waitcnt vmcnt(0)
	v_pk_mul_f32 v[26:27], v[26:27], v[44:45]
	s_nop 0
	v_pk_mul_f32 v[26:27], v[40:41], v[26:27]
	v_pk_mul_f32 v[40:41], v[42:43], v[36:37] op_sel_hi:[1,0]
	v_cvt_pk_bf16_f32 v26, v26, v27
	v_pk_mul_f32 v[28:29], v[28:29], v[40:41]
	v_lshlrev_b32_e32 v37, 16, v108
	v_pk_mul_f32 v[28:29], v[56:57], v[28:29]
	v_mul_f32_e32 v40, 0xbfb8aa3b, v37
	v_cvt_pk_bf16_f32 v27, v28, v29
	global_store_dwordx2 v[30:31], v[26:27], off offset:32
	global_load_dwordx4 v[26:29], v[62:63], off offset:128
	v_fma_f32 v41, v37, s8, -v40
	v_rndne_f32_e32 v43, v40
	v_fmac_f32_e32 v41, 0xb2a5705f, v37
	v_sub_f32_e32 v40, v40, v43
	v_add_f32_e32 v40, v40, v41
	v_exp_f32_e32 v40, v40
	v_cvt_i32_f32_e32 v41, v43
	v_and_b32_e32 v42, 0xffff0000, v108
	v_cmp_nlt_f32_e32 vcc, s9, v37
	v_ldexp_f32 v40, v40, v41
	v_mul_f32_e32 v41, 0xbfb8aa3b, v42
	v_fma_f32 v43, v42, s8, -v41
	v_rndne_f32_e32 v44, v41
	v_fmac_f32_e32 v43, 0xb2a5705f, v42
	v_sub_f32_e32 v41, v41, v44
	v_add_f32_e32 v41, v41, v43
	v_exp_f32_e32 v41, v41
	v_cvt_i32_f32_e32 v43, v44
	v_cndmask_b32_e32 v40, 0, v40, vcc
	v_cmp_ngt_f32_e32 vcc, s10, v37
	v_ldexp_f32 v41, v41, v43
	s_nop 0
	v_cndmask_b32_e32 v40, v191, v40, vcc
	v_cmp_nlt_f32_e32 vcc, s9, v42
	s_nop 1
	v_cndmask_b32_e32 v41, 0, v41, vcc
	v_cmp_ngt_f32_e32 vcc, s10, v42
	s_nop 1
	v_cndmask_b32_e32 v41, v191, v41, vcc
	v_pk_add_f32 v[40:41], v[40:41], 1.0 op_sel_hi:[1,0]
	s_nop 0
	v_rcp_f32_e32 v43, v41
	s_nop 3
	v_mul_f32_e32 v41, v42, v43
	s_nop 1
	v_rcp_f32_e32 v42, v40
	s_nop 3
	v_mul_f32_e32 v40, v37, v42
	s_nop 1
	v_pk_mul_f32 v[42:43], v[64:65], v[36:37] op_sel_hi:[1,0]
	v_lshlrev_b32_e32 v37, 16, v109
	v_cmp_nlt_f32_e32 vcc, s9, v37
	v_pk_mul_f32 v[38:39], v[38:39], v[36:37] op_sel_hi:[1,0]
	s_waitcnt vmcnt(0)
	v_pk_mul_f32 v[26:27], v[26:27], v[42:43]
	s_nop 0
	v_pk_mul_f32 v[26:27], v[40:41], v[26:27]
	v_mul_f32_e32 v40, 0xbfb8aa3b, v37
	v_fma_f32 v41, v37, s8, -v40
	v_rndne_f32_e32 v43, v40
	v_fmac_f32_e32 v41, 0xb2a5705f, v37
	v_sub_f32_e32 v40, v40, v43
	v_add_f32_e32 v40, v40, v41
	v_exp_f32_e32 v40, v40
	v_cvt_i32_f32_e32 v41, v43
	v_and_b32_e32 v42, 0xffff0000, v109
	v_pk_mul_f32 v[28:29], v[28:29], v[38:39]
	v_cvt_pk_bf16_f32 v26, v26, v27
	v_ldexp_f32 v40, v40, v41
	v_mul_f32_e32 v41, 0xbfb8aa3b, v42
	v_fma_f32 v43, v42, s8, -v41
	v_rndne_f32_e32 v44, v41
	v_fmac_f32_e32 v43, 0xb2a5705f, v42
	v_sub_f32_e32 v41, v41, v44
	v_add_f32_e32 v41, v41, v43
	v_exp_f32_e32 v41, v41
	v_cvt_i32_f32_e32 v43, v44
	v_cndmask_b32_e32 v40, 0, v40, vcc
	v_cmp_ngt_f32_e32 vcc, s10, v37
	v_ldexp_f32 v41, v41, v43
	s_nop 0
	v_cndmask_b32_e32 v40, v191, v40, vcc
	v_cmp_nlt_f32_e32 vcc, s9, v42
	s_nop 1
	v_cndmask_b32_e32 v41, 0, v41, vcc
	v_cmp_ngt_f32_e32 vcc, s10, v42
	s_nop 1
	v_cndmask_b32_e32 v41, v191, v41, vcc
	v_pk_add_f32 v[40:41], v[40:41], 1.0 op_sel_hi:[1,0]
	s_nop 0
	v_rcp_f32_e32 v43, v41
	s_nop 3
	v_mul_f32_e32 v41, v42, v43
	s_nop 1
	v_rcp_f32_e32 v42, v40
	s_nop 3
	v_mul_f32_e32 v40, v37, v42
	s_nop 1
	v_pk_mul_f32 v[28:29], v[40:41], v[28:29]
	s_nop 0
	v_cvt_pk_bf16_f32 v27, v28, v29
	global_store_dwordx2 v[30:31], v[26:27], off offset:64
	global_load_dwordx2 v[38:39], v[46:47], off offset:3168
	s_nop 0
	global_load_dwordx4 v[26:29], v[62:63], off offset:192
	s_waitcnt vmcnt(1)
	v_lshlrev_b32_e32 v37, 16, v38
	v_mul_f32_e32 v40, 0xbfb8aa3b, v37
	v_fma_f32 v41, v37, s8, -v40
	v_rndne_f32_e32 v42, v40
	v_fmac_f32_e32 v41, 0xb2a5705f, v37
	v_sub_f32_e32 v40, v40, v42
	v_add_f32_e32 v40, v40, v41
	v_exp_f32_e32 v40, v40
	v_cvt_i32_f32_e32 v41, v42
	v_and_b32_e32 v38, 0xffff0000, v38
	v_cmp_nlt_f32_e32 vcc, s9, v37
	v_pk_mul_f32 v[34:35], v[34:35], v[36:37] op_sel_hi:[1,0]
	v_ldexp_f32 v40, v40, v41
	v_mul_f32_e32 v41, 0xbfb8aa3b, v38
	v_fma_f32 v42, v38, s8, -v41
	v_rndne_f32_e32 v43, v41
	v_fmac_f32_e32 v42, 0xb2a5705f, v38
	v_sub_f32_e32 v41, v41, v43
	v_add_f32_e32 v41, v41, v42
	v_exp_f32_e32 v41, v41
	v_cvt_i32_f32_e32 v42, v43
	v_cndmask_b32_e32 v40, 0, v40, vcc
	v_cmp_ngt_f32_e32 vcc, s10, v37
	s_waitcnt vmcnt(0)
	v_pk_mul_f32 v[26:27], v[26:27], v[34:35]
	v_ldexp_f32 v41, v41, v42
	v_cndmask_b32_e32 v40, v191, v40, vcc
	v_cmp_nlt_f32_e32 vcc, s9, v38
	s_nop 1
	v_cndmask_b32_e32 v41, 0, v41, vcc
	v_cmp_ngt_f32_e32 vcc, s10, v38
	s_nop 1
	v_cndmask_b32_e32 v41, v191, v41, vcc
	v_pk_add_f32 v[40:41], v[40:41], 1.0 op_sel_hi:[1,0]
	s_nop 0
	v_rcp_f32_e32 v42, v41
	s_nop 3
	v_mul_f32_e32 v41, v38, v42
	s_nop 1
	v_rcp_f32_e32 v38, v40
	s_nop 3
	v_mul_f32_e32 v40, v37, v38
	s_nop 1
	v_lshlrev_b32_e32 v37, 16, v39
	v_mul_f32_e32 v34, 0xbfb8aa3b, v37
	v_and_b32_e32 v38, 0xffff0000, v39
	v_fma_f32 v35, v37, s8, -v34
	v_rndne_f32_e32 v39, v34
	v_fmac_f32_e32 v35, 0xb2a5705f, v37
	v_sub_f32_e32 v34, v34, v39
	v_add_f32_e32 v34, v34, v35
	v_exp_f32_e32 v34, v34
	v_cvt_i32_f32_e32 v35, v39
	v_pk_mul_f32 v[26:27], v[40:41], v[26:27]
	v_cmp_nlt_f32_e32 vcc, s9, v37
	v_pk_mul_f32 v[32:33], v[32:33], v[36:37] op_sel_hi:[1,0]
	v_ldexp_f32 v34, v34, v35
	v_mul_f32_e32 v35, 0xbfb8aa3b, v38
	v_fma_f32 v39, v38, s8, -v35
	v_rndne_f32_e32 v40, v35
	v_fmac_f32_e32 v39, 0xb2a5705f, v38
	v_sub_f32_e32 v35, v35, v40
	v_add_f32_e32 v35, v35, v39
	v_exp_f32_e32 v35, v35
	v_cvt_i32_f32_e32 v39, v40
	v_cndmask_b32_e32 v34, 0, v34, vcc
	v_cmp_ngt_f32_e32 vcc, s10, v37
	v_pk_mul_f32 v[28:29], v[28:29], v[32:33]
	v_ldexp_f32 v35, v35, v39
	v_cndmask_b32_e32 v34, v191, v34, vcc
	v_cmp_nlt_f32_e32 vcc, s9, v38
	v_cvt_pk_bf16_f32 v26, v26, v27
	s_nop 0
	v_cndmask_b32_e32 v35, 0, v35, vcc
	v_cmp_ngt_f32_e32 vcc, s10, v38
	s_nop 1
	v_cndmask_b32_e32 v35, v191, v35, vcc
	v_pk_add_f32 v[34:35], v[34:35], 1.0 op_sel_hi:[1,0]
	s_nop 0
	v_rcp_f32_e32 v39, v35
	s_nop 3
	v_mul_f32_e32 v35, v38, v39
	s_nop 1
	v_rcp_f32_e32 v38, v34
	s_nop 3
	v_mul_f32_e32 v34, v37, v38
	s_nop 1
	v_pk_mul_f32 v[28:29], v[34:35], v[28:29]
	s_andn2_b64 vcc, exec, s[88:89]
	v_cvt_pk_bf16_f32 v27, v28, v29
	global_store_dwordx2 v[30:31], v[26:27], off offset:96
	s_cbranch_vccz .LBB0_3604
